# B3 router butterfly: never-matching entries of the last two select chains removed (index registers only hold 0 or 1)
# speedup vs baseline: 1.0205x; 1.0020x over previous
.LBB0_1336:
	s_add_i32 s18, s2, s65
	s_max_i32 s13, s18, 4
	s_add_i32 s14, s13, -4
	s_mov_b32 s15, s60
	s_max_i32 s13, s18, 3
	s_lshl_b64 s[36:37], s[14:15], 12
	s_add_i32 s14, s13, -3
	s_max_i32 s13, s18, 2
	s_lshl_b64 s[52:53], s[14:15], 12
	s_add_i32 s14, s13, -2
	s_max_i32 s13, s18, 1
	s_lshl_b64 s[50:51], s[14:15], 12
	s_add_i32 s14, s13, -1
	s_and_b32 s12, s18, 0x7fc
	s_lshl_b64 s[26:27], s[14:15], 12
	s_max_i32 s14, s18, 0
	s_max_i32 s13, s18, -1
	s_lshl_b64 s[24:25], s[14:15], 12
	s_add_i32 s14, s13, 1
	s_min_u32 s13, s12, 15
	s_add_i32 s13, s13, 1
	s_lshl_b64 s[78:79], s[14:15], 12
	s_min_u32 s14, s12, 14
	v_cvt_f32_ubyte0_e32 v0, s13
	s_add_i32 s16, s14, 2
	v_div_scale_f32 v1, s[14:15], v0, v0, 1.0
	v_rcp_f32_e32 v2, v1
	s_min_u32 s13, s12, 7
	s_add_i32 s13, s13, 1
	s_waitcnt lgkmcnt(0)
	v_fma_f32 v3, -v1, v2, 1.0
	v_fmac_f32_e32 v2, v3, v2
	v_div_scale_f32 v3, vcc, 1.0, v0, 1.0
	v_mul_f32_e32 v4, v3, v2
	v_fma_f32 v5, -v1, v4, v3
	v_fmac_f32_e32 v4, v5, v2
	v_fma_f32 v1, -v1, v4, v3
	v_div_fmas_f32 v1, v1, v2, v4
	v_div_fixup_f32 v92, v1, v0, 1.0
	v_cvt_f32_ubyte0_e32 v0, s16
	v_div_scale_f32 v1, s[14:15], v0, v0, 1.0
	v_rcp_f32_e32 v2, v1
	s_min_u32 s14, s12, 6
	s_add_i32 s16, s14, 2
	s_waitcnt lgkmcnt(0)
	v_fma_f32 v3, -v1, v2, 1.0
	v_fmac_f32_e32 v2, v3, v2
	v_div_scale_f32 v3, vcc, 1.0, v0, 1.0
	v_mul_f32_e32 v4, v3, v2
	v_fma_f32 v5, -v1, v4, v3
	v_fmac_f32_e32 v4, v5, v2
	v_fma_f32 v1, -v1, v4, v3
	v_div_fmas_f32 v1, v1, v2, v4
	v_div_fixup_f32 v94, v1, v0, 1.0
	v_cvt_f32_ubyte0_e32 v0, s13
	v_div_scale_f32 v1, s[14:15], v0, v0, 1.0
	v_rcp_f32_e32 v2, v1
	s_min_u32 s13, s12, 3
	s_add_i32 s13, s13, 1
	s_barrier
	v_fma_f32 v3, -v1, v2, 1.0
	v_fmac_f32_e32 v2, v3, v2
	v_div_scale_f32 v3, vcc, 1.0, v0, 1.0
	v_mul_f32_e32 v4, v3, v2
	v_fma_f32 v5, -v1, v4, v3
	v_fmac_f32_e32 v4, v5, v2
	v_fma_f32 v1, -v1, v4, v3
	v_div_fmas_f32 v1, v1, v2, v4
	v_div_fixup_f32 v8, v1, v0, 1.0
	v_cvt_f32_ubyte0_e32 v0, s16
	v_div_scale_f32 v1, s[14:15], v0, v0, 1.0
	v_rcp_f32_e32 v2, v1
	s_min_u32 s14, s12, 2
	s_add_i32 s16, s14, 2
	v_fma_f32 v3, -v1, v2, 1.0
	v_fmac_f32_e32 v2, v3, v2
	v_div_scale_f32 v3, vcc, 1.0, v0, 1.0
	v_mul_f32_e32 v4, v3, v2
	v_fma_f32 v5, -v1, v4, v3
	v_fmac_f32_e32 v4, v5, v2
	v_fma_f32 v1, -v1, v4, v3
	v_div_fmas_f32 v1, v1, v2, v4
	v_div_fixup_f32 v10, v1, v0, 1.0
	v_cvt_f32_ubyte0_e32 v0, s13
	v_div_scale_f32 v1, s[14:15], v0, v0, 1.0
	v_rcp_f32_e32 v2, v1
	v_mov_b32_e32 v27, s7
	s_max_i32 s0, s18, 15
	s_add_i32 s0, s0, -15
	v_fma_f32 v3, -v1, v2, 1.0
	v_fmac_f32_e32 v2, v3, v2
	v_div_scale_f32 v3, vcc, 1.0, v0, 1.0
	v_mul_f32_e32 v4, v3, v2
	v_fma_f32 v5, -v1, v4, v3
	v_fmac_f32_e32 v4, v5, v2
	v_fma_f32 v1, -v1, v4, v3
	v_div_fmas_f32 v1, v1, v2, v4
	v_div_fixup_f32 v4, v1, v0, 1.0
	v_cvt_f32_ubyte0_e32 v0, s16
	v_div_scale_f32 v1, s[14:15], v0, v0, 1.0
	v_rcp_f32_e32 v2, v1
	s_mov_b32 s1, s60
	s_lshl_b64 s[76:77], s[0:1], 12
	s_max_i32 s0, s18, 14
	v_fma_f32 v3, -v1, v2, 1.0
	v_fmac_f32_e32 v2, v3, v2
	v_div_scale_f32 v3, vcc, 1.0, v0, 1.0
	v_mul_f32_e32 v5, v3, v2
	v_fma_f32 v6, -v1, v5, v3
	v_fmac_f32_e32 v5, v6, v2
	v_fma_f32 v1, -v1, v5, v3
	v_div_fmas_f32 v1, v1, v2, v5
	v_mov_b32_e32 v5, v21
	v_div_fixup_f32 v6, v1, v0, 1.0
	ds_read_b64 v[2:3], v27 offset:56
	ds_read_b32 v12, v27 offset:64
	v_lshlrev_b32_e32 v0, 2, v5
	v_ashrrev_i32_e32 v1, 31, v0
	v_lshlrev_b64 v[84:85], 1, v[0:1]
	v_lshl_add_u64 v[0:1], s[92:93], 0, v[84:85]
	v_lshl_add_u64 v[236:237], v[0:1], 0, s[78:79]
	global_load_dwordx2 v[236:237], v[236:237], off
	v_lshl_add_u64 v[238:239], v[0:1], 0, s[26:27]
	global_load_dwordx2 v[238:239], v[238:239], off
	v_lshl_add_u64 v[240:241], v[0:1], 0, s[24:25]
	global_load_dwordx2 v[240:241], v[240:241], off
	s_nop 0
	s_nop 0
	s_nop 0
	s_nop 0
	s_nop 0
	s_add_i32 s0, s0, -14
	s_nop 0
	s_lshl_b64 s[10:11], s[0:1], 12
	s_max_i32 s0, s18, 13
	s_add_i32 s0, s0, -13
	s_lshl_b64 s[8:9], s[0:1], 12
	s_max_i32 s0, s18, 12
	s_add_i32 s0, s0, -12
	s_lshl_b64 s[44:45], s[0:1], 12
	s_max_i32 s0, s18, 11
	s_add_i32 s0, s0, -11
	s_lshl_b64 s[48:49], s[0:1], 12
	s_max_i32 s0, s18, 10
	s_add_i32 s0, s0, -10
	s_lshl_b64 s[46:47], s[0:1], 12
	s_max_i32 s0, s18, 9
	s_add_i32 s0, s0, -9
	s_lshl_b64 s[30:31], s[0:1], 12
	s_max_i32 s0, s18, 8
	s_max_i32 s2, s18, 6
	s_add_i32 s0, s0, -8
	s_add_i32 s2, s2, -6
	s_mov_b32 s3, s60
	s_lshl_b64 s[28:29], s[0:1], 12
	s_max_i32 s0, s18, 7
	s_lshl_b64 s[42:43], s[2:3], 12
	s_max_i32 s2, s18, 5
	s_add_i32 s0, s0, -7
	s_add_i32 s2, s2, -5
	s_lshl_b64 s[0:1], s[0:1], 12
	s_lshl_b64 s[2:3], s[2:3], 12
	s_cmp_eq_u32 s12, 0
	s_cselect_b32 s54, 1.0, 0.5
	s_ashr_i32 s19, s18, 31
	s_lshl_b64 s[12:13], s[18:19], 12
	s_add_u32 s22, s4, s12
	s_addc_u32 s23, s5, s13
	s_or_b32 s16, s18, 1
	s_ashr_i32 s17, s16, 31
	s_lshl_b64 s[12:13], s[16:17], 12
	s_add_u32 s20, s4, s12
	s_addc_u32 s21, s5, s13
	s_add_i32 s17, 0, 0x12000
	s_add_u32 vcc_lo, s92, s78
	s_addc_u32 vcc_hi, s93, s79
	s_add_u32 s26, s92, s26
	s_addc_u32 s27, s93, s27
	s_add_u32 s24, s92, s24
	s_addc_u32 s25, s93, s25
	s_add_u32 s52, s92, s52
	s_addc_u32 s53, s93, s53
	s_add_u32 s50, s92, s50
	s_addc_u32 s51, s93, s51
	s_nop 0
	s_waitcnt vmcnt(2)
	v_lshlrev_b32_e32 v80, 16, v236
	v_and_b32_e32 v81, 0xffff0000, v236
	s_nop 0
	s_waitcnt vmcnt(1)
	v_lshlrev_b32_e32 v90, 16, v238
	v_and_b32_e32 v91, 0xffff0000, v238
	v_lshlrev_b32_e32 v88, 16, v239
	v_and_b32_e32 v89, 0xffff0000, v239
	s_waitcnt lgkmcnt(1)
	v_pk_fma_f32 v[96:97], v[2:3], v[90:91], 0 op_sel_hi:[0,1,0]
	v_pk_fma_f32 v[98:99], v[2:3], v[88:89], 0 op_sel_hi:[0,1,0]
	s_nop 0
	s_waitcnt vmcnt(0)
	v_lshlrev_b32_e32 v100, 16, v240
	v_and_b32_e32 v101, 0xffff0000, v240
	v_lshlrev_b32_e32 v0, 16, v241
	v_and_b32_e32 v1, 0xffff0000, v241
	v_pk_mul_f32 v[102:103], v[2:3], v[0:1] op_sel:[1,0]
	v_pk_fma_f32 v[0:1], v[2:3], v[0:1], v[98:99] op_sel:[1,0,0]
	v_pk_fma_f32 v[96:97], v[2:3], v[100:101], v[96:97] op_sel:[1,0,0]
	v_lshlrev_b32_e32 v14, 16, v237
	v_and_b32_e32 v15, 0xffff0000, v237
	v_pk_mul_f32 v[104:105], v[2:3], v[100:101] op_sel:[1,0]
	v_pk_fma_f32 v[90:91], v[2:3], v[90:91], v[96:97] op_sel_hi:[0,1,1] neg_lo:[1,0,0] neg_hi:[1,0,0]
	v_pk_fma_f32 v[2:3], v[2:3], v[88:89], v[0:1] op_sel_hi:[0,1,1] neg_lo:[1,0,0] neg_hi:[1,0,0]
	s_waitcnt lgkmcnt(0)
	v_pk_mul_f32 v[82:83], v[12:13], v[14:15] op_sel_hi:[0,1]
	v_pk_mul_f32 v[86:87], v[12:13], v[80:81] op_sel_hi:[0,1]
	v_pk_fma_f32 v[2:3], v[12:13], v[14:15], v[2:3] op_sel_hi:[0,1,1]
	v_pk_fma_f32 v[12:13], v[12:13], v[80:81], v[90:91] op_sel_hi:[0,1,1]
	v_lshl_add_u64 v[236:237], s[22:23], 0, v[84:85]
	global_load_dwordx2 v[236:237], v[236:237], off
	v_lshl_add_u64 v[238:239], s[20:21], 0, v[84:85]
	global_load_dwordx2 v[238:239], v[238:239], off
	v_lshl_add_u64 v[88:89], s[22:23], 0, v[84:85]
	v_pk_fma_f32 v[12:13], v[12:13], 0.5, v[86:87] op_sel_hi:[1,0,1] neg_lo:[0,0,1] neg_hi:[0,0,1]
	s_nop 0
	v_pk_fma_f32 v[80:81], s[54:55], v[0:1], v[102:103] op_sel_hi:[0,1,1] neg_lo:[0,0,1] neg_hi:[0,0,1]
	v_lshl_add_u32 v0, v5, 4, s17
	v_pk_fma_f32 v[14:15], v[2:3], 0.5, v[82:83] op_sel_hi:[1,0,1] neg_lo:[0,0,1] neg_hi:[0,0,1]
	ds_read_b128 v[0:3], v0
	v_pk_fma_f32 v[82:83], s[54:55], v[96:97], v[104:105] op_sel_hi:[0,1,1] neg_lo:[0,0,1] neg_hi:[0,0,1]
	s_nop 0
	s_waitcnt vmcnt(1)
	v_lshlrev_b32_e32 v90, 16, v236
	v_and_b32_e32 v91, 0xffff0000, v236
	s_waitcnt lgkmcnt(0)
	v_pk_fma_f32 v[82:83], v[0:1], v[82:83], v[90:91]
	v_lshl_add_u64 v[90:91], s[20:21], 0, v[84:85]
	s_nop 0
	v_lshlrev_b32_e32 v86, 16, v237
	v_and_b32_e32 v87, 0xffff0000, v237
	v_pk_fma_f32 v[80:81], v[2:3], v[80:81], v[86:87]
	s_nop 0
	s_waitcnt vmcnt(0)
	v_lshlrev_b32_e32 v86, 16, v238
	v_and_b32_e32 v87, 0xffff0000, v238
	v_lshlrev_b32_e32 v84, 16, v239
	v_and_b32_e32 v85, 0xffff0000, v239
	v_pk_fma_f32 v[86:87], v[0:1], v[12:13], v[86:87]
	v_cvt_pk_bf16_f32 v0, v82, v83
	v_cvt_pk_bf16_f32 v1, v80, v81
	v_pk_fma_f32 v[84:85], v[2:3], v[14:15], v[84:85]
	v_cvt_pk_bf16_f32 v2, v86, v87
	s_nop 0
	v_cvt_pk_bf16_f32 v3, v84, v85
	global_store_dwordx2 v[88:89], v[0:1], off
	global_store_dwordx2 v[90:91], v[2:3], off
	v_mov_b32_e32 v0, v21
	ds_read_b64 v[2:3], v27 offset:56
	ds_read_b32 v12, v27 offset:64
	v_lshlrev_b32_e32 v88, 2, v0
	v_add_u32_e32 v0, 0x100, v88
	v_ashrrev_i32_e32 v1, 31, v0
	v_lshlrev_b64 v[14:15], 1, v[0:1]
	v_lshl_add_u64 v[236:237], vcc, 0, v[14:15]
	global_load_dwordx2 v[236:237], v[236:237], off
	v_lshl_add_u64 v[238:239], s[26:27], 0, v[14:15]
	global_load_dwordx2 v[238:239], v[238:239], off
	v_lshl_add_u64 v[240:241], s[24:25], 0, v[14:15]
	global_load_dwordx2 v[240:241], v[240:241], off
	s_nop 0
	s_nop 0
	s_nop 0
	s_nop 0
	s_nop 0
	v_ashrrev_i32_e32 v89, 31, v88
	s_nop 0
	v_lshl_add_u32 v0, v0, 2, s17
	s_nop 0
	s_waitcnt vmcnt(2)
	v_lshlrev_b32_e32 v96, 16, v236
	v_and_b32_e32 v97, 0xffff0000, v236
	s_nop 0
	s_waitcnt vmcnt(1)
	v_lshlrev_b32_e32 v104, 16, v238
	v_and_b32_e32 v105, 0xffff0000, v238
	v_lshlrev_b32_e32 v102, 16, v239
	v_and_b32_e32 v103, 0xffff0000, v239
	s_waitcnt lgkmcnt(1)
	v_pk_fma_f32 v[106:107], v[2:3], v[104:105], 0 op_sel_hi:[0,1,0]
	v_pk_fma_f32 v[108:109], v[2:3], v[102:103], 0 op_sel_hi:[0,1,0]
	s_nop 0
	s_waitcnt vmcnt(0)
	v_lshlrev_b32_e32 v110, 16, v240
	v_and_b32_e32 v111, 0xffff0000, v240
	v_lshlrev_b32_e32 v14, 16, v241
	v_and_b32_e32 v15, 0xffff0000, v241
	v_pk_fma_f32 v[108:109], v[2:3], v[14:15], v[108:109] op_sel:[1,0,0]
	v_pk_fma_f32 v[106:107], v[2:3], v[110:111], v[106:107] op_sel:[1,0,0]
	v_lshlrev_b32_e32 v90, 16, v237
	v_and_b32_e32 v91, 0xffff0000, v237
	v_pk_mul_f32 v[112:113], v[2:3], v[14:15] op_sel:[1,0]
	v_pk_mul_f32 v[114:115], v[2:3], v[110:111] op_sel:[1,0]
	v_pk_fma_f32 v[14:15], v[2:3], v[104:105], v[106:107] op_sel_hi:[0,1,1] neg_lo:[1,0,0] neg_hi:[1,0,0]
	v_pk_fma_f32 v[2:3], v[2:3], v[102:103], v[108:109] op_sel_hi:[0,1,1] neg_lo:[1,0,0] neg_hi:[1,0,0]
	s_waitcnt lgkmcnt(0)
	v_pk_mul_f32 v[98:99], v[12:13], v[90:91] op_sel_hi:[0,1]
	v_pk_fma_f32 v[2:3], v[12:13], v[90:91], v[2:3] op_sel_hi:[0,1,1]
	v_pk_mul_f32 v[100:101], v[12:13], v[96:97] op_sel_hi:[0,1]
	v_pk_fma_f32 v[12:13], v[12:13], v[96:97], v[14:15] op_sel_hi:[0,1,1]
	v_pk_fma_f32 v[14:15], v[2:3], 0.5, v[98:99] op_sel_hi:[1,0,1] neg_lo:[0,0,1] neg_hi:[0,0,1]
	v_lshlrev_b64 v[98:99], 1, v[88:89]
	v_pk_fma_f32 v[12:13], v[12:13], 0.5, v[100:101] op_sel_hi:[1,0,1] neg_lo:[0,0,1] neg_hi:[0,0,1]
	v_lshl_add_u64 v[236:237], s[22:23], 0, v[98:99]
	global_load_dwordx2 v[236:237], v[236:237], off offset:512
	v_lshl_add_u64 v[238:239], s[20:21], 0, v[98:99]
	global_load_dwordx2 v[238:239], v[238:239], off offset:512
	v_lshl_add_u64 v[100:101], s[22:23], 0, v[98:99]
	s_nop 0
	ds_read_b128 v[0:3], v0
	v_pk_fma_f32 v[90:91], s[54:55], v[106:107], v[114:115] op_sel_hi:[0,1,1] neg_lo:[0,0,1] neg_hi:[0,0,1]
	v_pk_fma_f32 v[96:97], s[54:55], v[108:109], v[112:113] op_sel_hi:[0,1,1] neg_lo:[0,0,1] neg_hi:[0,0,1]
	s_nop 0
	s_waitcnt vmcnt(1)
	v_lshlrev_b32_e32 v102, 16, v236
	v_and_b32_e32 v103, 0xffff0000, v236
	v_lshlrev_b32_e32 v88, 16, v237
	v_and_b32_e32 v89, 0xffff0000, v237
	s_waitcnt lgkmcnt(0)
	v_pk_fma_f32 v[90:91], v[0:1], v[90:91], v[102:103]
	v_lshl_add_u64 v[102:103], s[20:21], 0, v[98:99]
	v_pk_fma_f32 v[88:89], v[2:3], v[96:97], v[88:89]
	s_nop 0
	s_nop 0
	s_waitcnt vmcnt(0)
	v_lshlrev_b32_e32 v98, 16, v238
	v_and_b32_e32 v99, 0xffff0000, v238
	v_lshlrev_b32_e32 v96, 16, v239
	v_and_b32_e32 v97, 0xffff0000, v239
	v_pk_fma_f32 v[98:99], v[0:1], v[12:13], v[98:99]
	v_cvt_pk_bf16_f32 v0, v90, v91
	v_cvt_pk_bf16_f32 v1, v88, v89
	v_pk_fma_f32 v[96:97], v[2:3], v[14:15], v[96:97]
	v_cvt_pk_bf16_f32 v2, v98, v99
	s_nop 0
	v_cvt_pk_bf16_f32 v3, v96, v97
	global_store_dwordx2 v[100:101], v[0:1], off offset:512
	global_store_dwordx2 v[102:103], v[2:3], off offset:512
	v_mov_b32_e32 v0, v21
	s_nop 0
	v_lshlrev_b32_e32 v100, 2, v0
	v_add_u32_e32 v102, 0x200, v100
	v_ashrrev_i32_e32 v103, 31, v102
	v_lshlrev_b64 v[14:15], 1, v[102:103]
	v_lshl_add_u64 v[236:237], vcc, 0, v[14:15]
	global_load_dwordx2 v[236:237], v[236:237], off
	v_lshl_add_u64 v[238:239], s[52:53], 0, v[14:15]
	global_load_dwordx2 v[238:239], v[238:239], off
	v_lshl_add_u64 v[240:241], s[50:51], 0, v[14:15]
	global_load_dwordx2 v[240:241], v[240:241], off
	v_lshl_add_u64 v[242:243], s[26:27], 0, v[14:15]
	global_load_dwordx2 v[242:243], v[242:243], off
	v_lshl_add_u64 v[244:245], s[24:25], 0, v[14:15]
	global_load_dwordx2 v[244:245], v[244:245], off
	s_nop 0
	s_nop 0
	ds_read_b128 v[0:3], v27 offset:48
	ds_read_b32 v12, v27 offset:64
	s_nop 0
	s_nop 0
	s_nop 0
	v_ashrrev_i32_e32 v101, 31, v100
	s_nop 0
	s_nop 0
	s_waitcnt vmcnt(3)
	v_lshlrev_b32_e32 v114, 16, v238
	v_and_b32_e32 v115, 0xffff0000, v238
	v_lshlrev_b32_e32 v112, 16, v239
	v_and_b32_e32 v113, 0xffff0000, v239
	s_waitcnt lgkmcnt(1)
	v_pk_fma_f32 v[118:119], v[0:1], v[112:113], 0 op_sel_hi:[0,1,0]
	s_nop 0
	s_waitcnt vmcnt(2)
	v_lshlrev_b32_e32 v122, 16, v240
	v_and_b32_e32 v123, 0xffff0000, v240
	v_lshlrev_b32_e32 v120, 16, v241
	v_and_b32_e32 v121, 0xffff0000, v241
	v_pk_fma_f32 v[118:119], v[0:1], v[120:121], v[118:119] op_sel:[1,0,0]
	s_nop 0
	s_nop 0
	s_nop 0
	s_nop 0
	v_pk_fma_f32 v[116:117], v[0:1], v[114:115], 0 op_sel_hi:[0,1,0]
	v_pk_fma_f32 v[116:117], v[0:1], v[122:123], v[116:117] op_sel:[1,0,0]
	v_lshlrev_b32_e32 v106, 16, v236
	v_and_b32_e32 v107, 0xffff0000, v236
	v_lshlrev_b32_e32 v104, 16, v237
	v_and_b32_e32 v105, 0xffff0000, v237
	s_waitcnt lgkmcnt(0)
	v_pk_mul_f32 v[108:109], v[12:13], v[104:105] op_sel_hi:[0,1]
	v_pk_mul_f32 v[110:111], v[12:13], v[106:107] op_sel_hi:[0,1]
	s_nop 0
	s_waitcnt vmcnt(1)
	v_lshlrev_b32_e32 v122, 16, v242
	v_and_b32_e32 v123, 0xffff0000, v242
	v_lshlrev_b32_e32 v120, 16, v243
	v_and_b32_e32 v121, 0xffff0000, v243
	v_pk_fma_f32 v[116:117], v[2:3], v[122:123], v[116:117] op_sel_hi:[0,1,1]
	v_pk_fma_f32 v[118:119], v[2:3], v[120:121], v[118:119] op_sel_hi:[0,1,1]
	s_nop 0
	s_waitcnt vmcnt(0)
	v_lshlrev_b32_e32 v120, 16, v244
	v_and_b32_e32 v121, 0xffff0000, v244
	v_lshlrev_b32_e32 v14, 16, v245
	v_and_b32_e32 v15, 0xffff0000, v245
	v_mov_b32_e32 v2, v3
	v_pk_mul_f32 v[122:123], v[2:3], v[14:15] op_sel_hi:[0,1]
	v_pk_mul_f32 v[124:125], v[2:3], v[120:121] op_sel_hi:[0,1]
	v_pk_fma_f32 v[118:119], v[2:3], v[14:15], v[118:119] op_sel_hi:[0,1,1]
	v_pk_fma_f32 v[2:3], v[2:3], v[120:121], v[116:117] op_sel_hi:[0,1,1]
	v_pk_fma_f32 v[14:15], v[0:1], v[114:115], v[2:3] op_sel_hi:[0,1,1] neg_lo:[1,0,0] neg_hi:[1,0,0]
	v_pk_fma_f32 v[0:1], v[0:1], v[112:113], v[118:119] op_sel_hi:[0,1,1] neg_lo:[1,0,0] neg_hi:[1,0,0]
	v_pk_fma_f32 v[0:1], v[12:13], v[104:105], v[0:1] op_sel_hi:[0,1,1]
	v_pk_fma_f32 v[12:13], v[12:13], v[106:107], v[14:15] op_sel_hi:[0,1,1]
	v_pk_fma_f32 v[12:13], v[6:7], v[12:13], v[110:111] op_sel_hi:[0,1,1] neg_lo:[0,0,1] neg_hi:[0,0,1]
	v_lshlrev_b64 v[110:111], 1, v[100:101]
	v_pk_fma_f32 v[14:15], v[6:7], v[0:1], v[108:109] op_sel_hi:[0,1,1] neg_lo:[0,0,1] neg_hi:[0,0,1]
	v_lshl_add_u64 v[108:109], s[22:23], 0, v[110:111]
	global_load_dwordx2 v[100:101], v[108:109], off offset:1024
	v_lshl_add_u32 v0, v102, 2, s17
	v_pk_fma_f32 v[104:105], v[4:5], v[2:3], v[124:125] op_sel_hi:[0,1,1] neg_lo:[0,0,1] neg_hi:[0,0,1]
	ds_read_b128 v[0:3], v0
	v_lshl_add_u64 v[110:111], s[20:21], 0, v[110:111]
	v_pk_fma_f32 v[106:107], v[4:5], v[118:119], v[122:123] op_sel_hi:[0,1,1] neg_lo:[0,0,1] neg_hi:[0,0,1]
	s_nop 0
	s_waitcnt vmcnt(0)
	v_lshlrev_b32_e32 v102, 16, v100
	v_and_b32_e32 v103, 0xffff0000, v100
	s_waitcnt lgkmcnt(0)
	v_pk_fma_f32 v[102:103], v[0:1], v[104:105], v[102:103]
	global_load_dwordx2 v[104:105], v[110:111], off offset:1024
	v_lshlrev_b32_e32 v100, 16, v101
	v_and_b32_e32 v101, 0xffff0000, v101
	v_pk_fma_f32 v[100:101], v[2:3], v[106:107], v[100:101]
	s_nop 0
	s_waitcnt vmcnt(0)
	v_lshlrev_b32_e32 v106, 16, v104
	v_and_b32_e32 v107, 0xffff0000, v104
	v_lshlrev_b32_e32 v104, 16, v105
	v_and_b32_e32 v105, 0xffff0000, v105
	v_pk_fma_f32 v[106:107], v[0:1], v[12:13], v[106:107]
	v_cvt_pk_bf16_f32 v0, v102, v103
	v_cvt_pk_bf16_f32 v1, v100, v101
	v_pk_fma_f32 v[104:105], v[2:3], v[14:15], v[104:105]
	v_cvt_pk_bf16_f32 v2, v106, v107
	s_nop 0
	v_cvt_pk_bf16_f32 v3, v104, v105
	global_store_dwordx2 v[108:109], v[0:1], off offset:1024
	global_store_dwordx2 v[110:111], v[2:3], off offset:1024
	v_mov_b32_e32 v0, v21
	s_nop 0
	v_lshlrev_b32_e32 v14, 2, v0
	v_add_u32_e32 v108, 0x300, v14
	v_ashrrev_i32_e32 v109, 31, v108
	v_lshlrev_b64 v[110:111], 1, v[108:109]
	v_lshl_add_u64 v[236:237], vcc, 0, v[110:111]
	global_load_dwordx2 v[236:237], v[236:237], off
	v_lshl_add_u64 v[238:239], s[52:53], 0, v[110:111]
	global_load_dwordx2 v[238:239], v[238:239], off
	v_lshl_add_u64 v[240:241], s[50:51], 0, v[110:111]
	global_load_dwordx2 v[240:241], v[240:241], off
	v_lshl_add_u64 v[242:243], s[26:27], 0, v[110:111]
	global_load_dwordx2 v[242:243], v[242:243], off
	v_lshl_add_u64 v[244:245], s[24:25], 0, v[110:111]
	global_load_dwordx2 v[244:245], v[244:245], off
	s_nop 0
	s_nop 0
	ds_read_b128 v[0:3], v27 offset:48
	ds_read_b32 v12, v27 offset:64
	s_nop 0
	s_nop 0
	s_nop 0
	v_ashrrev_i32_e32 v15, 31, v14
	s_nop 0
	v_lshlrev_b64 v[14:15], 1, v[14:15]
	s_nop 0
	s_waitcnt vmcnt(3)
	v_lshlrev_b32_e32 v122, 16, v238
	v_and_b32_e32 v123, 0xffff0000, v238
	v_lshlrev_b32_e32 v120, 16, v239
	v_and_b32_e32 v121, 0xffff0000, v239
	s_waitcnt lgkmcnt(1)
	v_pk_fma_f32 v[126:127], v[0:1], v[120:121], 0 op_sel_hi:[0,1,0]
	s_nop 0
	s_waitcnt vmcnt(2)
	v_lshlrev_b32_e32 v130, 16, v240
	v_and_b32_e32 v131, 0xffff0000, v240
	v_lshlrev_b32_e32 v128, 16, v241
	v_and_b32_e32 v129, 0xffff0000, v241
	v_pk_fma_f32 v[126:127], v[0:1], v[128:129], v[126:127] op_sel:[1,0,0]
	s_nop 0
	s_nop 0
	s_nop 0
	s_nop 0
	v_pk_fma_f32 v[124:125], v[0:1], v[122:123], 0 op_sel_hi:[0,1,0]
	v_pk_fma_f32 v[124:125], v[0:1], v[130:131], v[124:125] op_sel:[1,0,0]
	v_lshlrev_b32_e32 v114, 16, v236
	v_and_b32_e32 v115, 0xffff0000, v236
	v_lshlrev_b32_e32 v112, 16, v237
	v_and_b32_e32 v113, 0xffff0000, v237
	s_waitcnt lgkmcnt(0)
	v_pk_mul_f32 v[116:117], v[12:13], v[112:113] op_sel_hi:[0,1]
	v_pk_mul_f32 v[118:119], v[12:13], v[114:115] op_sel_hi:[0,1]
	s_nop 0
	s_waitcnt vmcnt(1)
	v_lshlrev_b32_e32 v130, 16, v242
	v_and_b32_e32 v131, 0xffff0000, v242
	v_lshlrev_b32_e32 v128, 16, v243
	v_and_b32_e32 v129, 0xffff0000, v243
	v_pk_fma_f32 v[124:125], v[2:3], v[130:131], v[124:125] op_sel_hi:[0,1,1]
	v_pk_fma_f32 v[126:127], v[2:3], v[128:129], v[126:127] op_sel_hi:[0,1,1]
	s_nop 0
	s_waitcnt vmcnt(0)
	v_lshlrev_b32_e32 v128, 16, v244
	v_and_b32_e32 v129, 0xffff0000, v244
	v_lshlrev_b32_e32 v110, 16, v245
	v_and_b32_e32 v111, 0xffff0000, v245
	v_mov_b32_e32 v2, v3
	v_pk_mul_f32 v[130:131], v[2:3], v[110:111] op_sel_hi:[0,1]
	v_pk_mul_f32 v[132:133], v[2:3], v[128:129] op_sel_hi:[0,1]
	v_pk_fma_f32 v[110:111], v[2:3], v[110:111], v[126:127] op_sel_hi:[0,1,1]
	v_pk_fma_f32 v[2:3], v[2:3], v[128:129], v[124:125] op_sel_hi:[0,1,1]
	v_pk_fma_f32 v[122:123], v[0:1], v[122:123], v[2:3] op_sel_hi:[0,1,1] neg_lo:[1,0,0] neg_hi:[1,0,0]
	v_pk_fma_f32 v[0:1], v[0:1], v[120:121], v[110:111] op_sel_hi:[0,1,1] neg_lo:[1,0,0] neg_hi:[1,0,0]
	v_pk_fma_f32 v[0:1], v[12:13], v[112:113], v[0:1] op_sel_hi:[0,1,1]
	v_pk_fma_f32 v[12:13], v[12:13], v[114:115], v[122:123] op_sel_hi:[0,1,1]
	v_pk_fma_f32 v[112:113], v[4:5], v[2:3], v[132:133] op_sel_hi:[0,1,1] neg_lo:[0,0,1] neg_hi:[0,0,1]
	v_pk_fma_f32 v[110:111], v[4:5], v[110:111], v[130:131] op_sel_hi:[0,1,1] neg_lo:[0,0,1] neg_hi:[0,0,1]
	v_lshl_add_u64 v[4:5], s[22:23], 0, v[14:15]
	v_pk_fma_f32 v[12:13], v[6:7], v[12:13], v[118:119] op_sel_hi:[0,1,1] neg_lo:[0,0,1] neg_hi:[0,0,1]
	v_pk_fma_f32 v[6:7], v[6:7], v[0:1], v[116:117] op_sel_hi:[0,1,1] neg_lo:[0,0,1] neg_hi:[0,0,1]
	v_lshl_add_u32 v0, v108, 2, s17
	global_load_dwordx2 v[108:109], v[4:5], off offset:1536
	ds_read_b128 v[0:3], v0
	v_lshl_add_u64 v[14:15], s[20:21], 0, v[14:15]
	s_nop 0
	s_waitcnt vmcnt(0)
	v_lshlrev_b32_e32 v114, 16, v108
	v_and_b32_e32 v115, 0xffff0000, v108
	v_lshlrev_b32_e32 v108, 16, v109
	v_and_b32_e32 v109, 0xffff0000, v109
	s_waitcnt lgkmcnt(0)
	v_pk_fma_f32 v[108:109], v[2:3], v[110:111], v[108:109]
	v_pk_fma_f32 v[110:111], v[0:1], v[112:113], v[114:115]
	global_load_dwordx2 v[112:113], v[14:15], off offset:1536
	s_nop 0
	s_waitcnt vmcnt(0)
	v_lshlrev_b32_e32 v114, 16, v112
	v_and_b32_e32 v115, 0xffff0000, v112
	v_lshlrev_b32_e32 v112, 16, v113
	v_and_b32_e32 v113, 0xffff0000, v113
	v_pk_fma_f32 v[114:115], v[0:1], v[12:13], v[114:115]
	v_cvt_pk_bf16_f32 v0, v110, v111
	v_cvt_pk_bf16_f32 v1, v108, v109
	v_pk_fma_f32 v[112:113], v[2:3], v[6:7], v[112:113]
	v_cvt_pk_bf16_f32 v2, v114, v115
	s_nop 0
	v_cvt_pk_bf16_f32 v3, v112, v113
	global_store_dwordx2 v[4:5], v[0:1], off offset:1536
	global_store_dwordx2 v[14:15], v[2:3], off offset:1536
	v_mov_b32_e32 v0, v21
	s_add_u32 s0, s92, s0
	v_lshlrev_b32_e32 v12, 2, v0
	v_add_u32_e32 v14, 0x400, v12
	v_ashrrev_i32_e32 v15, 31, v14
	s_addc_u32 s1, s93, s1
	v_lshlrev_b64 v[126:127], 1, v[14:15]
	s_add_u32 s42, s92, s42
	v_lshl_add_u64 v[128:129], s[0:1], 0, v[126:127]
	s_addc_u32 s43, s93, s43
	ds_read_b128 v[0:3], v27 offset:32
	ds_read_b128 v[4:7], v27 offset:48
	ds_read_b32 v116, v27 offset:64
	global_load_dwordx2 v[130:131], v[128:129], off
	v_lshl_add_u64 v[238:239], s[42:43], 0, v[126:127]
	global_load_dwordx2 v[238:239], v[238:239], off
	v_lshl_add_u64 v[240:241], vcc, 0, v[126:127]
	global_load_dwordx2 v[240:241], v[240:241], off
	s_nop 0
	s_nop 0
	s_add_u32 s2, s92, s2
	s_addc_u32 s3, s93, s3
	s_add_u32 s36, s92, s36
	s_addc_u32 s37, s93, s37
	v_lshl_add_u64 v[118:119], vcc, 0, v[126:127]
	s_nop 0
	v_ashrrev_i32_e32 v13, 31, v12
	s_add_u32 s76, s92, s76
	s_addc_u32 s77, s93, s77
	s_add_u32 s10, s92, s10
	s_addc_u32 s11, s93, s11
	s_add_u32 s8, s92, s8
	s_addc_u32 s9, s93, s9
	s_add_u32 s44, s92, s44
	s_addc_u32 s45, s93, s45
	s_add_u32 s48, s92, s48
	s_addc_u32 s49, s93, s49
	s_add_u32 s46, s92, s46
	s_addc_u32 s47, s93, s47
	s_add_u32 s30, s92, s30
	s_addc_u32 s31, s93, s31
	s_add_u32 s28, s92, s28
	s_addc_u32 s29, s93, s29
	s_nop 0
	s_waitcnt vmcnt(2)
	v_lshlrev_b32_e32 v128, 16, v130
	v_and_b32_e32 v129, 0xffff0000, v130
	v_lshlrev_b32_e32 v130, 16, v131
	v_and_b32_e32 v131, 0xffff0000, v131
	s_waitcnt lgkmcnt(2)
	v_pk_fma_f32 v[134:135], v[0:1], v[130:131], 0 op_sel_hi:[0,1,0]
	s_nop 0
	s_waitcnt vmcnt(1)
	v_lshlrev_b32_e32 v138, 16, v238
	v_and_b32_e32 v139, 0xffff0000, v238
	v_lshlrev_b32_e32 v136, 16, v239
	v_and_b32_e32 v137, 0xffff0000, v239
	v_pk_fma_f32 v[134:135], v[0:1], v[136:137], v[134:135] op_sel:[1,0,0]
	v_lshl_add_u64 v[236:237], s[2:3], 0, v[126:127]
	global_load_dwordx2 v[236:237], v[236:237], off
	v_lshl_add_u64 v[238:239], s[36:37], 0, v[126:127]
	global_load_dwordx2 v[238:239], v[238:239], off
	v_lshl_add_u64 v[242:243], s[52:53], 0, v[126:127]
	global_load_dwordx2 v[242:243], v[242:243], off
	v_lshl_add_u64 v[244:245], s[50:51], 0, v[126:127]
	global_load_dwordx2 v[244:245], v[244:245], off
	v_lshl_add_u64 v[246:247], s[24:25], 0, v[126:127]
	global_load_dwordx2 v[246:247], v[246:247], off
	v_lshl_add_u64 v[230:231], s[26:27], 0, v[126:127]
	global_load_dwordx2 v[230:231], v[230:231], off
	s_nop 0
	s_nop 0
	v_pk_fma_f32 v[132:133], v[0:1], v[128:129], 0 op_sel_hi:[0,1,0]
	v_pk_fma_f32 v[132:133], v[0:1], v[138:139], v[132:133] op_sel:[1,0,0]
	s_nop 0
	s_waitcnt vmcnt(5)
	v_lshlrev_b32_e32 v138, 16, v236
	v_and_b32_e32 v139, 0xffff0000, v236
	v_lshlrev_b32_e32 v136, 16, v237
	v_and_b32_e32 v137, 0xffff0000, v237
	v_pk_fma_f32 v[134:135], v[2:3], v[136:137], v[134:135] op_sel_hi:[0,1,1]
	s_nop 0
	s_nop 0
	v_pk_fma_f32 v[132:133], v[2:3], v[138:139], v[132:133] op_sel_hi:[0,1,1]
	v_mov_b32_e32 v2, v3
	s_nop 0
	s_waitcnt vmcnt(4)
	v_lshlrev_b32_e32 v138, 16, v238
	v_and_b32_e32 v139, 0xffff0000, v238
	v_lshlrev_b32_e32 v136, 16, v239
	v_and_b32_e32 v137, 0xffff0000, v239
	v_pk_fma_f32 v[134:135], v[2:3], v[136:137], v[134:135] op_sel_hi:[0,1,1]
	v_pk_fma_f32 v[2:3], v[2:3], v[138:139], v[132:133] op_sel_hi:[0,1,1]
	s_nop 0
	s_nop 0
	s_nop 0
	s_waitcnt vmcnt(3)
	v_lshlrev_b32_e32 v136, 16, v242
	v_and_b32_e32 v137, 0xffff0000, v242
	v_lshlrev_b32_e32 v132, 16, v243
	v_and_b32_e32 v133, 0xffff0000, v243
	s_waitcnt lgkmcnt(1)
	v_pk_fma_f32 v[132:133], v[4:5], v[132:133], v[134:135] op_sel_hi:[0,1,1]
	s_nop 0
	s_nop 0
	v_pk_fma_f32 v[2:3], v[4:5], v[136:137], v[2:3] op_sel_hi:[0,1,1]
	s_nop 0
	s_waitcnt vmcnt(2)
	v_lshlrev_b32_e32 v136, 16, v244
	v_and_b32_e32 v137, 0xffff0000, v244
	v_lshlrev_b32_e32 v134, 16, v245
	v_and_b32_e32 v135, 0xffff0000, v245
	v_pk_fma_f32 v[132:133], v[4:5], v[134:135], v[132:133] op_sel:[1,0,0]
	v_pk_fma_f32 v[2:3], v[4:5], v[136:137], v[2:3] op_sel:[1,0,0]
	s_nop 0
	s_nop 0
	s_nop 0
	s_nop 0
	s_nop 0
	v_lshlrev_b32_e32 v122, 16, v241
	v_and_b32_e32 v123, 0xffff0000, v241
	v_lshlrev_b32_e32 v118, 16, v240
	v_and_b32_e32 v119, 0xffff0000, v240
	s_waitcnt lgkmcnt(0)
	v_pk_mul_f32 v[120:121], v[116:117], v[122:123] op_sel_hi:[0,1]
	v_pk_mul_f32 v[124:125], v[116:117], v[118:119] op_sel_hi:[0,1]
	s_nop 0
	s_waitcnt vmcnt(0)
	v_lshlrev_b32_e32 v134, 16, v230
	v_and_b32_e32 v135, 0xffff0000, v230
	v_lshlrev_b32_e32 v4, 16, v231
	v_and_b32_e32 v5, 0xffff0000, v231
	v_pk_fma_f32 v[2:3], v[6:7], v[134:135], v[2:3] op_sel_hi:[0,1,1]
	v_pk_fma_f32 v[4:5], v[6:7], v[4:5], v[132:133] op_sel_hi:[0,1,1]
	v_lshlrev_b32_e32 v132, 16, v246
	v_and_b32_e32 v133, 0xffff0000, v246
	v_lshlrev_b32_e32 v126, 16, v247
	v_and_b32_e32 v127, 0xffff0000, v247
	v_mov_b32_e32 v6, v7
	v_pk_mul_f32 v[134:135], v[6:7], v[126:127] op_sel_hi:[0,1]
	v_pk_fma_f32 v[126:127], v[6:7], v[126:127], v[4:5] op_sel_hi:[0,1,1]
	v_pk_fma_f32 v[2:3], v[6:7], v[132:133], v[2:3] op_sel_hi:[0,1,1]
	v_pk_fma_f32 v[4:5], v[0:1], v[128:129], v[2:3] op_sel_hi:[0,1,1] neg_lo:[1,0,0] neg_hi:[1,0,0]
	v_pk_fma_f32 v[0:1], v[0:1], v[130:131], v[126:127] op_sel_hi:[0,1,1] neg_lo:[1,0,0] neg_hi:[1,0,0]
	v_pk_fma_f32 v[0:1], v[116:117], v[122:123], v[0:1] op_sel_hi:[0,1,1]
	v_pk_mul_f32 v[136:137], v[6:7], v[132:133] op_sel_hi:[0,1]
	v_pk_fma_f32 v[6:7], v[10:11], v[0:1], v[120:121] op_sel_hi:[0,1,1] neg_lo:[0,0,1] neg_hi:[0,0,1]
	v_lshl_add_u32 v0, v14, 2, s17
	v_lshlrev_b64 v[14:15], 1, v[12:13]
	v_lshl_add_u64 v[12:13], s[22:23], 0, v[14:15]
	global_load_dwordx2 v[120:121], v[12:13], off offset:2048
	v_pk_fma_f32 v[4:5], v[116:117], v[118:119], v[4:5] op_sel_hi:[0,1,1]
	v_pk_fma_f32 v[118:119], v[8:9], v[2:3], v[136:137] op_sel_hi:[0,1,1] neg_lo:[0,0,1] neg_hi:[0,0,1]
	ds_read_b128 v[0:3], v0
	v_pk_fma_f32 v[116:117], v[8:9], v[126:127], v[134:135] op_sel_hi:[0,1,1] neg_lo:[0,0,1] neg_hi:[0,0,1]
	v_lshl_add_u64 v[14:15], s[20:21], 0, v[14:15]
	v_pk_fma_f32 v[4:5], v[10:11], v[4:5], v[124:125] op_sel_hi:[0,1,1] neg_lo:[0,0,1] neg_hi:[0,0,1]
	s_nop 0
	s_waitcnt vmcnt(0)
	v_lshlrev_b32_e32 v122, 16, v120
	v_and_b32_e32 v123, 0xffff0000, v120
	v_lshlrev_b32_e32 v120, 16, v121
	v_and_b32_e32 v121, 0xffff0000, v121
	s_waitcnt lgkmcnt(0)
	v_pk_fma_f32 v[116:117], v[2:3], v[116:117], v[120:121]
	global_load_dwordx2 v[120:121], v[14:15], off offset:2048
	v_pk_fma_f32 v[118:119], v[0:1], v[118:119], v[122:123]
	s_nop 0
	s_waitcnt vmcnt(0)
	v_lshlrev_b32_e32 v122, 16, v120
	v_and_b32_e32 v123, 0xffff0000, v120
	v_lshlrev_b32_e32 v120, 16, v121
	v_and_b32_e32 v121, 0xffff0000, v121
	v_pk_fma_f32 v[122:123], v[0:1], v[4:5], v[122:123]
	v_cvt_pk_bf16_f32 v0, v118, v119
	v_cvt_pk_bf16_f32 v1, v116, v117
	v_pk_fma_f32 v[120:121], v[2:3], v[6:7], v[120:121]
	v_cvt_pk_bf16_f32 v2, v122, v123
	s_nop 0
	v_cvt_pk_bf16_f32 v3, v120, v121
	global_store_dwordx2 v[12:13], v[0:1], off offset:2048
	global_store_dwordx2 v[14:15], v[2:3], off offset:2048
	v_mov_b32_e32 v0, v21
	s_nop 0
	v_lshlrev_b32_e32 v12, 2, v0
	v_add_u32_e32 v14, 0x500, v12
	v_ashrrev_i32_e32 v15, 31, v14
	v_lshlrev_b64 v[134:135], 1, v[14:15]
	v_lshl_add_u64 v[236:237], s[0:1], 0, v[134:135]
	global_load_dwordx2 v[236:237], v[236:237], off
	v_lshl_add_u64 v[238:239], s[42:43], 0, v[134:135]
	global_load_dwordx2 v[238:239], v[238:239], off
	v_lshl_add_u64 v[240:241], vcc, 0, v[134:135]
	global_load_dwordx2 v[240:241], v[240:241], off
	v_lshl_add_u64 v[242:243], s[2:3], 0, v[134:135]
	global_load_dwordx2 v[242:243], v[242:243], off
	v_lshl_add_u64 v[244:245], s[36:37], 0, v[134:135]
	global_load_dwordx2 v[244:245], v[244:245], off
	v_lshl_add_u64 v[246:247], s[52:53], 0, v[134:135]
	global_load_dwordx2 v[246:247], v[246:247], off
	v_lshl_add_u64 v[230:231], s[50:51], 0, v[134:135]
	global_load_dwordx2 v[230:231], v[230:231], off
	v_lshl_add_u64 v[232:233], s[24:25], 0, v[134:135]
	global_load_dwordx2 v[232:233], v[232:233], off
	v_lshl_add_u64 v[234:235], s[26:27], 0, v[134:135]
	global_load_dwordx2 v[234:235], v[234:235], off
	v_lshl_add_u64 v[136:137], s[0:1], 0, v[134:135]
	ds_read_b128 v[0:3], v27 offset:32
	ds_read_b128 v[4:7], v27 offset:48
	ds_read_b32 v124, v27 offset:64
	s_nop 0
	s_nop 0
	s_nop 0
	v_lshl_add_u64 v[126:127], vcc, 0, v[134:135]
	s_nop 0
	v_ashrrev_i32_e32 v13, 31, v12
	v_lshlrev_b64 v[12:13], 1, v[12:13]
	s_nop 0
	s_waitcnt vmcnt(8)
	v_lshlrev_b32_e32 v136, 16, v236
	v_and_b32_e32 v137, 0xffff0000, v236
	v_lshlrev_b32_e32 v138, 16, v237
	v_and_b32_e32 v139, 0xffff0000, v237
	s_waitcnt lgkmcnt(2)
	v_pk_fma_f32 v[142:143], v[0:1], v[138:139], 0 op_sel_hi:[0,1,0]
	s_nop 0
	s_waitcnt vmcnt(7)
	v_lshlrev_b32_e32 v146, 16, v238
	v_and_b32_e32 v147, 0xffff0000, v238
	v_lshlrev_b32_e32 v144, 16, v239
	v_and_b32_e32 v145, 0xffff0000, v239
	v_pk_fma_f32 v[142:143], v[0:1], v[144:145], v[142:143] op_sel:[1,0,0]
	s_nop 0
	s_nop 0
	v_pk_fma_f32 v[140:141], v[0:1], v[136:137], 0 op_sel_hi:[0,1,0]
	v_pk_fma_f32 v[140:141], v[0:1], v[146:147], v[140:141] op_sel:[1,0,0]
	s_nop 0
	s_waitcnt vmcnt(5)
	v_lshlrev_b32_e32 v146, 16, v242
	v_and_b32_e32 v147, 0xffff0000, v242
	v_lshlrev_b32_e32 v144, 16, v243
	v_and_b32_e32 v145, 0xffff0000, v243
	v_pk_fma_f32 v[142:143], v[2:3], v[144:145], v[142:143] op_sel_hi:[0,1,1]
	s_nop 0
	s_nop 0
	v_pk_fma_f32 v[140:141], v[2:3], v[146:147], v[140:141] op_sel_hi:[0,1,1]
	v_mov_b32_e32 v2, v3
	s_nop 0
	s_waitcnt vmcnt(4)
	v_lshlrev_b32_e32 v146, 16, v244
	v_and_b32_e32 v147, 0xffff0000, v244
	v_lshlrev_b32_e32 v144, 16, v245
	v_and_b32_e32 v145, 0xffff0000, v245
	v_pk_fma_f32 v[142:143], v[2:3], v[144:145], v[142:143] op_sel_hi:[0,1,1]
	v_pk_fma_f32 v[2:3], v[2:3], v[146:147], v[140:141] op_sel_hi:[0,1,1]
	s_nop 0
	s_nop 0
	s_nop 0
	s_waitcnt vmcnt(3)
	v_lshlrev_b32_e32 v144, 16, v246
	v_and_b32_e32 v145, 0xffff0000, v246
	v_lshlrev_b32_e32 v140, 16, v247
	v_and_b32_e32 v141, 0xffff0000, v247
	s_waitcnt lgkmcnt(1)
	v_pk_fma_f32 v[140:141], v[4:5], v[140:141], v[142:143] op_sel_hi:[0,1,1]
	s_nop 0
	s_nop 0
	v_pk_fma_f32 v[2:3], v[4:5], v[144:145], v[2:3] op_sel_hi:[0,1,1]
	s_nop 0
	s_waitcnt vmcnt(2)
	v_lshlrev_b32_e32 v144, 16, v230
	v_and_b32_e32 v145, 0xffff0000, v230
	v_lshlrev_b32_e32 v142, 16, v231
	v_and_b32_e32 v143, 0xffff0000, v231
	v_pk_fma_f32 v[140:141], v[4:5], v[142:143], v[140:141] op_sel:[1,0,0]
	v_pk_fma_f32 v[2:3], v[4:5], v[144:145], v[2:3] op_sel:[1,0,0]
	s_nop 0
	s_nop 0
	s_nop 0
	s_nop 0
	s_nop 0
	v_lshlrev_b32_e32 v126, 16, v240
	v_and_b32_e32 v127, 0xffff0000, v240
	v_lshlrev_b32_e32 v130, 16, v241
	v_and_b32_e32 v131, 0xffff0000, v241
	s_waitcnt lgkmcnt(0)
	v_pk_mul_f32 v[128:129], v[124:125], v[130:131] op_sel_hi:[0,1]
	v_pk_mul_f32 v[132:133], v[124:125], v[126:127] op_sel_hi:[0,1]
	s_nop 0
	s_waitcnt vmcnt(0)
	v_lshlrev_b32_e32 v142, 16, v234
	v_and_b32_e32 v143, 0xffff0000, v234
	v_lshlrev_b32_e32 v4, 16, v235
	v_and_b32_e32 v5, 0xffff0000, v235
	v_pk_fma_f32 v[2:3], v[6:7], v[142:143], v[2:3] op_sel_hi:[0,1,1]
	v_pk_fma_f32 v[4:5], v[6:7], v[4:5], v[140:141] op_sel_hi:[0,1,1]
	v_lshlrev_b32_e32 v140, 16, v232
	v_and_b32_e32 v141, 0xffff0000, v232
	v_lshlrev_b32_e32 v134, 16, v233
	v_and_b32_e32 v135, 0xffff0000, v233
	v_mov_b32_e32 v6, v7
	v_pk_mul_f32 v[142:143], v[6:7], v[134:135] op_sel_hi:[0,1]
	v_pk_fma_f32 v[134:135], v[6:7], v[134:135], v[4:5] op_sel_hi:[0,1,1]
	v_pk_fma_f32 v[2:3], v[6:7], v[140:141], v[2:3] op_sel_hi:[0,1,1]
	v_pk_fma_f32 v[4:5], v[0:1], v[136:137], v[2:3] op_sel_hi:[0,1,1] neg_lo:[1,0,0] neg_hi:[1,0,0]
	v_pk_fma_f32 v[0:1], v[0:1], v[138:139], v[134:135] op_sel_hi:[0,1,1] neg_lo:[1,0,0] neg_hi:[1,0,0]
	v_pk_mul_f32 v[144:145], v[6:7], v[140:141] op_sel_hi:[0,1]
	v_pk_fma_f32 v[0:1], v[124:125], v[130:131], v[0:1] op_sel_hi:[0,1,1]
	v_pk_fma_f32 v[4:5], v[124:125], v[126:127], v[4:5] op_sel_hi:[0,1,1]
	v_pk_fma_f32 v[4:5], v[10:11], v[4:5], v[132:133] op_sel_hi:[0,1,1] neg_lo:[0,0,1] neg_hi:[0,0,1]
	v_pk_fma_f32 v[6:7], v[10:11], v[0:1], v[128:129] op_sel_hi:[0,1,1] neg_lo:[0,0,1] neg_hi:[0,0,1]
	v_pk_fma_f32 v[10:11], v[8:9], v[2:3], v[144:145] op_sel_hi:[0,1,1] neg_lo:[0,0,1] neg_hi:[0,0,1]
	v_pk_fma_f32 v[124:125], v[8:9], v[134:135], v[142:143] op_sel_hi:[0,1,1] neg_lo:[0,0,1] neg_hi:[0,0,1]
	v_lshl_add_u64 v[236:237], s[22:23], 0, v[12:13]
	global_load_dwordx2 v[236:237], v[236:237], off offset:2560
	v_lshl_add_u64 v[238:239], s[20:21], 0, v[12:13]
	global_load_dwordx2 v[238:239], v[238:239], off offset:2560
	v_lshl_add_u64 v[8:9], s[22:23], 0, v[12:13]
	v_lshl_add_u32 v0, v14, 2, s17
	s_nop 0
	ds_read_b128 v[0:3], v0
	s_nop 0
	s_waitcnt vmcnt(1)
	v_lshlrev_b32_e32 v126, 16, v236
	v_and_b32_e32 v127, 0xffff0000, v236
	s_waitcnt lgkmcnt(0)
	v_pk_fma_f32 v[126:127], v[0:1], v[10:11], v[126:127]
	v_lshl_add_u64 v[10:11], s[20:21], 0, v[12:13]
	s_nop 0
	v_lshlrev_b32_e32 v14, 16, v237
	v_and_b32_e32 v15, 0xffff0000, v237
	v_pk_fma_f32 v[124:125], v[2:3], v[124:125], v[14:15]
	s_nop 0
	s_waitcnt vmcnt(0)
	v_lshlrev_b32_e32 v14, 16, v238
	v_and_b32_e32 v15, 0xffff0000, v238
	v_lshlrev_b32_e32 v12, 16, v239
	v_and_b32_e32 v13, 0xffff0000, v239
	v_pk_fma_f32 v[130:131], v[0:1], v[4:5], v[14:15]
	v_cvt_pk_bf16_f32 v0, v126, v127
	v_cvt_pk_bf16_f32 v1, v124, v125
	v_pk_fma_f32 v[128:129], v[2:3], v[6:7], v[12:13]
	v_cvt_pk_bf16_f32 v2, v130, v131
	s_nop 0
	v_cvt_pk_bf16_f32 v3, v128, v129
	global_store_dwordx2 v[8:9], v[0:1], off offset:2560
	global_store_dwordx2 v[10:11], v[2:3], off offset:2560
	v_mov_b32_e32 v0, v21
	ds_read_b32 v136, v27 offset:64
	v_lshlrev_b32_e32 v132, 2, v0
	v_add_u32_e32 v134, 0x600, v132
	v_ashrrev_i32_e32 v135, 31, v134
	v_lshlrev_b64 v[146:147], 1, v[134:135]
	v_lshl_add_u64 v[0:1], vcc, 0, v[146:147]
	global_load_dwordx2 v[0:1], v[0:1], off
	v_lshl_add_u64 v[148:149], s[76:77], 0, v[146:147]
	v_lshl_add_u64 v[156:157], s[10:11], 0, v[146:147]
	v_ashrrev_i32_e32 v133, 31, v132
	s_nop 0
	s_waitcnt vmcnt(0)
	v_lshlrev_b32_e32 v138, 16, v0
	v_and_b32_e32 v139, 0xffff0000, v0
	v_lshlrev_b32_e32 v142, 16, v1
	v_and_b32_e32 v143, 0xffff0000, v1
	ds_read_b128 v[0:3], v27
	ds_read_b128 v[12:15], v27 offset:16
	ds_read_b128 v[8:11], v27 offset:32
	ds_read_b128 v[4:7], v27 offset:48
	global_load_dwordx2 v[150:151], v[148:149], off
	s_waitcnt lgkmcnt(4)
	v_pk_mul_f32 v[140:141], v[136:137], v[142:143] op_sel_hi:[0,1]
	global_load_dwordx2 v[156:157], v[156:157], off
	v_pk_mul_f32 v[144:145], v[136:137], v[138:139] op_sel_hi:[0,1]
	s_nop 0
	s_waitcnt vmcnt(1)
	v_lshlrev_b32_e32 v148, 16, v150
	v_and_b32_e32 v149, 0xffff0000, v150
	v_lshlrev_b32_e32 v150, 16, v151
	v_and_b32_e32 v151, 0xffff0000, v151
	s_waitcnt lgkmcnt(3)
	v_pk_fma_f32 v[154:155], v[0:1], v[150:151], 0 op_sel_hi:[0,1,0]
	s_nop 0
	s_waitcnt vmcnt(0)
	v_lshlrev_b32_e32 v158, 16, v156
	v_and_b32_e32 v159, 0xffff0000, v156
	v_lshlrev_b32_e32 v156, 16, v157
	v_and_b32_e32 v157, 0xffff0000, v157
	v_pk_fma_f32 v[154:155], v[0:1], v[156:157], v[154:155] op_sel:[1,0,0]
	v_lshl_add_u64 v[236:237], s[8:9], 0, v[146:147]
	global_load_dwordx2 v[236:237], v[236:237], off
	v_lshl_add_u64 v[238:239], s[44:45], 0, v[146:147]
	global_load_dwordx2 v[238:239], v[238:239], off
	v_lshl_add_u64 v[240:241], s[48:49], 0, v[146:147]
	global_load_dwordx2 v[240:241], v[240:241], off
	v_lshl_add_u64 v[242:243], s[46:47], 0, v[146:147]
	global_load_dwordx2 v[242:243], v[242:243], off
	v_lshl_add_u64 v[244:245], s[30:31], 0, v[146:147]
	global_load_dwordx2 v[244:245], v[244:245], off
	v_lshl_add_u64 v[246:247], s[28:29], 0, v[146:147]
	global_load_dwordx2 v[246:247], v[246:247], off
	v_lshl_add_u64 v[230:231], s[0:1], 0, v[146:147]
	global_load_dwordx2 v[230:231], v[230:231], off
	v_lshl_add_u64 v[232:233], s[42:43], 0, v[146:147]
	global_load_dwordx2 v[232:233], v[232:233], off
	v_lshl_add_u64 v[234:235], s[2:3], 0, v[146:147]
	global_load_dwordx2 v[234:235], v[234:235], off
	s_nop 0
	s_nop 0
	v_pk_fma_f32 v[152:153], v[0:1], v[148:149], 0 op_sel_hi:[0,1,0]
	v_pk_fma_f32 v[152:153], v[0:1], v[158:159], v[152:153] op_sel:[1,0,0]
	s_nop 0
	s_waitcnt vmcnt(8)
	v_lshlrev_b32_e32 v158, 16, v236
	v_and_b32_e32 v159, 0xffff0000, v236
	v_lshlrev_b32_e32 v156, 16, v237
	v_and_b32_e32 v157, 0xffff0000, v237
	v_pk_fma_f32 v[154:155], v[2:3], v[156:157], v[154:155] op_sel_hi:[0,1,1]
	s_nop 0
	s_nop 0
	v_pk_fma_f32 v[152:153], v[2:3], v[158:159], v[152:153] op_sel_hi:[0,1,1]
	v_mov_b32_e32 v2, v3
	s_nop 0
	s_waitcnt vmcnt(7)
	v_lshlrev_b32_e32 v158, 16, v238
	v_and_b32_e32 v159, 0xffff0000, v238
	v_lshlrev_b32_e32 v156, 16, v239
	v_and_b32_e32 v157, 0xffff0000, v239
	v_pk_fma_f32 v[154:155], v[2:3], v[156:157], v[154:155] op_sel_hi:[0,1,1]
	v_pk_fma_f32 v[2:3], v[2:3], v[158:159], v[152:153] op_sel_hi:[0,1,1]
	s_nop 0
	s_nop 0
	s_nop 0
	s_waitcnt vmcnt(6)
	v_lshlrev_b32_e32 v156, 16, v240
	v_and_b32_e32 v157, 0xffff0000, v240
	v_lshlrev_b32_e32 v152, 16, v241
	v_and_b32_e32 v153, 0xffff0000, v241
	s_waitcnt lgkmcnt(2)
	v_pk_fma_f32 v[152:153], v[12:13], v[152:153], v[154:155] op_sel_hi:[0,1,1]
	s_nop 0
	s_nop 0
	v_pk_fma_f32 v[2:3], v[12:13], v[156:157], v[2:3] op_sel_hi:[0,1,1]
	s_nop 0
	s_waitcnt vmcnt(5)
	v_lshlrev_b32_e32 v156, 16, v242
	v_and_b32_e32 v157, 0xffff0000, v242
	v_lshlrev_b32_e32 v154, 16, v243
	v_and_b32_e32 v155, 0xffff0000, v243
	v_pk_fma_f32 v[152:153], v[12:13], v[154:155], v[152:153] op_sel:[1,0,0]
	v_pk_fma_f32 v[2:3], v[12:13], v[156:157], v[2:3] op_sel:[1,0,0]
	s_nop 0
	s_nop 0
	s_nop 0
	s_waitcnt vmcnt(4)
	v_lshlrev_b32_e32 v154, 16, v244
	v_and_b32_e32 v155, 0xffff0000, v244
	v_lshlrev_b32_e32 v12, 16, v245
	v_and_b32_e32 v13, 0xffff0000, v245
	v_pk_fma_f32 v[12:13], v[14:15], v[12:13], v[152:153] op_sel_hi:[0,1,1]
	s_nop 0
	s_nop 0
	v_pk_fma_f32 v[2:3], v[14:15], v[154:155], v[2:3] op_sel_hi:[0,1,1]
	v_mov_b32_e32 v14, v15
	s_nop 0
	s_waitcnt vmcnt(3)
	v_lshlrev_b32_e32 v154, 16, v246
	v_and_b32_e32 v155, 0xffff0000, v246
	v_lshlrev_b32_e32 v152, 16, v247
	v_and_b32_e32 v153, 0xffff0000, v247
	v_pk_fma_f32 v[12:13], v[14:15], v[152:153], v[12:13] op_sel_hi:[0,1,1]
	v_pk_fma_f32 v[2:3], v[14:15], v[154:155], v[2:3] op_sel_hi:[0,1,1]
	s_nop 0
	s_nop 0
	s_nop 0
	s_waitcnt vmcnt(2)
	v_lshlrev_b32_e32 v152, 16, v230
	v_and_b32_e32 v153, 0xffff0000, v230
	v_lshlrev_b32_e32 v14, 16, v231
	v_and_b32_e32 v15, 0xffff0000, v231
	s_waitcnt lgkmcnt(1)
	v_pk_fma_f32 v[12:13], v[8:9], v[14:15], v[12:13] op_sel_hi:[0,1,1]
	s_nop 0
	s_nop 0
	v_pk_fma_f32 v[2:3], v[8:9], v[152:153], v[2:3] op_sel_hi:[0,1,1]
	s_nop 0
	s_waitcnt vmcnt(1)
	v_lshlrev_b32_e32 v152, 16, v232
	v_and_b32_e32 v153, 0xffff0000, v232
	v_lshlrev_b32_e32 v14, 16, v233
	v_and_b32_e32 v15, 0xffff0000, v233
	v_pk_fma_f32 v[12:13], v[8:9], v[14:15], v[12:13] op_sel:[1,0,0]
	v_pk_fma_f32 v[2:3], v[8:9], v[152:153], v[2:3] op_sel:[1,0,0]
	s_nop 0
	s_nop 0
	s_nop 0
	s_waitcnt vmcnt(0)
	v_lshlrev_b32_e32 v14, 16, v234
	v_and_b32_e32 v15, 0xffff0000, v234
	v_lshlrev_b32_e32 v8, 16, v235
	v_and_b32_e32 v9, 0xffff0000, v235
	v_pk_fma_f32 v[8:9], v[10:11], v[8:9], v[12:13] op_sel_hi:[0,1,1]
	v_lshl_add_u64 v[236:237], s[36:37], 0, v[146:147]
	global_load_dwordx2 v[236:237], v[236:237], off
	v_lshl_add_u64 v[238:239], s[52:53], 0, v[146:147]
	global_load_dwordx2 v[238:239], v[238:239], off
	v_lshl_add_u64 v[240:241], s[50:51], 0, v[146:147]
	global_load_dwordx2 v[240:241], v[240:241], off
	v_lshl_add_u64 v[242:243], s[26:27], 0, v[146:147]
	global_load_dwordx2 v[242:243], v[242:243], off
	v_lshl_add_u64 v[244:245], s[24:25], 0, v[146:147]
	global_load_dwordx2 v[244:245], v[244:245], off
	s_nop 0
	s_nop 0
	v_pk_fma_f32 v[2:3], v[10:11], v[14:15], v[2:3] op_sel_hi:[0,1,1]
	v_mov_b32_e32 v10, v11
	s_nop 0
	s_waitcnt vmcnt(4)
	v_lshlrev_b32_e32 v14, 16, v236
	v_and_b32_e32 v15, 0xffff0000, v236
	v_lshlrev_b32_e32 v12, 16, v237
	v_and_b32_e32 v13, 0xffff0000, v237
	v_pk_fma_f32 v[8:9], v[10:11], v[12:13], v[8:9] op_sel_hi:[0,1,1]
	v_pk_fma_f32 v[2:3], v[10:11], v[14:15], v[2:3] op_sel_hi:[0,1,1]
	s_nop 0
	s_nop 0
	s_nop 0
	s_waitcnt vmcnt(3)
	v_lshlrev_b32_e32 v12, 16, v238
	v_and_b32_e32 v13, 0xffff0000, v238
	v_lshlrev_b32_e32 v10, 16, v239
	v_and_b32_e32 v11, 0xffff0000, v239
	s_waitcnt lgkmcnt(0)
	v_pk_fma_f32 v[8:9], v[4:5], v[10:11], v[8:9] op_sel_hi:[0,1,1]
	s_nop 0
	s_nop 0
	v_pk_fma_f32 v[2:3], v[4:5], v[12:13], v[2:3] op_sel_hi:[0,1,1]
	s_nop 0
	s_waitcnt vmcnt(2)
	v_lshlrev_b32_e32 v12, 16, v240
	v_and_b32_e32 v13, 0xffff0000, v240
	v_lshlrev_b32_e32 v10, 16, v241
	v_and_b32_e32 v11, 0xffff0000, v241
	v_pk_fma_f32 v[8:9], v[4:5], v[10:11], v[8:9] op_sel:[1,0,0]
	v_pk_fma_f32 v[2:3], v[4:5], v[12:13], v[2:3] op_sel:[1,0,0]
	s_nop 0
	s_nop 0
	s_nop 0
	s_waitcnt vmcnt(1)
	v_lshlrev_b32_e32 v10, 16, v242
	v_and_b32_e32 v11, 0xffff0000, v242
	v_lshlrev_b32_e32 v4, 16, v243
	v_and_b32_e32 v5, 0xffff0000, v243
	v_pk_fma_f32 v[4:5], v[6:7], v[4:5], v[8:9] op_sel_hi:[0,1,1]
	s_nop 0
	s_nop 0
	v_pk_fma_f32 v[2:3], v[6:7], v[10:11], v[2:3] op_sel_hi:[0,1,1]
	v_mov_b32_e32 v6, v7
	s_nop 0
	s_waitcnt vmcnt(0)
	v_lshlrev_b32_e32 v10, 16, v244
	v_and_b32_e32 v11, 0xffff0000, v244
	v_lshlrev_b32_e32 v8, 16, v245
	v_and_b32_e32 v9, 0xffff0000, v245
	v_pk_mul_f32 v[14:15], v[6:7], v[10:11] op_sel_hi:[0,1]
	v_pk_fma_f32 v[2:3], v[6:7], v[10:11], v[2:3] op_sel_hi:[0,1,1]
	v_pk_mul_f32 v[12:13], v[6:7], v[8:9] op_sel_hi:[0,1]
	v_pk_fma_f32 v[8:9], v[6:7], v[8:9], v[4:5] op_sel_hi:[0,1,1]
	v_pk_fma_f32 v[10:11], v[92:93], v[2:3], v[14:15] op_sel_hi:[0,1,1] neg_lo:[0,0,1] neg_hi:[0,0,1]
	v_lshlrev_b64 v[14:15], 1, v[132:133]
	v_pk_fma_f32 v[4:5], v[0:1], v[148:149], v[2:3] op_sel_hi:[0,1,1] neg_lo:[1,0,0] neg_hi:[1,0,0]
	v_pk_fma_f32 v[0:1], v[0:1], v[150:151], v[8:9] op_sel_hi:[0,1,1] neg_lo:[1,0,0] neg_hi:[1,0,0]
	v_pk_fma_f32 v[12:13], v[92:93], v[8:9], v[12:13] op_sel_hi:[0,1,1] neg_lo:[0,0,1] neg_hi:[0,0,1]
	v_lshl_add_u64 v[236:237], s[22:23], 0, v[14:15]
	global_load_dwordx2 v[236:237], v[236:237], off offset:3072
	v_lshl_add_u64 v[238:239], s[20:21], 0, v[14:15]
	global_load_dwordx2 v[238:239], v[238:239], off offset:3072
	v_lshl_add_u64 v[8:9], s[22:23], 0, v[14:15]
	s_nop 0
	v_pk_fma_f32 v[0:1], v[136:137], v[142:143], v[0:1] op_sel_hi:[0,1,1]
	v_pk_fma_f32 v[6:7], v[94:95], v[0:1], v[140:141] op_sel_hi:[0,1,1] neg_lo:[0,0,1] neg_hi:[0,0,1]
	v_lshl_add_u32 v0, v134, 2, s17
	ds_read_b128 v[0:3], v0
	v_pk_fma_f32 v[4:5], v[136:137], v[138:139], v[4:5] op_sel_hi:[0,1,1]
	v_pk_fma_f32 v[4:5], v[94:95], v[4:5], v[144:145] op_sel_hi:[0,1,1] neg_lo:[0,0,1] neg_hi:[0,0,1]
	s_nop 0
	s_waitcnt vmcnt(1)
	v_lshlrev_b32_e32 v134, 16, v236
	v_and_b32_e32 v135, 0xffff0000, v236
	v_lshlrev_b32_e32 v132, 16, v237
	v_and_b32_e32 v133, 0xffff0000, v237
	s_waitcnt lgkmcnt(0)
	v_pk_fma_f32 v[134:135], v[0:1], v[10:11], v[134:135]
	v_lshl_add_u64 v[10:11], s[20:21], 0, v[14:15]
	v_pk_fma_f32 v[132:133], v[2:3], v[12:13], v[132:133]
	s_nop 0
	s_nop 0
	s_waitcnt vmcnt(0)
	v_lshlrev_b32_e32 v14, 16, v238
	v_and_b32_e32 v15, 0xffff0000, v238
	v_lshlrev_b32_e32 v12, 16, v239
	v_and_b32_e32 v13, 0xffff0000, v239
	v_pk_fma_f32 v[138:139], v[0:1], v[4:5], v[14:15]
	v_cvt_pk_bf16_f32 v0, v134, v135
	v_cvt_pk_bf16_f32 v1, v132, v133
	v_pk_fma_f32 v[136:137], v[2:3], v[6:7], v[12:13]
	v_cvt_pk_bf16_f32 v2, v138, v139
	s_nop 0
	v_cvt_pk_bf16_f32 v3, v136, v137
	global_store_dwordx2 v[8:9], v[0:1], off offset:3072
	global_store_dwordx2 v[10:11], v[2:3], off offset:3072
	v_mov_b32_e32 v0, v21
	ds_read_b32 v144, v27 offset:64
	v_lshlrev_b32_e32 v140, 2, v0
	v_add_u32_e32 v142, 0x700, v140
	v_ashrrev_i32_e32 v143, 31, v142
	v_lshlrev_b64 v[154:155], 1, v[142:143]
	v_lshl_add_u64 v[0:1], vcc, 0, v[154:155]
	global_load_dwordx2 v[0:1], v[0:1], off
	v_lshl_add_u64 v[156:157], s[76:77], 0, v[154:155]
	v_lshl_add_u64 v[164:165], s[10:11], 0, v[154:155]
	v_ashrrev_i32_e32 v141, 31, v140
	s_nop 0
	s_waitcnt vmcnt(0)
	v_lshlrev_b32_e32 v146, 16, v0
	v_and_b32_e32 v147, 0xffff0000, v0
	v_lshlrev_b32_e32 v150, 16, v1
	v_and_b32_e32 v151, 0xffff0000, v1
	ds_read_b128 v[0:3], v27
	ds_read_b128 v[12:15], v27 offset:16
	ds_read_b128 v[8:11], v27 offset:32
	ds_read_b128 v[4:7], v27 offset:48
	global_load_dwordx2 v[158:159], v[156:157], off
	s_waitcnt lgkmcnt(4)
	v_pk_mul_f32 v[152:153], v[144:145], v[146:147] op_sel_hi:[0,1]
	global_load_dwordx2 v[164:165], v[164:165], off
	v_pk_mul_f32 v[148:149], v[144:145], v[150:151] op_sel_hi:[0,1]
	s_nop 0
	s_waitcnt vmcnt(1)
	v_lshlrev_b32_e32 v156, 16, v158
	v_and_b32_e32 v157, 0xffff0000, v158
	v_lshlrev_b32_e32 v158, 16, v159
	v_and_b32_e32 v159, 0xffff0000, v159
	s_waitcnt lgkmcnt(3)
	v_pk_fma_f32 v[162:163], v[0:1], v[158:159], 0 op_sel_hi:[0,1,0]
	s_nop 0
	s_waitcnt vmcnt(0)
	v_lshlrev_b32_e32 v166, 16, v164
	v_and_b32_e32 v167, 0xffff0000, v164
	v_lshlrev_b32_e32 v164, 16, v165
	v_and_b32_e32 v165, 0xffff0000, v165
	v_pk_fma_f32 v[162:163], v[0:1], v[164:165], v[162:163] op_sel:[1,0,0]
	v_lshl_add_u64 v[236:237], s[8:9], 0, v[154:155]
	global_load_dwordx2 v[236:237], v[236:237], off
	v_lshl_add_u64 v[238:239], s[44:45], 0, v[154:155]
	global_load_dwordx2 v[238:239], v[238:239], off
	v_lshl_add_u64 v[240:241], s[48:49], 0, v[154:155]
	global_load_dwordx2 v[240:241], v[240:241], off
	v_lshl_add_u64 v[242:243], s[46:47], 0, v[154:155]
	global_load_dwordx2 v[242:243], v[242:243], off
	v_lshl_add_u64 v[244:245], s[30:31], 0, v[154:155]
	global_load_dwordx2 v[244:245], v[244:245], off
	v_lshl_add_u64 v[246:247], s[28:29], 0, v[154:155]
	global_load_dwordx2 v[246:247], v[246:247], off
	v_lshl_add_u64 v[230:231], s[0:1], 0, v[154:155]
	global_load_dwordx2 v[230:231], v[230:231], off
	v_lshl_add_u64 v[232:233], s[42:43], 0, v[154:155]
	global_load_dwordx2 v[232:233], v[232:233], off
	v_lshl_add_u64 v[234:235], s[2:3], 0, v[154:155]
	global_load_dwordx2 v[234:235], v[234:235], off
	s_nop 0
	s_nop 0
	v_pk_fma_f32 v[160:161], v[0:1], v[156:157], 0 op_sel_hi:[0,1,0]
	v_pk_fma_f32 v[160:161], v[0:1], v[166:167], v[160:161] op_sel:[1,0,0]
	s_nop 0
	s_waitcnt vmcnt(8)
	v_lshlrev_b32_e32 v166, 16, v236
	v_and_b32_e32 v167, 0xffff0000, v236
	v_lshlrev_b32_e32 v164, 16, v237
	v_and_b32_e32 v165, 0xffff0000, v237
	v_pk_fma_f32 v[162:163], v[2:3], v[164:165], v[162:163] op_sel_hi:[0,1,1]
	s_nop 0
	s_nop 0
	v_pk_fma_f32 v[160:161], v[2:3], v[166:167], v[160:161] op_sel_hi:[0,1,1]
	v_mov_b32_e32 v2, v3
	s_nop 0
	s_waitcnt vmcnt(7)
	v_lshlrev_b32_e32 v166, 16, v238
	v_and_b32_e32 v167, 0xffff0000, v238
	v_lshlrev_b32_e32 v164, 16, v239
	v_and_b32_e32 v165, 0xffff0000, v239
	v_pk_fma_f32 v[162:163], v[2:3], v[164:165], v[162:163] op_sel_hi:[0,1,1]
	v_pk_fma_f32 v[2:3], v[2:3], v[166:167], v[160:161] op_sel_hi:[0,1,1]
	s_nop 0
	s_nop 0
	s_nop 0
	s_waitcnt vmcnt(6)
	v_lshlrev_b32_e32 v164, 16, v240
	v_and_b32_e32 v165, 0xffff0000, v240
	v_lshlrev_b32_e32 v160, 16, v241
	v_and_b32_e32 v161, 0xffff0000, v241
	s_waitcnt lgkmcnt(2)
	v_pk_fma_f32 v[160:161], v[12:13], v[160:161], v[162:163] op_sel_hi:[0,1,1]
	s_nop 0
	s_nop 0
	v_pk_fma_f32 v[2:3], v[12:13], v[164:165], v[2:3] op_sel_hi:[0,1,1]
	s_nop 0
	s_waitcnt vmcnt(5)
	v_lshlrev_b32_e32 v164, 16, v242
	v_and_b32_e32 v165, 0xffff0000, v242
	v_lshlrev_b32_e32 v162, 16, v243
	v_and_b32_e32 v163, 0xffff0000, v243
	v_pk_fma_f32 v[160:161], v[12:13], v[162:163], v[160:161] op_sel:[1,0,0]
	v_pk_fma_f32 v[2:3], v[12:13], v[164:165], v[2:3] op_sel:[1,0,0]
	s_nop 0
	s_nop 0
	s_nop 0
	s_waitcnt vmcnt(4)
	v_lshlrev_b32_e32 v162, 16, v244
	v_and_b32_e32 v163, 0xffff0000, v244
	v_lshlrev_b32_e32 v12, 16, v245
	v_and_b32_e32 v13, 0xffff0000, v245
	v_pk_fma_f32 v[12:13], v[14:15], v[12:13], v[160:161] op_sel_hi:[0,1,1]
	s_nop 0
	s_nop 0
	v_pk_fma_f32 v[2:3], v[14:15], v[162:163], v[2:3] op_sel_hi:[0,1,1]
	v_mov_b32_e32 v14, v15
	s_nop 0
	s_waitcnt vmcnt(3)
	v_lshlrev_b32_e32 v162, 16, v246
	v_and_b32_e32 v163, 0xffff0000, v246
	v_lshlrev_b32_e32 v160, 16, v247
	v_and_b32_e32 v161, 0xffff0000, v247
	v_pk_fma_f32 v[12:13], v[14:15], v[160:161], v[12:13] op_sel_hi:[0,1,1]
	v_pk_fma_f32 v[2:3], v[14:15], v[162:163], v[2:3] op_sel_hi:[0,1,1]
	s_nop 0
	s_nop 0
	s_nop 0
	s_waitcnt vmcnt(2)
	v_lshlrev_b32_e32 v160, 16, v230
	v_and_b32_e32 v161, 0xffff0000, v230
	v_lshlrev_b32_e32 v14, 16, v231
	v_and_b32_e32 v15, 0xffff0000, v231
	s_waitcnt lgkmcnt(1)
	v_pk_fma_f32 v[12:13], v[8:9], v[14:15], v[12:13] op_sel_hi:[0,1,1]
	s_nop 0
	s_nop 0
	v_pk_fma_f32 v[2:3], v[8:9], v[160:161], v[2:3] op_sel_hi:[0,1,1]
	s_nop 0
	s_waitcnt vmcnt(1)
	v_lshlrev_b32_e32 v160, 16, v232
	v_and_b32_e32 v161, 0xffff0000, v232
	v_lshlrev_b32_e32 v14, 16, v233
	v_and_b32_e32 v15, 0xffff0000, v233
	v_pk_fma_f32 v[12:13], v[8:9], v[14:15], v[12:13] op_sel:[1,0,0]
	v_pk_fma_f32 v[2:3], v[8:9], v[160:161], v[2:3] op_sel:[1,0,0]
	s_nop 0
	s_nop 0
	s_nop 0
	s_waitcnt vmcnt(0)
	v_lshlrev_b32_e32 v14, 16, v234
	v_and_b32_e32 v15, 0xffff0000, v234
	v_lshlrev_b32_e32 v8, 16, v235
	v_and_b32_e32 v9, 0xffff0000, v235
	v_pk_fma_f32 v[8:9], v[10:11], v[8:9], v[12:13] op_sel_hi:[0,1,1]
	v_lshl_add_u64 v[236:237], s[36:37], 0, v[154:155]
	global_load_dwordx2 v[236:237], v[236:237], off
	v_lshl_add_u64 v[238:239], s[52:53], 0, v[154:155]
	global_load_dwordx2 v[238:239], v[238:239], off
	v_lshl_add_u64 v[240:241], s[50:51], 0, v[154:155]
	global_load_dwordx2 v[240:241], v[240:241], off
	v_lshl_add_u64 v[242:243], s[26:27], 0, v[154:155]
	global_load_dwordx2 v[242:243], v[242:243], off
	v_lshl_add_u64 v[244:245], s[24:25], 0, v[154:155]
	global_load_dwordx2 v[244:245], v[244:245], off
	s_nop 0
	s_nop 0
	v_pk_fma_f32 v[2:3], v[10:11], v[14:15], v[2:3] op_sel_hi:[0,1,1]
	v_mov_b32_e32 v10, v11
	s_nop 0
	s_waitcnt vmcnt(4)
	v_lshlrev_b32_e32 v14, 16, v236
	v_and_b32_e32 v15, 0xffff0000, v236
	v_lshlrev_b32_e32 v12, 16, v237
	v_and_b32_e32 v13, 0xffff0000, v237
	v_pk_fma_f32 v[8:9], v[10:11], v[12:13], v[8:9] op_sel_hi:[0,1,1]
	v_pk_fma_f32 v[2:3], v[10:11], v[14:15], v[2:3] op_sel_hi:[0,1,1]
	s_nop 0
	s_nop 0
	s_nop 0
	s_waitcnt vmcnt(3)
	v_lshlrev_b32_e32 v12, 16, v238
	v_and_b32_e32 v13, 0xffff0000, v238
	v_lshlrev_b32_e32 v10, 16, v239
	v_and_b32_e32 v11, 0xffff0000, v239
	s_waitcnt lgkmcnt(0)
	v_pk_fma_f32 v[8:9], v[4:5], v[10:11], v[8:9] op_sel_hi:[0,1,1]
	s_nop 0
	s_nop 0
	v_pk_fma_f32 v[2:3], v[4:5], v[12:13], v[2:3] op_sel_hi:[0,1,1]
	s_nop 0
	s_waitcnt vmcnt(2)
	v_lshlrev_b32_e32 v12, 16, v240
	v_and_b32_e32 v13, 0xffff0000, v240
	v_lshlrev_b32_e32 v10, 16, v241
	v_and_b32_e32 v11, 0xffff0000, v241
	v_pk_fma_f32 v[8:9], v[4:5], v[10:11], v[8:9] op_sel:[1,0,0]
	v_pk_fma_f32 v[2:3], v[4:5], v[12:13], v[2:3] op_sel:[1,0,0]
	s_nop 0
	s_nop 0
	s_nop 0
	s_waitcnt vmcnt(1)
	v_lshlrev_b32_e32 v10, 16, v242
	v_and_b32_e32 v11, 0xffff0000, v242
	v_lshlrev_b32_e32 v4, 16, v243
	v_and_b32_e32 v5, 0xffff0000, v243
	v_pk_fma_f32 v[4:5], v[6:7], v[4:5], v[8:9] op_sel_hi:[0,1,1]
	s_nop 0
	s_nop 0
	v_pk_fma_f32 v[2:3], v[6:7], v[10:11], v[2:3] op_sel_hi:[0,1,1]
	v_mov_b32_e32 v6, v7
	s_nop 0
	s_waitcnt vmcnt(0)
	v_lshlrev_b32_e32 v10, 16, v244
	v_and_b32_e32 v11, 0xffff0000, v244
	v_lshlrev_b32_e32 v8, 16, v245
	v_and_b32_e32 v9, 0xffff0000, v245
	v_pk_fma_f32 v[2:3], v[6:7], v[10:11], v[2:3] op_sel_hi:[0,1,1]
	v_pk_mul_f32 v[12:13], v[6:7], v[8:9] op_sel_hi:[0,1]
	v_pk_mul_f32 v[14:15], v[6:7], v[10:11] op_sel_hi:[0,1]
	v_pk_fma_f32 v[4:5], v[6:7], v[8:9], v[4:5] op_sel_hi:[0,1,1]
	v_pk_fma_f32 v[6:7], v[0:1], v[156:157], v[2:3] op_sel_hi:[0,1,1] neg_lo:[1,0,0] neg_hi:[1,0,0]
	v_pk_fma_f32 v[0:1], v[0:1], v[158:159], v[4:5] op_sel_hi:[0,1,1] neg_lo:[1,0,0] neg_hi:[1,0,0]
	v_pk_fma_f32 v[6:7], v[144:145], v[146:147], v[6:7] op_sel_hi:[0,1,1]
	v_pk_fma_f32 v[4:5], v[92:93], v[4:5], v[12:13] op_sel_hi:[0,1,1] neg_lo:[0,0,1] neg_hi:[0,0,1]
	v_lshlrev_b64 v[12:13], 1, v[140:141]
	v_pk_fma_f32 v[8:9], v[94:95], v[6:7], v[152:153] op_sel_hi:[0,1,1] neg_lo:[0,0,1] neg_hi:[0,0,1]
	v_pk_fma_f32 v[6:7], v[92:93], v[2:3], v[14:15] op_sel_hi:[0,1,1] neg_lo:[0,0,1] neg_hi:[0,0,1]
	v_lshl_add_u64 v[236:237], s[22:23], 0, v[12:13]
	global_load_dwordx2 v[236:237], v[236:237], off offset:3584
	v_lshl_add_u64 v[238:239], s[20:21], 0, v[12:13]
	global_load_dwordx2 v[238:239], v[238:239], off offset:3584
	v_lshl_add_u64 v[14:15], s[22:23], 0, v[12:13]
	s_nop 0
	v_pk_fma_f32 v[0:1], v[144:145], v[150:151], v[0:1] op_sel_hi:[0,1,1]
	v_pk_fma_f32 v[10:11], v[94:95], v[0:1], v[148:149] op_sel_hi:[0,1,1] neg_lo:[0,0,1] neg_hi:[0,0,1]
	v_lshl_add_u32 v0, v142, 2, s17
	ds_read_b128 v[0:3], v0
	s_nop 0
	s_waitcnt vmcnt(1)
	v_lshlrev_b32_e32 v94, 16, v236
	v_and_b32_e32 v95, 0xffff0000, v236
	v_lshlrev_b32_e32 v92, 16, v237
	v_and_b32_e32 v93, 0xffff0000, v237
	s_waitcnt lgkmcnt(0)
	v_pk_fma_f32 v[4:5], v[2:3], v[4:5], v[92:93]
	v_lshl_add_u64 v[92:93], s[20:21], 0, v[12:13]
	s_nop 0
	v_pk_fma_f32 v[6:7], v[0:1], v[6:7], v[94:95]
	s_nop 0
	s_waitcnt vmcnt(0)
	v_lshlrev_b32_e32 v94, 16, v238
	v_and_b32_e32 v95, 0xffff0000, v238
	v_lshlrev_b32_e32 v12, 16, v239
	v_and_b32_e32 v13, 0xffff0000, v239
	v_pk_fma_f32 v[10:11], v[2:3], v[10:11], v[12:13]
	v_pk_fma_f32 v[12:13], v[0:1], v[8:9], v[94:95]
	v_cvt_pk_bf16_f32 v0, v6, v7
	v_cvt_pk_bf16_f32 v1, v4, v5
	s_nop 0
	v_cvt_pk_bf16_f32 v2, v12, v13
	v_cvt_pk_bf16_f32 v3, v10, v11
	global_store_dwordx2 v[14:15], v[0:1], off offset:3584
	global_store_dwordx2 v[92:93], v[2:3], off offset:3584
	v_mul_f32_e32 v0, v87, v87
	v_mul_f32_e32 v1, v85, v85
	v_fmac_f32_e32 v0, v86, v86
	v_fmac_f32_e32 v1, v84, v84
	v_mov_b32_e32 v2, v83
	v_mov_b32_e32 v3, v91
	v_add_f32_e32 v14, v0, v1
	v_mov_b32_e32 v0, v82
	v_mov_b32_e32 v1, v90
	v_pk_mul_f32 v[2:3], v[2:3], v[2:3]
	v_mov_b32_e32 v8, v81
	v_mov_b32_e32 v9, v89
	v_pk_fma_f32 v[0:1], v[0:1], v[0:1], v[2:3]
	v_mov_b32_e32 v2, v80
	v_mov_b32_e32 v3, v88
	v_pk_mul_f32 v[8:9], v[8:9], v[8:9]
	v_mul_f32_e32 v29, v115, v115
	v_pk_fma_f32 v[2:3], v[2:3], v[2:3], v[8:9]
	v_pk_mul_f32 v[8:9], v[102:103], v[102:103]
	v_pk_add_f32 v[0:1], v[0:1], v[2:3]
	v_mul_f32_e32 v2, v99, v99
	v_mul_f32_e32 v3, v97, v97
	v_fmac_f32_e32 v2, v98, v98
	v_fmac_f32_e32 v3, v96, v96
	v_add_f32_e32 v2, v2, v3
	v_add_f32_e32 v27, v14, v2
	v_pk_mul_f32 v[2:3], v[100:101], v[100:101]
	v_pk_add_f32 v[0:1], v[0:1], v[0:1] op_sel:[0,1] op_sel_hi:[1,0]
	v_pk_mov_b32 v[14:15], v[8:9], v[2:3] op_sel:[1,0]
	v_mov_b32_e32 v9, v3
	v_pk_add_f32 v[2:3], v[14:15], v[8:9]
	v_mul_f32_e32 v8, v107, v107
	v_mul_f32_e32 v9, v105, v105
	v_fmac_f32_e32 v8, v106, v106
	v_fmac_f32_e32 v9, v104, v104
	v_add_f32_e32 v8, v8, v9
	v_add_f32_e32 v27, v27, v8
	v_mul_f32_e32 v8, v118, v118
	v_mul_f32_e32 v9, v119, v119
	v_pk_add_f32 v[2:3], v[2:3], v[2:3] op_sel:[0,1] op_sel_hi:[1,0]
	v_mov_b32_e32 v1, v8
	v_mov_b32_e32 v3, v9
	v_pk_add_f32 v[0:1], v[0:1], v[2:3]
	v_mul_f32_e32 v2, v111, v111
	v_mul_f32_e32 v8, v109, v109
	v_mul_f32_e32 v14, v116, v116
	v_mul_f32_e32 v15, v117, v117
	v_pk_fma_f32 v[2:3], v[110:111], v[110:111], v[2:3] op_sel_hi:[1,1,0]
	v_pk_fma_f32 v[8:9], v[108:109], v[108:109], v[8:9] op_sel_hi:[1,1,0]
	v_mov_b32_e32 v3, v14
	v_mov_b32_e32 v9, v15
	v_pk_add_f32 v[2:3], v[2:3], v[8:9]
	v_pk_mul_f32 v[8:9], v[126:127], v[126:127]
	v_pk_add_f32 v[0:1], v[0:1], v[2:3]
	v_pk_mul_f32 v[2:3], v[124:125], v[124:125]
	v_pk_add_f32 v[0:1], v[0:1], v[0:1] op_sel:[0,1] op_sel_hi:[1,0]
	v_pk_mov_b32 v[14:15], v[8:9], v[2:3] op_sel:[1,0]
	v_mov_b32_e32 v9, v3
	v_pk_add_f32 v[2:3], v[14:15], v[8:9]
	v_mul_f32_e32 v8, v6, v6
	v_mul_f32_e32 v9, v7, v7
	v_pk_add_f32 v[2:3], v[2:3], v[2:3] op_sel:[0,1] op_sel_hi:[1,0]
	v_mov_b32_e32 v1, v8
	v_mov_b32_e32 v3, v9
	v_pk_add_f32 v[0:1], v[0:1], v[2:3]
	v_mul_f32_e32 v2, v135, v135
	v_mul_f32_e32 v8, v133, v133
	v_mul_f32_e32 v14, v4, v4
	v_mul_f32_e32 v15, v5, v5
	v_pk_fma_f32 v[2:3], v[134:135], v[134:135], v[2:3] op_sel_hi:[1,1,0]
	v_pk_fma_f32 v[8:9], v[132:133], v[132:133], v[8:9] op_sel_hi:[1,1,0]
	v_mov_b32_e32 v3, v14
	v_mov_b32_e32 v9, v15
	v_pk_add_f32 v[2:3], v[2:3], v[8:9]
	v_mul_f32_e32 v33, v113, v113
	v_pk_add_f32 v[0:1], v[0:1], v[2:3]
	v_xor_b32_e32 v2, 1, v188
	v_add_f32_e32 v0, v0, v1
	v_and_b32_e32 v1, 64, v188
	v_add_u32_e32 v1, 64, v1
	v_cmp_lt_i32_e32 vcc, v2, v1
	v_fmac_f32_e32 v29, v114, v114
	v_fmac_f32_e32 v33, v112, v112
	v_cndmask_b32_e32 v2, v188, v2, vcc
	v_lshlrev_b32_e32 v31, 2, v2
	ds_bpermute_b32 v2, v31, v0
	v_add_f32_e32 v3, v29, v33
	v_mul_f32_e32 v8, v123, v123
	v_mul_f32_e32 v9, v121, v121
	v_fmac_f32_e32 v8, v122, v122
	s_waitcnt lgkmcnt(0)
	v_add_f32_e32 v0, v0, v2
	v_xor_b32_e32 v2, 2, v188
	v_cmp_lt_i32_e32 vcc, v2, v1
	v_fmac_f32_e32 v9, v120, v120
	v_add_f32_e32 v3, v27, v3
	v_cndmask_b32_e32 v2, v188, v2, vcc
	v_lshlrev_b32_e32 v33, 2, v2
	ds_bpermute_b32 v2, v33, v0
	v_add_f32_e32 v8, v8, v9
	v_add_f32_e32 v3, v3, v8
	v_mul_f32_e32 v8, v131, v131
	v_mul_f32_e32 v9, v129, v129
	s_waitcnt lgkmcnt(0)
	v_add_f32_e32 v0, v0, v2
	v_xor_b32_e32 v2, 4, v188
	v_cmp_lt_i32_e32 vcc, v2, v1
	v_fmac_f32_e32 v8, v130, v130
	v_fmac_f32_e32 v9, v128, v128
	v_cndmask_b32_e32 v2, v188, v2, vcc
	v_lshlrev_b32_e32 v35, 2, v2
	ds_bpermute_b32 v2, v35, v0
	v_add_f32_e32 v8, v8, v9
	v_add_f32_e32 v3, v3, v8
	v_mul_f32_e32 v8, v139, v139
	v_mul_f32_e32 v9, v137, v137
	s_waitcnt lgkmcnt(0)
	v_add_f32_e32 v0, v0, v2
	v_xor_b32_e32 v2, 8, v188
	v_cmp_lt_i32_e32 vcc, v2, v1
	v_fmac_f32_e32 v8, v138, v138
	v_fmac_f32_e32 v9, v136, v136
	v_cndmask_b32_e32 v2, v188, v2, vcc
	v_lshlrev_b32_e32 v41, 2, v2
	ds_bpermute_b32 v2, v41, v0
	v_add_f32_e32 v8, v8, v9
	s_waitcnt lgkmcnt(0)
	v_add_f32_e32 v0, v0, v2
	v_xor_b32_e32 v2, 16, v188
	v_cmp_lt_i32_e32 vcc, v2, v1
	s_nop 1
	v_cndmask_b32_e32 v2, v188, v2, vcc
	v_lshlrev_b32_e32 v37, 2, v2
	ds_bpermute_b32 v2, v37, v0
	s_waitcnt lgkmcnt(0)
	v_add_f32_e32 v0, v0, v2
	v_xor_b32_e32 v2, 32, v188
	v_cmp_lt_i32_e32 vcc, v2, v1
	s_nop 1
	v_cndmask_b32_e32 v1, v188, v2, vcc
	v_lshlrev_b32_e32 v39, 2, v1
	ds_bpermute_b32 v1, v39, v0
	v_add_f32_e32 v2, v3, v8
	v_mul_f32_e32 v3, v13, v13
	v_mul_f32_e32 v8, v11, v11
	v_fmac_f32_e32 v3, v12, v12
	s_waitcnt lgkmcnt(0)
	v_add_f32_e32 v0, v0, v1
	v_fmamk_f32 v0, v0, 0x3a000000, v189
	v_mul_f32_e32 v1, 0x4f800000, v0
	v_cmp_gt_f32_e32 vcc, s84, v0
	v_fmac_f32_e32 v8, v10, v10
	v_add_f32_e32 v3, v3, v8
	v_cndmask_b32_e32 v0, v0, v1, vcc
	v_sqrt_f32_e32 v1, v0
	v_add_f32_e32 v2, v2, v3
	v_add_u32_e32 v3, -1, v1
	v_fma_f32 v8, -v3, v1, v0
	v_cmp_ge_f32_e64 s[46:47], 0, v8
	v_add_u32_e32 v8, 1, v1
	s_nop 0
	v_cndmask_b32_e64 v3, v1, v3, s[46:47]
	v_fma_f32 v1, -v8, v1, v0
	v_cmp_lt_f32_e64 s[46:47], 0, v1
	s_nop 1
	v_cndmask_b32_e64 v1, v3, v8, s[46:47]
	v_mul_f32_e32 v3, 0x37800000, v1
	v_cndmask_b32_e32 v1, v1, v3, vcc
	ds_bpermute_b32 v3, v31, v2
	v_cmp_class_f32_e32 vcc, v0, v190
	v_cndmask_b32_e32 v27, v1, v0, vcc
	s_waitcnt lgkmcnt(0)
	v_add_f32_e32 v0, v2, v3
	ds_bpermute_b32 v1, v33, v0
	v_div_scale_f32 v43, s[0:1], v27, v27, 1.0
	v_rcp_f32_e32 v29, v43
	v_div_scale_f32 v47, vcc, 1.0, v27, 1.0
	s_waitcnt lgkmcnt(0)
	v_add_f32_e32 v0, v0, v1
	ds_bpermute_b32 v1, v35, v0
	v_fma_f32 v2, -v43, v29, 1.0
	v_fmac_f32_e32 v29, v2, v29
	v_mul_f32_e32 v45, v47, v29
	v_fma_f32 v51, -v43, v45, v47
	s_waitcnt lgkmcnt(0)
	v_add_f32_e32 v49, v0, v1
	ds_read_b128 v[0:3], v25
	ds_read_b128 v[92:95], v25 offset:1024
	ds_read_b128 v[140:143], v25 offset:2048
	ds_read_b128 v[144:147], v25 offset:3072
	ds_read_b128 v[148:151], v25 offset:4096
	ds_read_b128 v[152:155], v25 offset:5120
	ds_read_b128 v[156:159], v25 offset:6144
	ds_read_b128 v[160:163], v25 offset:7168
	ds_read_b128 v[164:167], v25 offset:8192
	ds_read_b128 v[174:177], v25 offset:9216
	ds_read_b128 v[178:181], v25 offset:10240
	ds_read_b128 v[182:185], v25 offset:11264
	ds_read_b128 v[198:201], v25 offset:12288
	ds_read_b128 v[202:205], v25 offset:13312
	ds_read_b128 v[206:209], v25 offset:14336
	ds_read_b128 v[210:213], v25 offset:15360
	s_waitcnt lgkmcnt(7)
	v_mov_b32_e32 v8, v164
	v_mov_b32_e32 v9, v1
	v_mov_b32_e32 v1, v165
	v_mov_b32_e32 v164, v166
	v_mov_b32_e32 v165, v3
	v_pk_mul_f32 v[14:15], v[82:83], v[8:9]
	v_pk_mul_f32 v[214:215], v[80:81], v[164:165]
	v_mov_b32_e32 v3, v167
	v_pk_fma_f32 v[14:15], v[82:83], v[0:1], v[14:15] op_sel:[0,0,1] op_sel_hi:[1,1,0]
	v_pk_fma_f32 v[166:167], v[80:81], v[2:3], v[214:215] op_sel:[0,0,1] op_sel_hi:[1,1,0]
	v_pk_mul_f32 v[8:9], v[86:87], v[8:9]
	v_pk_add_f32 v[14:15], v[14:15], v[166:167]
	s_waitcnt lgkmcnt(6)
	v_mov_b32_e32 v166, v174
	v_mov_b32_e32 v167, v93
	v_pk_mul_f32 v[214:215], v[90:91], v[166:167]
	v_mov_b32_e32 v93, v175
	v_pk_fma_f32 v[174:175], v[90:91], v[92:93], v[214:215] op_sel:[0,0,1] op_sel_hi:[1,1,0]
	v_mov_b32_e32 v214, v176
	v_mov_b32_e32 v215, v95
	v_pk_mul_f32 v[216:217], v[88:89], v[214:215]
	v_mov_b32_e32 v95, v177
	v_pk_fma_f32 v[176:177], v[88:89], v[94:95], v[216:217] op_sel:[0,0,1] op_sel_hi:[1,1,0]
	v_pk_add_f32 v[14:15], v[14:15], 0 op_sel_hi:[1,0]
	v_pk_add_f32 v[174:175], v[174:175], v[176:177]
	v_pk_fma_f32 v[0:1], v[86:87], v[0:1], v[8:9] op_sel:[0,0,1] op_sel_hi:[1,1,0]
	v_pk_add_f32 v[14:15], v[14:15], v[174:175]
	s_waitcnt lgkmcnt(5)
	v_mov_b32_e32 v174, v178
	v_mov_b32_e32 v175, v141
	v_mov_b32_e32 v141, v179
	v_mov_b32_e32 v178, v180
	v_mov_b32_e32 v179, v143
	v_pk_mul_f32 v[176:177], v[102:103], v[174:175]
	v_pk_mul_f32 v[216:217], v[100:101], v[178:179]
	v_mov_b32_e32 v143, v181
	v_pk_mul_f32 v[8:9], v[84:85], v[164:165]
	v_pk_fma_f32 v[176:177], v[102:103], v[140:141], v[176:177] op_sel:[0,0,1] op_sel_hi:[1,1,0]
	v_pk_fma_f32 v[180:181], v[100:101], v[142:143], v[216:217] op_sel:[0,0,1] op_sel_hi:[1,1,0]
	v_pk_fma_f32 v[2:3], v[84:85], v[2:3], v[8:9] op_sel:[0,0,1] op_sel_hi:[1,1,0]
	v_pk_add_f32 v[176:177], v[176:177], v[180:181]
	v_pk_add_f32 v[0:1], v[0:1], v[2:3]
	v_pk_mul_f32 v[2:3], v[98:99], v[166:167]
	v_pk_mul_f32 v[8:9], v[96:97], v[214:215]
	v_pk_add_f32 v[14:15], v[14:15], v[176:177]
	s_waitcnt lgkmcnt(4)
	v_mov_b32_e32 v176, v182
	v_mov_b32_e32 v177, v145
	v_mov_b32_e32 v145, v183
	v_mov_b32_e32 v182, v184
	v_mov_b32_e32 v183, v147
	v_pk_fma_f32 v[2:3], v[98:99], v[92:93], v[2:3] op_sel:[0,0,1] op_sel_hi:[1,1,0]
	v_pk_fma_f32 v[8:9], v[96:97], v[94:95], v[8:9] op_sel:[0,0,1] op_sel_hi:[1,1,0]
	v_pk_mul_f32 v[180:181], v[110:111], v[176:177]
	v_pk_mul_f32 v[216:217], v[108:109], v[182:183]
	v_mov_b32_e32 v147, v185
	v_pk_add_f32 v[0:1], v[0:1], 0 op_sel_hi:[1,0]
	v_pk_add_f32 v[2:3], v[2:3], v[8:9]
	v_pk_fma_f32 v[180:181], v[110:111], v[144:145], v[180:181] op_sel:[0,0,1] op_sel_hi:[1,1,0]
	v_pk_fma_f32 v[184:185], v[108:109], v[146:147], v[216:217] op_sel:[0,0,1] op_sel_hi:[1,1,0]
	v_pk_add_f32 v[0:1], v[0:1], v[2:3]
	v_pk_mul_f32 v[2:3], v[106:107], v[174:175]
	v_pk_mul_f32 v[8:9], v[104:105], v[178:179]
	v_pk_add_f32 v[180:181], v[180:181], v[184:185]
	v_pk_fma_f32 v[2:3], v[106:107], v[140:141], v[2:3] op_sel:[0,0,1] op_sel_hi:[1,1,0]
	v_pk_fma_f32 v[8:9], v[104:105], v[142:143], v[8:9] op_sel:[0,0,1] op_sel_hi:[1,1,0]
	v_pk_add_f32 v[14:15], v[14:15], v[180:181]
	s_waitcnt lgkmcnt(3)
	v_mov_b32_e32 v180, v198
	v_mov_b32_e32 v181, v149
	v_mov_b32_e32 v149, v199
	v_mov_b32_e32 v198, v200
	v_mov_b32_e32 v199, v151
	v_pk_add_f32 v[2:3], v[2:3], v[8:9]
	v_pk_mul_f32 v[184:185], v[118:119], v[180:181]
	v_pk_mul_f32 v[216:217], v[116:117], v[198:199]
	v_mov_b32_e32 v151, v201
	v_pk_add_f32 v[0:1], v[0:1], v[2:3]
	v_pk_mul_f32 v[2:3], v[114:115], v[176:177]
	v_pk_mul_f32 v[8:9], v[112:113], v[182:183]
	v_pk_fma_f32 v[184:185], v[118:119], v[148:149], v[184:185] op_sel:[0,0,1] op_sel_hi:[1,1,0]
	v_pk_fma_f32 v[200:201], v[116:117], v[150:151], v[216:217] op_sel:[0,0,1] op_sel_hi:[1,1,0]
	v_pk_fma_f32 v[2:3], v[114:115], v[144:145], v[2:3] op_sel:[0,0,1] op_sel_hi:[1,1,0]
	v_pk_fma_f32 v[8:9], v[112:113], v[146:147], v[8:9] op_sel:[0,0,1] op_sel_hi:[1,1,0]
	v_pk_add_f32 v[184:185], v[184:185], v[200:201]
	v_pk_add_f32 v[2:3], v[2:3], v[8:9]
	v_pk_add_f32 v[14:15], v[14:15], v[184:185]
	s_waitcnt lgkmcnt(2)
	v_mov_b32_e32 v184, v202
	v_mov_b32_e32 v185, v153
	v_mov_b32_e32 v153, v203
	v_mov_b32_e32 v202, v204
	v_mov_b32_e32 v203, v155
	v_pk_add_f32 v[0:1], v[0:1], v[2:3]
	v_pk_mul_f32 v[2:3], v[122:123], v[180:181]
	v_pk_mul_f32 v[8:9], v[120:121], v[198:199]
	v_pk_mul_f32 v[200:201], v[126:127], v[184:185]
	v_pk_mul_f32 v[216:217], v[124:125], v[202:203]
	v_mov_b32_e32 v155, v205
	v_pk_fma_f32 v[2:3], v[122:123], v[148:149], v[2:3] op_sel:[0,0,1] op_sel_hi:[1,1,0]
	v_pk_fma_f32 v[8:9], v[120:121], v[150:151], v[8:9] op_sel:[0,0,1] op_sel_hi:[1,1,0]
	v_pk_fma_f32 v[200:201], v[126:127], v[152:153], v[200:201] op_sel:[0,0,1] op_sel_hi:[1,1,0]
	v_pk_fma_f32 v[204:205], v[124:125], v[154:155], v[216:217] op_sel:[0,0,1] op_sel_hi:[1,1,0]
	v_pk_add_f32 v[2:3], v[2:3], v[8:9]
	v_pk_add_f32 v[200:201], v[200:201], v[204:205]
	v_pk_add_f32 v[0:1], v[0:1], v[2:3]
	v_pk_mul_f32 v[2:3], v[130:131], v[184:185]
	v_pk_mul_f32 v[8:9], v[128:129], v[202:203]
	v_pk_add_f32 v[14:15], v[14:15], v[200:201]
	s_waitcnt lgkmcnt(1)
	v_mov_b32_e32 v200, v206
	v_mov_b32_e32 v201, v157
	v_mov_b32_e32 v157, v207
	v_mov_b32_e32 v206, v208
	v_mov_b32_e32 v207, v159
	v_pk_fma_f32 v[2:3], v[130:131], v[152:153], v[2:3] op_sel:[0,0,1] op_sel_hi:[1,1,0]
	v_pk_fma_f32 v[8:9], v[128:129], v[154:155], v[8:9] op_sel:[0,0,1] op_sel_hi:[1,1,0]
	v_pk_mul_f32 v[204:205], v[134:135], v[200:201]
	v_pk_mul_f32 v[216:217], v[132:133], v[206:207]
	v_mov_b32_e32 v159, v209
	v_pk_add_f32 v[2:3], v[2:3], v[8:9]
	v_pk_fma_f32 v[204:205], v[134:135], v[156:157], v[204:205] op_sel:[0,0,1] op_sel_hi:[1,1,0]
	v_pk_fma_f32 v[208:209], v[132:133], v[158:159], v[216:217] op_sel:[0,0,1] op_sel_hi:[1,1,0]
	v_pk_add_f32 v[0:1], v[0:1], v[2:3]
	v_pk_mul_f32 v[2:3], v[138:139], v[200:201]
	v_pk_mul_f32 v[8:9], v[136:137], v[206:207]
	v_pk_add_f32 v[204:205], v[204:205], v[208:209]
	v_pk_fma_f32 v[2:3], v[138:139], v[156:157], v[2:3] op_sel:[0,0,1] op_sel_hi:[1,1,0]
	v_pk_fma_f32 v[8:9], v[136:137], v[158:159], v[8:9] op_sel:[0,0,1] op_sel_hi:[1,1,0]
	v_pk_add_f32 v[14:15], v[14:15], v[204:205]
	s_waitcnt lgkmcnt(0)
	v_mov_b32_e32 v204, v210
	v_mov_b32_e32 v205, v161
	v_mov_b32_e32 v161, v211
	v_mov_b32_e32 v210, v212
	v_mov_b32_e32 v211, v163
	v_pk_add_f32 v[2:3], v[2:3], v[8:9]
	v_pk_mul_f32 v[208:209], v[6:7], v[204:205]
	v_pk_mul_f32 v[216:217], v[4:5], v[210:211]
	v_mov_b32_e32 v163, v213
	v_pk_add_f32 v[0:1], v[0:1], v[2:3]
	v_pk_mul_f32 v[2:3], v[12:13], v[204:205]
	v_pk_mul_f32 v[8:9], v[10:11], v[210:211]
	v_pk_fma_f32 v[208:209], v[6:7], v[160:161], v[208:209] op_sel:[0,0,1] op_sel_hi:[1,1,0]
	v_pk_fma_f32 v[212:213], v[4:5], v[162:163], v[216:217] op_sel:[0,0,1] op_sel_hi:[1,1,0]
	v_pk_fma_f32 v[2:3], v[12:13], v[160:161], v[2:3] op_sel:[0,0,1] op_sel_hi:[1,1,0]
	v_pk_fma_f32 v[8:9], v[10:11], v[162:163], v[8:9] op_sel:[0,0,1] op_sel_hi:[1,1,0]
	v_pk_add_f32 v[208:209], v[208:209], v[212:213]
	v_pk_add_f32 v[2:3], v[2:3], v[8:9]
	v_pk_add_f32 v[14:15], v[14:15], v[208:209]
	v_pk_add_f32 v[0:1], v[0:1], v[2:3]
	ds_read_b128 v[140:143], v25 offset:16384
	ds_read_b128 v[144:147], v25 offset:17408
	ds_read_b128 v[148:151], v25 offset:18432
	ds_read_b128 v[152:155], v25 offset:19456
	ds_read_b128 v[156:159], v25 offset:20480
	ds_read_b128 v[160:163], v25 offset:21504
	ds_read_b128 v[164:167], v25 offset:22528
	ds_read_b128 v[174:177], v25 offset:23552
	ds_read_b128 v[92:95], v25 offset:24576
	ds_read_b128 v[178:181], v25 offset:25600
	ds_read_b128 v[182:185], v25 offset:26624
	ds_read_b128 v[198:201], v25 offset:27648
	ds_read_b128 v[202:205], v25 offset:28672
	ds_read_b128 v[206:209], v25 offset:29696
	ds_read_b128 v[210:213], v25 offset:30720
	ds_read_b128 v[214:217], v25 offset:31744
	s_waitcnt lgkmcnt(7)
	v_mov_b32_e32 v2, v92
	v_mov_b32_e32 v3, v141
	v_mov_b32_e32 v218, v94
	v_mov_b32_e32 v219, v143
	v_pk_mul_f32 v[8:9], v[82:83], v[2:3]
	v_mov_b32_e32 v141, v93
	v_pk_mul_f32 v[92:93], v[80:81], v[218:219]
	v_mov_b32_e32 v143, v95
	v_pk_fma_f32 v[8:9], v[82:83], v[140:141], v[8:9] op_sel:[0,0,1] op_sel_hi:[1,1,0]
	v_pk_fma_f32 v[92:93], v[80:81], v[142:143], v[92:93] op_sel:[0,0,1] op_sel_hi:[1,1,0]
	s_waitcnt lgkmcnt(6)
	v_mov_b32_e32 v94, v178
	v_mov_b32_e32 v95, v145
	v_mov_b32_e32 v145, v179
	v_mov_b32_e32 v178, v180
	v_mov_b32_e32 v179, v147
	v_pk_add_f32 v[8:9], v[8:9], v[92:93]
	v_pk_mul_f32 v[92:93], v[90:91], v[94:95]
	v_pk_mul_f32 v[224:225], v[88:89], v[178:179]
	v_mov_b32_e32 v147, v181
	v_pk_fma_f32 v[92:93], v[90:91], v[144:145], v[92:93] op_sel:[0,0,1] op_sel_hi:[1,1,0]
	v_pk_fma_f32 v[180:181], v[88:89], v[146:147], v[224:225] op_sel:[0,0,1] op_sel_hi:[1,1,0]
	v_pk_add_f32 v[8:9], v[8:9], 0 op_sel_hi:[1,0]
	v_pk_add_f32 v[92:93], v[92:93], v[180:181]
	s_waitcnt lgkmcnt(5)
	v_mov_b32_e32 v180, v182
	v_mov_b32_e32 v181, v149
	v_mov_b32_e32 v149, v183
	v_mov_b32_e32 v182, v184
	v_mov_b32_e32 v183, v151
	v_pk_add_f32 v[8:9], v[8:9], v[92:93]
	v_pk_mul_f32 v[92:93], v[102:103], v[180:181]
	v_pk_mul_f32 v[224:225], v[100:101], v[182:183]
	v_mov_b32_e32 v151, v185
	v_pk_fma_f32 v[92:93], v[102:103], v[148:149], v[92:93] op_sel:[0,0,1] op_sel_hi:[1,1,0]
	v_pk_fma_f32 v[184:185], v[100:101], v[150:151], v[224:225] op_sel:[0,0,1] op_sel_hi:[1,1,0]
	v_pk_mul_f32 v[2:3], v[86:87], v[2:3]
	v_pk_add_f32 v[92:93], v[92:93], v[184:185]
	s_waitcnt lgkmcnt(4)
	v_mov_b32_e32 v184, v198
	v_mov_b32_e32 v185, v153
	v_mov_b32_e32 v153, v199
	v_mov_b32_e32 v198, v200
	v_mov_b32_e32 v199, v155
	v_pk_add_f32 v[8:9], v[8:9], v[92:93]
	v_pk_mul_f32 v[92:93], v[110:111], v[184:185]
	v_pk_mul_f32 v[224:225], v[108:109], v[198:199]
	v_mov_b32_e32 v155, v201
	v_pk_fma_f32 v[92:93], v[110:111], v[152:153], v[92:93] op_sel:[0,0,1] op_sel_hi:[1,1,0]
	v_pk_fma_f32 v[200:201], v[108:109], v[154:155], v[224:225] op_sel:[0,0,1] op_sel_hi:[1,1,0]
	v_pk_fma_f32 v[2:3], v[86:87], v[140:141], v[2:3] op_sel:[0,0,1] op_sel_hi:[1,1,0]
	v_pk_add_f32 v[92:93], v[92:93], v[200:201]
	s_waitcnt lgkmcnt(3)
	v_mov_b32_e32 v200, v202
	v_mov_b32_e32 v201, v157
	v_mov_b32_e32 v157, v203
	v_mov_b32_e32 v202, v204
	v_mov_b32_e32 v203, v159
	v_pk_add_f32 v[8:9], v[8:9], v[92:93]
	v_pk_mul_f32 v[92:93], v[118:119], v[200:201]
	v_pk_mul_f32 v[224:225], v[116:117], v[202:203]
	v_mov_b32_e32 v159, v205
	v_pk_fma_f32 v[92:93], v[118:119], v[156:157], v[92:93] op_sel:[0,0,1] op_sel_hi:[1,1,0]
	v_pk_fma_f32 v[204:205], v[116:117], v[158:159], v[224:225] op_sel:[0,0,1] op_sel_hi:[1,1,0]
	ds_bpermute_b32 v53, v41, v49
	v_pk_add_f32 v[92:93], v[92:93], v[204:205]
	s_waitcnt lgkmcnt(3)
	v_mov_b32_e32 v204, v206
	v_mov_b32_e32 v205, v161
	v_mov_b32_e32 v161, v207
	v_mov_b32_e32 v206, v208
	v_mov_b32_e32 v207, v163
	v_pk_add_f32 v[8:9], v[8:9], v[92:93]
	v_pk_mul_f32 v[92:93], v[126:127], v[204:205]
	v_pk_mul_f32 v[224:225], v[124:125], v[206:207]
	v_mov_b32_e32 v163, v209
	v_pk_fma_f32 v[92:93], v[126:127], v[160:161], v[92:93] op_sel:[0,0,1] op_sel_hi:[1,1,0]
	v_pk_fma_f32 v[208:209], v[124:125], v[162:163], v[224:225] op_sel:[0,0,1] op_sel_hi:[1,1,0]
	v_fmac_f32_e32 v45, v51, v29
	v_pk_add_f32 v[92:93], v[92:93], v[208:209]
	s_waitcnt lgkmcnt(2)
	v_mov_b32_e32 v208, v210
	v_mov_b32_e32 v209, v165
	v_mov_b32_e32 v165, v211
	v_mov_b32_e32 v210, v212
	v_mov_b32_e32 v211, v167
	v_pk_add_f32 v[8:9], v[8:9], v[92:93]
	v_pk_mul_f32 v[92:93], v[134:135], v[208:209]
	v_pk_mul_f32 v[224:225], v[132:133], v[210:211]
	v_mov_b32_e32 v167, v213
	v_pk_fma_f32 v[92:93], v[134:135], v[164:165], v[92:93] op_sel:[0,0,1] op_sel_hi:[1,1,0]
	v_pk_fma_f32 v[212:213], v[132:133], v[166:167], v[224:225] op_sel:[0,0,1] op_sel_hi:[1,1,0]
	v_pk_add_f32 v[92:93], v[92:93], v[212:213]
	s_waitcnt lgkmcnt(1)
	v_mov_b32_e32 v212, v214
	v_mov_b32_e32 v213, v175
	v_mov_b32_e32 v175, v215
	v_mov_b32_e32 v214, v216
	v_mov_b32_e32 v215, v177
	v_pk_add_f32 v[8:9], v[8:9], v[92:93]
	v_pk_mul_f32 v[92:93], v[6:7], v[212:213]
	v_pk_mul_f32 v[224:225], v[4:5], v[214:215]
	v_mov_b32_e32 v177, v217
	v_pk_fma_f32 v[92:93], v[6:7], v[174:175], v[92:93] op_sel:[0,0,1] op_sel_hi:[1,1,0]
	v_pk_fma_f32 v[216:217], v[4:5], v[176:177], v[224:225] op_sel:[0,0,1] op_sel_hi:[1,1,0]
	v_pk_add_f32 v[92:93], v[92:93], v[216:217]
	v_pk_add_f32 v[92:93], v[8:9], v[92:93]
	v_pk_mul_f32 v[8:9], v[84:85], v[218:219]
	v_pk_fma_f32 v[8:9], v[84:85], v[142:143], v[8:9] op_sel:[0,0,1] op_sel_hi:[1,1,0]
	v_pk_add_f32 v[2:3], v[2:3], v[8:9]
	v_pk_mul_f32 v[8:9], v[98:99], v[94:95]
	v_pk_mul_f32 v[94:95], v[96:97], v[178:179]
	v_pk_fma_f32 v[8:9], v[98:99], v[144:145], v[8:9] op_sel:[0,0,1] op_sel_hi:[1,1,0]
	v_pk_fma_f32 v[94:95], v[96:97], v[146:147], v[94:95] op_sel:[0,0,1] op_sel_hi:[1,1,0]
	v_pk_add_f32 v[2:3], v[2:3], 0 op_sel_hi:[1,0]
	v_pk_add_f32 v[8:9], v[8:9], v[94:95]
	v_pk_mul_f32 v[94:95], v[104:105], v[182:183]
	v_pk_add_f32 v[2:3], v[2:3], v[8:9]
	v_pk_mul_f32 v[8:9], v[106:107], v[180:181]
	v_pk_fma_f32 v[94:95], v[104:105], v[150:151], v[94:95] op_sel:[0,0,1] op_sel_hi:[1,1,0]
	v_pk_fma_f32 v[8:9], v[106:107], v[148:149], v[8:9] op_sel:[0,0,1] op_sel_hi:[1,1,0]
	v_pk_add_f32 v[8:9], v[8:9], v[94:95]
	v_pk_mul_f32 v[94:95], v[112:113], v[198:199]
	v_pk_add_f32 v[2:3], v[2:3], v[8:9]
	v_pk_mul_f32 v[8:9], v[114:115], v[184:185]
	v_pk_fma_f32 v[94:95], v[112:113], v[154:155], v[94:95] op_sel:[0,0,1] op_sel_hi:[1,1,0]
	v_pk_fma_f32 v[8:9], v[114:115], v[152:153], v[8:9] op_sel:[0,0,1] op_sel_hi:[1,1,0]
	v_pk_add_f32 v[8:9], v[8:9], v[94:95]
	v_pk_mul_f32 v[94:95], v[120:121], v[202:203]
	v_pk_add_f32 v[2:3], v[2:3], v[8:9]
	v_pk_mul_f32 v[8:9], v[122:123], v[200:201]
	v_pk_fma_f32 v[94:95], v[120:121], v[158:159], v[94:95] op_sel:[0,0,1] op_sel_hi:[1,1,0]
	v_pk_fma_f32 v[8:9], v[122:123], v[156:157], v[8:9] op_sel:[0,0,1] op_sel_hi:[1,1,0]
	v_pk_add_f32 v[8:9], v[8:9], v[94:95]
	v_pk_mul_f32 v[94:95], v[128:129], v[206:207]
	v_pk_add_f32 v[2:3], v[2:3], v[8:9]
	v_pk_mul_f32 v[8:9], v[130:131], v[204:205]
	v_pk_fma_f32 v[94:95], v[128:129], v[162:163], v[94:95] op_sel:[0,0,1] op_sel_hi:[1,1,0]
	v_pk_fma_f32 v[8:9], v[130:131], v[160:161], v[8:9] op_sel:[0,0,1] op_sel_hi:[1,1,0]
	v_pk_add_f32 v[8:9], v[8:9], v[94:95]
	v_pk_mul_f32 v[94:95], v[136:137], v[210:211]
	v_pk_add_f32 v[2:3], v[2:3], v[8:9]
	v_pk_mul_f32 v[8:9], v[138:139], v[208:209]
	v_pk_fma_f32 v[94:95], v[136:137], v[166:167], v[94:95] op_sel:[0,0,1] op_sel_hi:[1,1,0]
	v_pk_fma_f32 v[8:9], v[138:139], v[164:165], v[8:9] op_sel:[0,0,1] op_sel_hi:[1,1,0]
	v_pk_add_f32 v[8:9], v[8:9], v[94:95]
	v_pk_mul_f32 v[94:95], v[10:11], v[214:215]
	v_pk_add_f32 v[2:3], v[2:3], v[8:9]
	v_pk_mul_f32 v[8:9], v[12:13], v[212:213]
	v_pk_fma_f32 v[94:95], v[10:11], v[176:177], v[94:95] op_sel:[0,0,1] op_sel_hi:[1,1,0]
	v_pk_fma_f32 v[8:9], v[12:13], v[174:175], v[8:9] op_sel:[0,0,1] op_sel_hi:[1,1,0]
	ds_read_b128 v[140:143], v25 offset:32768
	ds_read_b128 v[144:147], v25 offset:33792
	ds_read_b128 v[148:151], v25 offset:34816
	ds_read_b128 v[152:155], v25 offset:35840
	ds_read_b128 v[156:159], v25 offset:36864
	ds_read_b128 v[160:163], v25 offset:37888
	ds_read_b128 v[164:167], v25 offset:38912
	ds_read_b128 v[174:177], v25 offset:39936
	ds_read_b128 v[178:181], v25 offset:40960
	ds_read_b128 v[182:185], v25 offset:41984
	ds_read_b128 v[198:201], v25 offset:43008
	ds_read_b128 v[202:205], v25 offset:44032
	ds_read_b128 v[206:209], v25 offset:45056
	ds_read_b128 v[210:213], v25 offset:46080
	ds_read_b128 v[214:217], v25 offset:47104
	ds_read_b128 v[224:227], v25 offset:48128
	v_pk_add_f32 v[8:9], v[8:9], v[94:95]
	v_pk_add_f32 v[2:3], v[2:3], v[8:9]
	s_waitcnt lgkmcnt(7)
	v_mov_b32_e32 v8, v178
	v_mov_b32_e32 v9, v141
	v_mov_b32_e32 v141, v179
	v_mov_b32_e32 v178, v180
	v_mov_b32_e32 v179, v143
	v_pk_mul_f32 v[94:95], v[82:83], v[8:9]
	v_pk_mul_f32 v[218:219], v[80:81], v[178:179]
	v_mov_b32_e32 v143, v181
	v_pk_fma_f32 v[94:95], v[82:83], v[140:141], v[94:95] op_sel:[0,0,1] op_sel_hi:[1,1,0]
	v_pk_fma_f32 v[180:181], v[80:81], v[142:143], v[218:219] op_sel:[0,0,1] op_sel_hi:[1,1,0]
	v_pk_mul_f32 v[8:9], v[86:87], v[8:9]
	v_pk_add_f32 v[94:95], v[94:95], v[180:181]
	s_waitcnt lgkmcnt(6)
	v_mov_b32_e32 v180, v182
	v_mov_b32_e32 v181, v145
	v_pk_mul_f32 v[218:219], v[90:91], v[180:181]
	v_mov_b32_e32 v145, v183
	v_pk_fma_f32 v[182:183], v[90:91], v[144:145], v[218:219] op_sel:[0,0,1] op_sel_hi:[1,1,0]
	v_mov_b32_e32 v218, v184
	v_mov_b32_e32 v219, v147
	v_pk_mul_f32 v[228:229], v[88:89], v[218:219]
	v_mov_b32_e32 v147, v185
	v_pk_fma_f32 v[184:185], v[88:89], v[146:147], v[228:229] op_sel:[0,0,1] op_sel_hi:[1,1,0]
	v_pk_add_f32 v[94:95], v[94:95], 0 op_sel_hi:[1,0]
	v_pk_add_f32 v[182:183], v[182:183], v[184:185]
	v_pk_fma_f32 v[8:9], v[86:87], v[140:141], v[8:9] op_sel:[0,0,1] op_sel_hi:[1,1,0]
	v_pk_add_f32 v[94:95], v[94:95], v[182:183]
	s_waitcnt lgkmcnt(5)
	v_mov_b32_e32 v182, v198
	v_mov_b32_e32 v183, v149
	v_mov_b32_e32 v149, v199
	v_mov_b32_e32 v198, v200
	v_mov_b32_e32 v199, v151
	v_pk_mul_f32 v[184:185], v[102:103], v[182:183]
	v_pk_mul_f32 v[228:229], v[100:101], v[198:199]
	v_mov_b32_e32 v151, v201
	v_pk_mul_f32 v[140:141], v[84:85], v[178:179]
	v_pk_fma_f32 v[184:185], v[102:103], v[148:149], v[184:185] op_sel:[0,0,1] op_sel_hi:[1,1,0]
	v_pk_fma_f32 v[200:201], v[100:101], v[150:151], v[228:229] op_sel:[0,0,1] op_sel_hi:[1,1,0]
	v_pk_fma_f32 v[140:141], v[84:85], v[142:143], v[140:141] op_sel:[0,0,1] op_sel_hi:[1,1,0]
	v_pk_add_f32 v[184:185], v[184:185], v[200:201]
	v_pk_add_f32 v[8:9], v[8:9], v[140:141]
	v_pk_mul_f32 v[140:141], v[98:99], v[180:181]
	v_pk_mul_f32 v[142:143], v[96:97], v[218:219]
	v_pk_add_f32 v[94:95], v[94:95], v[184:185]
	s_waitcnt lgkmcnt(4)
	v_mov_b32_e32 v184, v202
	v_mov_b32_e32 v185, v153
	v_mov_b32_e32 v153, v203
	v_mov_b32_e32 v202, v204
	v_mov_b32_e32 v203, v155
	v_pk_fma_f32 v[140:141], v[98:99], v[144:145], v[140:141] op_sel:[0,0,1] op_sel_hi:[1,1,0]
	v_pk_fma_f32 v[142:143], v[96:97], v[146:147], v[142:143] op_sel:[0,0,1] op_sel_hi:[1,1,0]
	v_pk_mul_f32 v[200:201], v[110:111], v[184:185]
	v_pk_mul_f32 v[228:229], v[108:109], v[202:203]
	v_mov_b32_e32 v155, v205
	v_pk_add_f32 v[8:9], v[8:9], 0 op_sel_hi:[1,0]
	v_pk_add_f32 v[140:141], v[140:141], v[142:143]
	v_pk_fma_f32 v[200:201], v[110:111], v[152:153], v[200:201] op_sel:[0,0,1] op_sel_hi:[1,1,0]
	v_pk_fma_f32 v[204:205], v[108:109], v[154:155], v[228:229] op_sel:[0,0,1] op_sel_hi:[1,1,0]
	v_pk_add_f32 v[8:9], v[8:9], v[140:141]
	v_pk_mul_f32 v[140:141], v[106:107], v[182:183]
	v_pk_mul_f32 v[142:143], v[104:105], v[198:199]
	v_pk_add_f32 v[200:201], v[200:201], v[204:205]
	v_pk_fma_f32 v[140:141], v[106:107], v[148:149], v[140:141] op_sel:[0,0,1] op_sel_hi:[1,1,0]
	v_pk_fma_f32 v[142:143], v[104:105], v[150:151], v[142:143] op_sel:[0,0,1] op_sel_hi:[1,1,0]
	v_pk_add_f32 v[94:95], v[94:95], v[200:201]
	s_waitcnt lgkmcnt(3)
	v_mov_b32_e32 v200, v206
	v_mov_b32_e32 v201, v157
	v_mov_b32_e32 v157, v207
	v_mov_b32_e32 v206, v208
	v_mov_b32_e32 v207, v159
	v_pk_add_f32 v[140:141], v[140:141], v[142:143]
	v_pk_mul_f32 v[204:205], v[118:119], v[200:201]
	v_pk_mul_f32 v[228:229], v[116:117], v[206:207]
	v_mov_b32_e32 v159, v209
	v_pk_add_f32 v[8:9], v[8:9], v[140:141]
	v_pk_mul_f32 v[140:141], v[114:115], v[184:185]
	v_pk_mul_f32 v[142:143], v[112:113], v[202:203]
	v_pk_fma_f32 v[204:205], v[118:119], v[156:157], v[204:205] op_sel:[0,0,1] op_sel_hi:[1,1,0]
	v_pk_fma_f32 v[208:209], v[116:117], v[158:159], v[228:229] op_sel:[0,0,1] op_sel_hi:[1,1,0]
	v_pk_fma_f32 v[140:141], v[114:115], v[152:153], v[140:141] op_sel:[0,0,1] op_sel_hi:[1,1,0]
	v_pk_fma_f32 v[142:143], v[112:113], v[154:155], v[142:143] op_sel:[0,0,1] op_sel_hi:[1,1,0]
	v_pk_add_f32 v[204:205], v[204:205], v[208:209]
	v_pk_add_f32 v[140:141], v[140:141], v[142:143]
	v_pk_add_f32 v[94:95], v[94:95], v[204:205]
	s_waitcnt lgkmcnt(2)
	v_mov_b32_e32 v204, v210
	v_mov_b32_e32 v205, v161
	v_mov_b32_e32 v161, v211
	v_mov_b32_e32 v210, v212
	v_mov_b32_e32 v211, v163
	v_pk_add_f32 v[8:9], v[8:9], v[140:141]
	v_pk_mul_f32 v[140:141], v[122:123], v[200:201]
	v_pk_mul_f32 v[142:143], v[120:121], v[206:207]
	v_pk_mul_f32 v[208:209], v[126:127], v[204:205]
	v_pk_mul_f32 v[228:229], v[124:125], v[210:211]
	v_mov_b32_e32 v163, v213
	v_pk_fma_f32 v[140:141], v[122:123], v[156:157], v[140:141] op_sel:[0,0,1] op_sel_hi:[1,1,0]
	v_pk_fma_f32 v[142:143], v[120:121], v[158:159], v[142:143] op_sel:[0,0,1] op_sel_hi:[1,1,0]
	v_pk_fma_f32 v[208:209], v[126:127], v[160:161], v[208:209] op_sel:[0,0,1] op_sel_hi:[1,1,0]
	v_pk_fma_f32 v[212:213], v[124:125], v[162:163], v[228:229] op_sel:[0,0,1] op_sel_hi:[1,1,0]
	v_pk_add_f32 v[140:141], v[140:141], v[142:143]
	v_pk_add_f32 v[208:209], v[208:209], v[212:213]
	v_pk_add_f32 v[8:9], v[8:9], v[140:141]
	v_pk_mul_f32 v[140:141], v[130:131], v[204:205]
	v_pk_mul_f32 v[142:143], v[128:129], v[210:211]
	v_pk_add_f32 v[94:95], v[94:95], v[208:209]
	s_waitcnt lgkmcnt(1)
	v_mov_b32_e32 v208, v214
	v_mov_b32_e32 v209, v165
	v_mov_b32_e32 v165, v215
	v_mov_b32_e32 v214, v216
	v_mov_b32_e32 v215, v167
	v_pk_fma_f32 v[140:141], v[130:131], v[160:161], v[140:141] op_sel:[0,0,1] op_sel_hi:[1,1,0]
	v_pk_fma_f32 v[142:143], v[128:129], v[162:163], v[142:143] op_sel:[0,0,1] op_sel_hi:[1,1,0]
	v_pk_mul_f32 v[212:213], v[134:135], v[208:209]
	v_pk_mul_f32 v[228:229], v[132:133], v[214:215]
	v_mov_b32_e32 v167, v217
	v_pk_add_f32 v[140:141], v[140:141], v[142:143]
	v_pk_fma_f32 v[212:213], v[134:135], v[164:165], v[212:213] op_sel:[0,0,1] op_sel_hi:[1,1,0]
	v_pk_fma_f32 v[216:217], v[132:133], v[166:167], v[228:229] op_sel:[0,0,1] op_sel_hi:[1,1,0]
	v_pk_add_f32 v[8:9], v[8:9], v[140:141]
	v_pk_mul_f32 v[140:141], v[138:139], v[208:209]
	v_pk_mul_f32 v[142:143], v[136:137], v[214:215]
	v_pk_add_f32 v[212:213], v[212:213], v[216:217]
	v_pk_fma_f32 v[140:141], v[138:139], v[164:165], v[140:141] op_sel:[0,0,1] op_sel_hi:[1,1,0]
	v_pk_fma_f32 v[142:143], v[136:137], v[166:167], v[142:143] op_sel:[0,0,1] op_sel_hi:[1,1,0]
	v_pk_add_f32 v[94:95], v[94:95], v[212:213]
	s_waitcnt lgkmcnt(0)
	v_mov_b32_e32 v212, v224
	v_mov_b32_e32 v213, v175
	v_mov_b32_e32 v175, v225
	v_mov_b32_e32 v224, v226
	v_mov_b32_e32 v225, v177
	v_pk_add_f32 v[140:141], v[140:141], v[142:143]
	v_pk_mul_f32 v[216:217], v[6:7], v[212:213]
	v_pk_mul_f32 v[228:229], v[4:5], v[224:225]
	v_mov_b32_e32 v177, v227
	v_pk_add_f32 v[8:9], v[8:9], v[140:141]
	v_pk_mul_f32 v[140:141], v[12:13], v[212:213]
	v_pk_mul_f32 v[142:143], v[10:11], v[224:225]
	v_pk_fma_f32 v[216:217], v[6:7], v[174:175], v[216:217] op_sel:[0,0,1] op_sel_hi:[1,1,0]
	v_pk_fma_f32 v[226:227], v[4:5], v[176:177], v[228:229] op_sel:[0,0,1] op_sel_hi:[1,1,0]
	v_pk_fma_f32 v[140:141], v[12:13], v[174:175], v[140:141] op_sel:[0,0,1] op_sel_hi:[1,1,0]
	v_pk_fma_f32 v[142:143], v[10:11], v[176:177], v[142:143] op_sel:[0,0,1] op_sel_hi:[1,1,0]
	v_pk_add_f32 v[216:217], v[216:217], v[226:227]
	v_pk_add_f32 v[140:141], v[140:141], v[142:143]
	v_pk_add_f32 v[94:95], v[94:95], v[216:217]
	v_pk_add_f32 v[8:9], v[8:9], v[140:141]
	ds_read_b128 v[140:143], v25 offset:49152
	ds_read_b128 v[144:147], v25 offset:50176
	ds_read_b128 v[148:151], v25 offset:51200
	ds_read_b128 v[152:155], v25 offset:52224
	ds_read_b128 v[156:159], v25 offset:53248
	ds_read_b128 v[160:163], v25 offset:54272
	ds_read_b128 v[164:167], v25 offset:55296
	ds_read_b128 v[174:177], v25 offset:56320
	ds_read_b128 v[178:181], v25 offset:57344
	ds_read_b128 v[182:185], v25 offset:58368
	ds_read_b128 v[198:201], v25 offset:59392
	ds_read_b128 v[202:205], v25 offset:60416
	ds_read_b128 v[206:209], v25 offset:61440
	ds_read_b128 v[210:213], v25 offset:62464
	ds_read_b128 v[214:217], v25 offset:63488
	ds_read_b128 v[224:227], v25 offset:64512
	s_waitcnt lgkmcnt(7)
	v_mov_b32_e32 v218, v178
	v_mov_b32_e32 v219, v141
	v_pk_mul_f32 v[228:229], v[82:83], v[218:219]
	v_mov_b32_e32 v141, v179
	v_mov_b32_e32 v178, v180
	v_mov_b32_e32 v179, v143
	v_pk_fma_f32 v[82:83], v[82:83], v[140:141], v[228:229] op_sel:[0,0,1] op_sel_hi:[1,1,0]
	v_pk_mul_f32 v[228:229], v[80:81], v[178:179]
	v_mov_b32_e32 v143, v181
	v_pk_fma_f32 v[80:81], v[80:81], v[142:143], v[228:229] op_sel:[0,0,1] op_sel_hi:[1,1,0]
	v_pk_add_f32 v[80:81], v[82:83], v[80:81]
	s_waitcnt lgkmcnt(6)
	v_mov_b32_e32 v82, v182
	v_mov_b32_e32 v83, v145
	v_pk_mul_f32 v[180:181], v[90:91], v[82:83]
	v_mov_b32_e32 v145, v183
	v_pk_fma_f32 v[90:91], v[90:91], v[144:145], v[180:181] op_sel:[0,0,1] op_sel_hi:[1,1,0]
	v_mov_b32_e32 v180, v184
	v_mov_b32_e32 v181, v147
	v_pk_mul_f32 v[182:183], v[88:89], v[180:181]
	v_mov_b32_e32 v147, v185
	v_pk_fma_f32 v[88:89], v[88:89], v[146:147], v[182:183] op_sel:[0,0,1] op_sel_hi:[1,1,0]
	v_pk_add_f32 v[80:81], v[80:81], 0 op_sel_hi:[1,0]
	v_pk_add_f32 v[88:89], v[90:91], v[88:89]
	v_pk_add_f32 v[80:81], v[80:81], v[88:89]
	s_waitcnt lgkmcnt(5)
	v_mov_b32_e32 v88, v198
	v_mov_b32_e32 v89, v149
	v_pk_mul_f32 v[90:91], v[102:103], v[88:89]
	v_mov_b32_e32 v149, v199
	v_pk_fma_f32 v[90:91], v[102:103], v[148:149], v[90:91] op_sel:[0,0,1] op_sel_hi:[1,1,0]
	v_mov_b32_e32 v102, v200
	v_mov_b32_e32 v103, v151
	v_pk_mul_f32 v[182:183], v[100:101], v[102:103]
	v_mov_b32_e32 v151, v201
	v_pk_fma_f32 v[100:101], v[100:101], v[150:151], v[182:183] op_sel:[0,0,1] op_sel_hi:[1,1,0]
	v_pk_add_f32 v[90:91], v[90:91], v[100:101]
	v_pk_add_f32 v[80:81], v[80:81], v[90:91]
	s_waitcnt lgkmcnt(4)
	v_mov_b32_e32 v90, v202
	v_mov_b32_e32 v91, v153
	v_pk_mul_f32 v[100:101], v[110:111], v[90:91]
	v_mov_b32_e32 v153, v203
	v_pk_fma_f32 v[100:101], v[110:111], v[152:153], v[100:101] op_sel:[0,0,1] op_sel_hi:[1,1,0]
	v_mov_b32_e32 v110, v204
	v_mov_b32_e32 v111, v155
	v_pk_mul_f32 v[182:183], v[108:109], v[110:111]
	v_mov_b32_e32 v155, v205
	v_pk_fma_f32 v[108:109], v[108:109], v[154:155], v[182:183] op_sel:[0,0,1] op_sel_hi:[1,1,0]
	v_pk_add_f32 v[100:101], v[100:101], v[108:109]
	v_pk_add_f32 v[80:81], v[80:81], v[100:101]
	s_waitcnt lgkmcnt(3)
	v_mov_b32_e32 v100, v206
	v_mov_b32_e32 v101, v157
	v_pk_mul_f32 v[108:109], v[118:119], v[100:101]
	v_mov_b32_e32 v157, v207
	v_pk_fma_f32 v[108:109], v[118:119], v[156:157], v[108:109] op_sel:[0,0,1] op_sel_hi:[1,1,0]
	v_mov_b32_e32 v118, v208
	v_mov_b32_e32 v119, v159
	v_pk_mul_f32 v[182:183], v[116:117], v[118:119]
	v_mov_b32_e32 v159, v209
	v_pk_fma_f32 v[116:117], v[116:117], v[158:159], v[182:183] op_sel:[0,0,1] op_sel_hi:[1,1,0]
	v_pk_add_f32 v[108:109], v[108:109], v[116:117]
	v_pk_add_f32 v[80:81], v[80:81], v[108:109]
	s_waitcnt lgkmcnt(2)
	v_mov_b32_e32 v108, v210
	v_mov_b32_e32 v109, v161
	v_pk_mul_f32 v[116:117], v[126:127], v[108:109]
	v_mov_b32_e32 v161, v211
	v_pk_fma_f32 v[116:117], v[126:127], v[160:161], v[116:117] op_sel:[0,0,1] op_sel_hi:[1,1,0]
	v_mov_b32_e32 v126, v212
	v_mov_b32_e32 v127, v163
	v_pk_mul_f32 v[182:183], v[124:125], v[126:127]
	v_mov_b32_e32 v163, v213
	v_pk_fma_f32 v[124:125], v[124:125], v[162:163], v[182:183] op_sel:[0,0,1] op_sel_hi:[1,1,0]
	v_pk_add_f32 v[116:117], v[116:117], v[124:125]
	v_pk_add_f32 v[80:81], v[80:81], v[116:117]
	s_waitcnt lgkmcnt(1)
	v_mov_b32_e32 v116, v214
	v_mov_b32_e32 v117, v165
	v_pk_mul_f32 v[124:125], v[134:135], v[116:117]
	v_mov_b32_e32 v165, v215
	v_pk_fma_f32 v[124:125], v[134:135], v[164:165], v[124:125] op_sel:[0,0,1] op_sel_hi:[1,1,0]
	v_mov_b32_e32 v134, v216
	v_mov_b32_e32 v135, v167
	v_pk_mul_f32 v[182:183], v[132:133], v[134:135]
	v_mov_b32_e32 v167, v217
	v_pk_fma_f32 v[132:133], v[132:133], v[166:167], v[182:183] op_sel:[0,0,1] op_sel_hi:[1,1,0]
	v_pk_add_f32 v[124:125], v[124:125], v[132:133]
	v_pk_add_f32 v[80:81], v[80:81], v[124:125]
	s_waitcnt lgkmcnt(0)
	v_mov_b32_e32 v124, v224
	v_mov_b32_e32 v125, v175
	v_pk_mul_f32 v[132:133], v[6:7], v[124:125]
	v_mov_b32_e32 v175, v225
	v_pk_fma_f32 v[6:7], v[6:7], v[174:175], v[132:133] op_sel:[0,0,1] op_sel_hi:[1,1,0]
	v_mov_b32_e32 v132, v226
	v_mov_b32_e32 v133, v177
	v_pk_mul_f32 v[182:183], v[4:5], v[132:133]
	v_mov_b32_e32 v177, v227
	v_pk_fma_f32 v[4:5], v[4:5], v[176:177], v[182:183] op_sel:[0,0,1] op_sel_hi:[1,1,0]
	v_pk_add_f32 v[4:5], v[6:7], v[4:5]
	v_pk_add_f32 v[6:7], v[80:81], v[4:5]
	v_pk_mul_f32 v[4:5], v[86:87], v[218:219]
	v_pk_mul_f32 v[80:81], v[84:85], v[178:179]
	v_pk_fma_f32 v[4:5], v[86:87], v[140:141], v[4:5] op_sel:[0,0,1] op_sel_hi:[1,1,0]
	v_pk_fma_f32 v[80:81], v[84:85], v[142:143], v[80:81] op_sel:[0,0,1] op_sel_hi:[1,1,0]
	v_pk_add_f32 v[4:5], v[4:5], v[80:81]
	v_pk_mul_f32 v[80:81], v[98:99], v[82:83]
	v_pk_mul_f32 v[82:83], v[96:97], v[180:181]
	v_pk_fma_f32 v[80:81], v[98:99], v[144:145], v[80:81] op_sel:[0,0,1] op_sel_hi:[1,1,0]
	v_pk_fma_f32 v[82:83], v[96:97], v[146:147], v[82:83] op_sel:[0,0,1] op_sel_hi:[1,1,0]
	v_pk_add_f32 v[4:5], v[4:5], 0 op_sel_hi:[1,0]
	v_pk_add_f32 v[80:81], v[80:81], v[82:83]
	v_pk_mul_f32 v[82:83], v[104:105], v[102:103]
	v_pk_add_f32 v[4:5], v[4:5], v[80:81]
	v_pk_mul_f32 v[80:81], v[106:107], v[88:89]
	v_pk_fma_f32 v[82:83], v[104:105], v[150:151], v[82:83] op_sel:[0,0,1] op_sel_hi:[1,1,0]
	v_pk_fma_f32 v[80:81], v[106:107], v[148:149], v[80:81] op_sel:[0,0,1] op_sel_hi:[1,1,0]
	v_pk_add_f32 v[80:81], v[80:81], v[82:83]
	v_pk_mul_f32 v[82:83], v[112:113], v[110:111]
	v_pk_add_f32 v[4:5], v[4:5], v[80:81]
	v_pk_mul_f32 v[80:81], v[114:115], v[90:91]
	v_pk_fma_f32 v[82:83], v[112:113], v[154:155], v[82:83] op_sel:[0,0,1] op_sel_hi:[1,1,0]
	v_pk_fma_f32 v[80:81], v[114:115], v[152:153], v[80:81] op_sel:[0,0,1] op_sel_hi:[1,1,0]
	v_pk_add_f32 v[80:81], v[80:81], v[82:83]
	v_pk_mul_f32 v[82:83], v[120:121], v[118:119]
	v_pk_add_f32 v[4:5], v[4:5], v[80:81]
	v_pk_mul_f32 v[80:81], v[122:123], v[100:101]
	v_pk_fma_f32 v[82:83], v[120:121], v[158:159], v[82:83] op_sel:[0,0,1] op_sel_hi:[1,1,0]
	v_pk_fma_f32 v[80:81], v[122:123], v[156:157], v[80:81] op_sel:[0,0,1] op_sel_hi:[1,1,0]
	v_pk_add_f32 v[80:81], v[80:81], v[82:83]
	v_pk_mul_f32 v[82:83], v[128:129], v[126:127]
	v_pk_add_f32 v[4:5], v[4:5], v[80:81]
	v_pk_mul_f32 v[80:81], v[130:131], v[108:109]
	v_pk_fma_f32 v[82:83], v[128:129], v[162:163], v[82:83] op_sel:[0,0,1] op_sel_hi:[1,1,0]
	v_pk_fma_f32 v[80:81], v[130:131], v[160:161], v[80:81] op_sel:[0,0,1] op_sel_hi:[1,1,0]
	v_pk_add_f32 v[80:81], v[80:81], v[82:83]
	v_pk_mul_f32 v[82:83], v[136:137], v[134:135]
	v_pk_add_f32 v[4:5], v[4:5], v[80:81]
	v_pk_mul_f32 v[80:81], v[138:139], v[116:117]
	v_pk_fma_f32 v[82:83], v[136:137], v[166:167], v[82:83] op_sel:[0,0,1] op_sel_hi:[1,1,0]
	v_pk_fma_f32 v[80:81], v[138:139], v[164:165], v[80:81] op_sel:[0,0,1] op_sel_hi:[1,1,0]
	v_pk_add_f32 v[80:81], v[80:81], v[82:83]
	v_pk_add_f32 v[4:5], v[4:5], v[80:81]
	v_pk_mul_f32 v[80:81], v[12:13], v[124:125]
	v_pk_fma_f32 v[12:13], v[12:13], v[174:175], v[80:81] op_sel:[0,0,1] op_sel_hi:[1,1,0]
	v_pk_mul_f32 v[80:81], v[10:11], v[132:133]
	v_pk_fma_f32 v[10:11], v[10:11], v[176:177], v[80:81] op_sel:[0,0,1] op_sel_hi:[1,1,0]
	v_pk_add_f32 v[10:11], v[12:13], v[10:11]
	v_pk_add_f32 v[4:5], v[4:5], v[10:11]
	v_cmp_eq_u32_e64 s[46:47], 8, v20
	s_nop 1
	v_cndmask_b32_e64 v10, v14, v0, s[46:47]
	ds_bpermute_b32 v10, v39, v10
	v_cmp_eq_u32_e64 s[46:47], 8, v22
	s_nop 1
	v_cndmask_b32_e64 v11, v14, v0, s[46:47]
	s_waitcnt lgkmcnt(0)
	v_add_f32_e32 v12, v11, v10
	v_cmp_eq_u32_e64 s[46:47], 9, v24
	s_nop 1
	v_cndmask_b32_e64 v10, v15, v1, s[46:47]
	ds_bpermute_b32 v10, v39, v10
	v_cmp_eq_u32_e64 s[46:47], 9, v26
	s_nop 1
	v_cndmask_b32_e64 v11, v15, v1, s[46:47]
	s_waitcnt lgkmcnt(0)
	v_add_f32_e32 v13, v11, v10
	v_cmp_eq_u32_e64 s[46:47], 10, v28
	s_nop 1
	v_cndmask_b32_e64 v10, v92, v2, s[46:47]
	ds_bpermute_b32 v10, v39, v10
	v_cmp_eq_u32_e64 s[46:47], 10, v30
	s_nop 1
	v_cndmask_b32_e64 v11, v92, v2, s[46:47]
	s_waitcnt lgkmcnt(0)
	v_add_f32_e32 v14, v11, v10
	v_cmp_eq_u32_e64 s[46:47], 11, v32
	s_nop 1
	v_cndmask_b32_e64 v10, v93, v3, s[46:47]
	ds_bpermute_b32 v10, v39, v10
	v_cmp_eq_u32_e64 s[46:47], 11, v34
	s_nop 1
	v_cndmask_b32_e64 v11, v93, v3, s[46:47]
	s_waitcnt lgkmcnt(0)
	v_add_f32_e32 v15, v11, v10
	v_cmp_eq_u32_e64 s[46:47], 12, v36
	s_nop 1
	v_cndmask_b32_e64 v10, v94, v8, s[46:47]
	ds_bpermute_b32 v10, v39, v10
	v_cmp_eq_u32_e64 s[46:47], 12, v38
	s_nop 1
	v_cndmask_b32_e64 v11, v94, v8, s[46:47]
	s_waitcnt lgkmcnt(0)
	v_add_f32_e32 v10, v11, v10
	v_cmp_eq_u32_e64 s[46:47], 13, v40
	s_nop 1
	v_cndmask_b32_e64 v11, v95, v9, s[46:47]
	ds_bpermute_b32 v11, v39, v11
	v_cmp_eq_u32_e64 s[46:47], 13, v42
	s_nop 1
	v_cndmask_b32_e64 v55, v95, v9, s[46:47]
	s_waitcnt lgkmcnt(0)
	v_add_f32_e32 v11, v55, v11
	v_cmp_eq_u32_e64 s[46:47], 14, v44
	s_nop 1
	v_cndmask_b32_e64 v55, v6, v4, s[46:47]
	ds_bpermute_b32 v55, v39, v55
	v_cmp_eq_u32_e64 s[46:47], 14, v46
	s_nop 1
	v_cndmask_b32_e64 v6, v6, v4, s[46:47]
	s_waitcnt lgkmcnt(0)
	v_add_f32_e32 v6, v6, v55
	v_cmp_eq_u32_e64 s[46:47], 15, v48
	s_nop 1
	v_cndmask_b32_e64 v55, v7, v5, s[46:47]
	ds_bpermute_b32 v55, v39, v55
	v_cmp_eq_u32_e64 s[46:47], 15, v50
	s_nop 1
	v_cndmask_b32_e64 v7, v7, v5, s[46:47]
	s_waitcnt lgkmcnt(0)
	v_add_f32_e32 v7, v7, v55
	v_cmp_eq_u32_e64 s[46:47], 4, v52
	s_nop 1
	v_cndmask_b32_e64 v55, v12, v10, s[46:47]
	ds_bpermute_b32 v55, v37, v55
	v_cmp_eq_u32_e64 s[46:47], 4, v54
	s_nop 1
	v_cndmask_b32_e64 v12, v12, v10, s[46:47]
	s_waitcnt lgkmcnt(0)
	v_add_f32_e32 v12, v12, v55
	v_cmp_eq_u32_e64 s[46:47], 5, v56
	s_nop 1
	v_cndmask_b32_e64 v55, v13, v11, s[46:47]
	ds_bpermute_b32 v55, v37, v55
	v_cmp_eq_u32_e64 s[46:47], 5, v58
	s_nop 1
	v_cndmask_b32_e64 v13, v13, v11, s[46:47]
	s_waitcnt lgkmcnt(0)
	v_add_f32_e32 v13, v13, v55
	v_cmp_eq_u32_e64 s[46:47], 6, v60
	s_nop 1
	v_cndmask_b32_e64 v55, v14, v6, s[46:47]
	ds_bpermute_b32 v55, v37, v55
	v_cmp_eq_u32_e64 s[46:47], 6, v62
	s_nop 1
	v_cndmask_b32_e64 v14, v14, v6, s[46:47]
	s_waitcnt lgkmcnt(0)
	v_add_f32_e32 v14, v14, v55
	v_cmp_eq_u32_e64 s[46:47], 7, v64
	s_nop 1
	v_cndmask_b32_e64 v55, v15, v7, s[46:47]
	ds_bpermute_b32 v55, v37, v55
	v_cmp_eq_u32_e64 s[46:47], 7, v66
	s_nop 1
	v_cndmask_b32_e64 v15, v15, v7, s[46:47]
	s_waitcnt lgkmcnt(0)
	v_add_f32_e32 v15, v15, v55
	v_cmp_eq_u32_e64 s[46:47], 2, v68
	s_nop 1
	v_cndmask_b32_e64 v55, v12, v14, s[46:47]
	ds_bpermute_b32 v55, v41, v55
	v_cmp_eq_u32_e64 s[46:47], 2, v70
	s_nop 1
	v_cndmask_b32_e64 v12, v12, v14, s[46:47]
	s_waitcnt lgkmcnt(0)
	v_add_f32_e32 v12, v12, v55
	v_cmp_eq_u32_e64 s[46:47], 3, v72
	s_nop 1
	v_cndmask_b32_e64 v55, v13, v15, s[46:47]
	ds_bpermute_b32 v55, v41, v55
	v_cmp_eq_u32_e64 s[46:47], 3, v74
	s_nop 1
	v_cndmask_b32_e64 v13, v13, v15, s[46:47]
	s_waitcnt lgkmcnt(0)
	v_add_f32_e32 v13, v13, v55
	v_cmp_ne_u64_e64 s[46:47], 0, v[76:77]
	s_nop 1
	v_cndmask_b32_e64 v55, v12, v13, s[46:47]
	v_cmp_ne_u64_e64 s[46:47], 0, v[78:79]
	s_nop 1
	v_cndmask_b32_e64 v12, v12, v13, s[46:47]
	v_mov_b32_e32 v10, v12
	v_mov_b32_e32 v6, v10
	v_mov_b32_e32 v0, v6
	v_fma_f32 v2, -v43, v45, v47
	v_add_f32_e32 v3, v49, v53
	ds_bpermute_b32 v0, v35, v0
	v_mov_b32_e32 v1, v55
	ds_bpermute_b32 v4, v37, v3
	s_waitcnt lgkmcnt(1)
	v_add_f32_e32 v0, v1, v0
	ds_bpermute_b32 v1, v33, v0
	s_waitcnt lgkmcnt(0)
	v_add_f32_e32 v5, v0, v1
	ds_bpermute_b32 v6, v31, v5
	v_div_fmas_f32 v0, v2, v29, v45
	v_div_fixup_f32 v8, v0, v27, 1.0
	v_add_f32_e32 v0, v3, v4
	ds_bpermute_b32 v1, v39, v0
	s_waitcnt lgkmcnt(1)
	v_add_f32_e32 v2, v5, v6
	s_nop 0
	v_readlane_b32 s1, v2, 0
	v_readlane_b32 s0, v2, 4
	v_readlane_b32 s8, v2, 32
	v_readlane_b32 s9, v2, 36
	v_pk_mul_f32 v[6:7], v[8:9], s[0:1] op_sel_hi:[0,1]
	v_readlane_b32 s0, v2, 8
	v_cmp_gt_f32_e32 vcc, v6, v7
	v_readlane_b32 s10, v2, 40
	v_mul_f32_e32 v3, s0, v8
	v_readlane_b32 s0, v2, 12
	v_readlane_b32 s11, v2, 44
	v_readlane_b32 s12, v2, 48
	v_mul_f32_e32 v4, s0, v8
	v_readlane_b32 s0, v2, 16
	v_readlane_b32 s13, v2, 52
	v_readlane_b32 s14, v2, 56
	v_mul_f32_e32 v9, s0, v8
	v_readlane_b32 s0, v2, 20
	v_readlane_b32 s15, v2, 60
	v_cndmask_b32_e64 v12, 0, 1, vcc
	v_mul_f32_e32 v10, s0, v8
	v_readlane_b32 s0, v2, 24
	v_cmp_lt_f32_e64 s[52:53], s33, v7
	s_nop 0
	v_mul_f32_e32 v11, s0, v8
	v_readlane_b32 s0, v2, 28
	v_cndmask_b32_e32 v2, v7, v6, vcc
	v_cmp_gt_f32_e32 vcc, v3, v2
	v_mul_f32_e32 v5, s0, v8
	s_nop 0
	v_cndmask_b32_e32 v2, v2, v3, vcc
	v_cndmask_b32_e64 v12, v12, 2, vcc
	v_cmp_gt_f32_e32 vcc, v4, v2
	s_nop 1
	v_cndmask_b32_e32 v2, v2, v4, vcc
	v_cndmask_b32_e64 v12, v12, 3, vcc
	v_cmp_gt_f32_e32 vcc, v9, v2
	s_nop 1
	v_cndmask_b32_e32 v2, v2, v9, vcc
	v_cndmask_b32_e64 v12, v12, 4, vcc
	v_cmp_gt_f32_e32 vcc, v10, v2
	s_nop 1
	v_cndmask_b32_e32 v2, v2, v10, vcc
	v_cndmask_b32_e64 v12, v12, 5, vcc
	v_cmp_ngt_f32_e32 vcc, v11, v2
	s_nop 1
	v_cndmask_b32_e32 v2, v11, v2, vcc
	v_cndmask_b32_e32 v12, 6, v12, vcc
	v_cmp_gt_f32_e64 s[48:49], v5, v2
	s_or_b64 s[0:1], vcc, s[48:49]
	v_cmp_ngt_f32_e64 s[46:47], v5, v2
	v_cndmask_b32_e64 v172, v12, 7, s[48:49]
	v_cmp_ne_u32_e64 s[50:51], 0, v172
	s_and_b64 s[50:51], s[50:51], s[52:53]
	s_nop 0
	v_cndmask_b32_e64 v7, v196, v7, s[50:51]
	v_cmp_ne_u32_e64 s[50:51], 1, v172
	v_cmp_gt_f32_e64 s[52:53], v6, v7
	s_and_b64 s[50:51], s[50:51], s[52:53]
	v_cndmask_b32_e64 v6, v7, v6, s[50:51]
	v_cndmask_b32_e64 v7, 0, 1, s[50:51]
	v_cmp_ne_u32_e64 s[50:51], 2, v172
	v_cmp_gt_f32_e64 s[52:53], v3, v6
	s_and_b64 s[50:51], s[50:51], s[52:53]
	v_cndmask_b32_e64 v3, v6, v3, s[50:51]
	v_cndmask_b32_e64 v6, v7, 2, s[50:51]
	v_cmp_ne_u32_e64 s[50:51], 3, v172
	v_cmp_gt_f32_e64 s[52:53], v4, v3
	s_and_b64 s[50:51], s[50:51], s[52:53]
	v_cndmask_b32_e64 v3, v3, v4, s[50:51]
	v_cndmask_b32_e64 v4, v6, 3, s[50:51]
	v_cmp_ne_u32_e64 s[50:51], 4, v172
	v_cmp_gt_f32_e64 s[52:53], v9, v3
	s_and_b64 s[50:51], s[50:51], s[52:53]
	v_cndmask_b32_e64 v3, v3, v9, s[50:51]
	v_cndmask_b32_e64 v4, v4, 4, s[50:51]
	v_cmp_ne_u32_e64 s[50:51], 5, v172
	v_cmp_gt_f32_e64 s[52:53], v10, v3
	s_and_b64 s[50:51], s[50:51], s[52:53]
	v_cndmask_b32_e64 v3, v3, v10, s[50:51]
	v_cmp_gt_f32_e32 vcc, v11, v3
	v_cndmask_b32_e64 v4, v4, 5, s[50:51]
	s_and_b64 vcc, s[0:1], vcc
	v_cndmask_b32_e32 v43, v3, v11, vcc
	v_cndmask_b32_e64 v9, v4, 6, vcc
	s_and_saveexec_b64 s[0:1], s[46:47]
	s_cbranch_execz .LBB0_1340
	v_cmp_gt_f32_e32 vcc, v5, v43
	s_and_saveexec_b64 s[2:3], vcc
	v_mov_b32_e32 v9, 7
	v_mov_b32_e32 v43, v5
	s_or_b64 exec, exec, s[2:3]
	v_mov_b32_e32 v5, v2

.LBB0_1348:
	s_or_b64 exec, exec, s[0:1]
	s_waitcnt lgkmcnt(1)
	v_readfirstlane_b32 s19, v0
	s_waitcnt lgkmcnt(0)
	v_readfirstlane_b32 s54, v1
	s_or_b32 s26, s18, 2
	s_max_i32 s12, s26, 4
	s_add_i32 s12, s12, -4
	s_mov_b32 s13, s60
	s_lshl_b64 s[96:97], s[12:13], 12
	s_max_i32 s12, s26, 3
	s_add_i32 s12, s12, -3
	s_lshl_b64 s[52:53], s[12:13], 12
	s_max_i32 s12, s26, 2
	s_add_i32 s12, s12, -2
	s_lshl_b64 s[50:51], s[12:13], 12
	s_max_i32 s12, s26, 1
	s_add_i32 s12, s12, -1
	s_lshl_b64 s[48:49], s[12:13], 12
	s_max_i32 s12, s26, 0
	s_lshl_b64 s[46:47], s[12:13], 12
	s_max_i32 s12, s26, -1
	s_and_b32 s14, s26, 0x7fe
	s_add_i32 s12, s12, 1
	s_lshl_b64 s[92:93], s[12:13], 12
	s_min_u32 s12, s14, 15
	s_add_i32 s12, s12, 1
	s_min_u32 s13, s14, 14
	v_cvt_f32_ubyte0_e32 v0, s12
	s_add_i32 s15, s13, 2
	v_div_scale_f32 v1, s[12:13], v0, v0, 1.0
	v_rcp_f32_e32 v2, v1
	s_max_i32 s0, s26, 15
	s_add_i32 s0, s0, -15
	s_mov_b32 s1, s60
	v_fma_f32 v3, -v1, v2, 1.0
	v_fmac_f32_e32 v2, v3, v2
	v_div_scale_f32 v3, vcc, 1.0, v0, 1.0
	v_mul_f32_e32 v10, v3, v2
	v_fma_f32 v11, -v1, v10, v3
	v_fmac_f32_e32 v10, v11, v2
	v_fma_f32 v1, -v1, v10, v3
	v_div_fmas_f32 v1, v1, v2, v10
	v_div_fixup_f32 v90, v1, v0, 1.0
	v_cvt_f32_ubyte0_e32 v0, s15
	v_div_scale_f32 v1, s[12:13], v0, v0, 1.0
	v_rcp_f32_e32 v2, v1
	s_min_u32 s12, s14, 7
	s_add_i32 s12, s12, 1
	s_min_u32 s13, s14, 6
	v_fma_f32 v3, -v1, v2, 1.0
	v_fmac_f32_e32 v2, v3, v2
	v_div_scale_f32 v3, vcc, 1.0, v0, 1.0
	v_mul_f32_e32 v10, v3, v2
	v_fma_f32 v11, -v1, v10, v3
	v_fmac_f32_e32 v10, v11, v2
	v_fma_f32 v1, -v1, v10, v3
	v_div_fmas_f32 v1, v1, v2, v10
	v_div_fixup_f32 v92, v1, v0, 1.0
	v_cvt_f32_ubyte0_e32 v0, s12
	s_add_i32 s15, s13, 2
	v_div_scale_f32 v1, s[12:13], v0, v0, 1.0
	v_rcp_f32_e32 v2, v1
	s_lshl_b64 s[42:43], s[0:1], 12
	s_max_i32 s0, s26, 14
	s_add_i32 s0, s0, -14
	v_fma_f32 v3, -v1, v2, 1.0
	v_fmac_f32_e32 v2, v3, v2
	v_div_scale_f32 v3, vcc, 1.0, v0, 1.0
	v_mul_f32_e32 v10, v3, v2
	v_fma_f32 v11, -v1, v10, v3
	v_fmac_f32_e32 v10, v11, v2
	v_fma_f32 v1, -v1, v10, v3
	v_div_fmas_f32 v1, v1, v2, v10
	v_div_fixup_f32 v118, v1, v0, 1.0
	v_cvt_f32_ubyte0_e32 v0, s15
	v_div_scale_f32 v1, s[12:13], v0, v0, 1.0
	v_rcp_f32_e32 v2, v1
	s_lshl_b64 s[88:89], s[0:1], 12
	s_max_i32 s0, s26, 13
	s_add_i32 s0, s0, -13
	s_lshl_b64 s[36:37], s[0:1], 12
	s_max_i32 s0, s26, 12
	v_fma_f32 v3, -v1, v2, 1.0
	s_add_i32 s0, s0, -12
	v_fmac_f32_e32 v2, v3, v2
	v_div_scale_f32 v3, vcc, 1.0, v0, 1.0
	s_lshl_b64 s[78:79], s[0:1], 12
	s_max_i32 s0, s26, 11
	v_mul_f32_e32 v10, v3, v2
	s_add_i32 s0, s0, -11
	v_fma_f32 v11, -v1, v10, v3
	s_lshl_b64 s[76:77], s[0:1], 12
	s_max_i32 s0, s26, 10
	v_fmac_f32_e32 v10, v11, v2
	s_add_i32 s0, s0, -10
	v_fma_f32 v1, -v1, v10, v3
	s_min_u32 s12, s14, 3
	s_lshl_b64 s[10:11], s[0:1], 12
	s_max_i32 s0, s26, 9
	v_div_fmas_f32 v1, v1, v2, v10
	s_add_i32 s12, s12, 1
	s_add_i32 s0, s0, -9
	v_div_fixup_f32 v120, v1, v0, 1.0
	v_cvt_f32_ubyte0_e32 v0, s12
	s_lshl_b64 s[8:9], s[0:1], 12
	s_max_i32 s0, s26, 8
	v_div_scale_f32 v1, s[12:13], v0, v0, 1.0
	s_add_i32 s0, s0, -8
	v_rcp_f32_e32 v2, v1
	s_lshl_b64 s[44:45], s[0:1], 12
	s_max_i32 s0, s26, 7
	s_add_i32 s0, s0, -7
	s_lshl_b64 s[86:87], s[0:1], 12
	s_max_i32 s0, s26, 6
	s_max_i32 s2, s26, 5
	s_add_i32 s0, s0, -6
	s_add_i32 s2, s2, -5
	s_mov_b32 s3, s60
	v_fma_f32 v3, -v1, v2, 1.0
	s_ashr_i32 s27, s26, 31
	s_lshl_b64 s[0:1], s[0:1], 12
	s_lshl_b64 s[2:3], s[2:3], 12
	v_fmac_f32_e32 v2, v3, v2
	v_div_scale_f32 v3, vcc, 1.0, v0, 1.0
	s_lshl_b64 s[12:13], s[26:27], 12
	v_mul_f32_e32 v10, v3, v2
	s_add_u32 s30, s4, s12
	v_fma_f32 v11, -v1, v10, v3
	s_addc_u32 s31, s5, s13
	s_or_b32 s24, s18, 3
	v_fmac_f32_e32 v10, v11, v2
	s_ashr_i32 s25, s24, 31
	v_fma_f32 v1, -v1, v10, v3
	s_lshl_b64 s[12:13], s[24:25], 12
	v_mov_b32_e32 v55, v21
	v_div_fmas_f32 v1, v1, v2, v10
	s_add_u32 s28, s4, s12
	s_addc_u32 s29, s5, s13
	v_lshlrev_b32_e32 v10, 2, v55
	v_ashrrev_i32_e32 v11, 31, v10
	v_readlane_b32 s12, v253, 40
	v_lshlrev_b64 v[82:83], 1, v[10:11]
	v_readlane_b32 s13, v253, 41
	v_mov_b32_e32 v53, s7
	v_div_fixup_f32 v102, v1, v0, 1.0
	v_lshl_add_u64 v[10:11], s[12:13], 0, v[82:83]
	v_lshl_add_u64 v[236:237], v[10:11], 0, s[92:93]
	global_load_dwordx2 v[236:237], v[236:237], off
	v_lshl_add_u64 v[238:239], v[10:11], 0, s[48:49]
	global_load_dwordx2 v[238:239], v[238:239], off
	v_lshl_add_u64 v[240:241], v[10:11], 0, s[46:47]
	global_load_dwordx2 v[240:241], v[240:241], off
	v_lshl_add_u64 v[242:243], s[30:31], 0, v[82:83]
	global_load_dwordx2 v[242:243], v[242:243], off
	s_nop 0
	s_nop 0
	s_nop 0
	s_nop 0
	s_nop 0
	ds_read_b96 v[0:2], v53 offset:64
	s_nop 0
	s_add_u32 vcc_lo, s12, s92
	s_addc_u32 vcc_hi, s13, s93
	s_mov_b64 s[92:93], s[12:13]
	s_add_u32 s48, s92, s48
	s_addc_u32 s49, s93, s49
	s_add_u32 s46, s92, s46
	s_addc_u32 s47, s93, s47
	s_add_u32 s52, s92, s52
	s_addc_u32 s53, s93, s53
	s_add_u32 s50, s92, s50
	s_addc_u32 s51, s93, s51
	s_mov_b32 s12, 0x3e800000
	s_nop 0
	s_waitcnt vmcnt(3)
	v_lshlrev_b32_e32 v14, 16, v236
	v_and_b32_e32 v15, 0xffff0000, v236
	s_nop 0
	s_waitcnt vmcnt(2)
	v_lshlrev_b32_e32 v88, 16, v238
	v_and_b32_e32 v89, 0xffff0000, v238
	v_lshlrev_b32_e32 v86, 16, v239
	v_and_b32_e32 v87, 0xffff0000, v239
	s_waitcnt lgkmcnt(0)
	v_pk_fma_f32 v[94:95], v[0:1], v[88:89], 0 op_sel_hi:[0,1,0]
	v_pk_fma_f32 v[96:97], v[0:1], v[86:87], 0 op_sel_hi:[0,1,0]
	s_nop 0
	s_waitcnt vmcnt(1)
	v_lshlrev_b32_e32 v98, 16, v240
	v_and_b32_e32 v99, 0xffff0000, v240
	v_lshlrev_b32_e32 v10, 16, v241
	v_and_b32_e32 v11, 0xffff0000, v241
	v_pk_mul_f32 v[100:101], v[0:1], v[10:11] op_sel:[1,0]
	v_pk_fma_f32 v[10:11], v[0:1], v[10:11], v[96:97] op_sel:[1,0,0]
	v_pk_fma_f32 v[94:95], v[0:1], v[98:99], v[94:95] op_sel:[1,0,0]
	v_lshlrev_b32_e32 v12, 16, v237
	v_and_b32_e32 v13, 0xffff0000, v237
	v_pk_mul_f32 v[104:105], v[0:1], v[98:99] op_sel:[1,0]
	v_pk_fma_f32 v[88:89], v[0:1], v[88:89], v[94:95] op_sel_hi:[0,1,1] neg_lo:[1,0,0] neg_hi:[1,0,0]
	v_pk_fma_f32 v[0:1], v[0:1], v[86:87], v[10:11] op_sel_hi:[0,1,1] neg_lo:[1,0,0] neg_hi:[1,0,0]
	v_pk_mul_f32 v[84:85], v[2:3], v[12:13] op_sel_hi:[0,1]
	v_pk_fma_f32 v[0:1], v[2:3], v[12:13], v[0:1] op_sel_hi:[0,1,1]
	v_pk_mul_f32 v[80:81], v[2:3], v[14:15] op_sel_hi:[0,1]
	v_pk_fma_f32 v[2:3], v[2:3], v[14:15], v[88:89] op_sel_hi:[0,1,1]
	v_pk_fma_f32 v[14:15], v[0:1], 0.5, v[84:85] op_sel_hi:[1,0,1] neg_lo:[0,0,1] neg_hi:[0,0,1]
	v_lshl_add_u64 v[84:85], s[30:31], 0, v[82:83]
	s_nop 0
	v_lshl_add_u32 v0, v55, 4, s17
	v_pk_fma_f32 v[80:81], v[2:3], 0.5, v[80:81] op_sel_hi:[1,0,1] neg_lo:[0,0,1] neg_hi:[0,0,1]
	ds_read_b128 v[0:3], v0
	v_pk_fma_f32 v[10:11], v[10:11], 0.5, v[100:101] op_sel_hi:[1,0,1] neg_lo:[0,0,1] neg_hi:[0,0,1]
	v_lshl_add_u64 v[82:83], s[28:29], 0, v[82:83]
	v_pk_fma_f32 v[12:13], v[94:95], 0.5, v[104:105] op_sel_hi:[1,0,1] neg_lo:[0,0,1] neg_hi:[0,0,1]
	s_nop 0
	s_waitcnt vmcnt(0)
	v_lshlrev_b32_e32 v88, 16, v242
	v_and_b32_e32 v89, 0xffff0000, v242
	v_lshlrev_b32_e32 v86, 16, v243
	v_and_b32_e32 v87, 0xffff0000, v243
	s_waitcnt lgkmcnt(0)
	v_pk_fma_f32 v[10:11], v[2:3], v[10:11], v[86:87]
	global_load_dwordx2 v[86:87], v[82:83], off
	v_pk_fma_f32 v[12:13], v[0:1], v[12:13], v[88:89]
	s_nop 0
	s_waitcnt vmcnt(0)
	v_lshlrev_b32_e32 v88, 16, v86
	v_and_b32_e32 v89, 0xffff0000, v86
	v_lshlrev_b32_e32 v86, 16, v87
	v_and_b32_e32 v87, 0xffff0000, v87
	v_pk_fma_f32 v[80:81], v[0:1], v[80:81], v[88:89]
	v_cvt_pk_bf16_f32 v0, v12, v13
	v_cvt_pk_bf16_f32 v1, v10, v11
	v_pk_fma_f32 v[14:15], v[2:3], v[14:15], v[86:87]
	v_cvt_pk_bf16_f32 v2, v80, v81
	s_nop 0
	v_cvt_pk_bf16_f32 v3, v14, v15
	global_store_dwordx2 v[84:85], v[0:1], off
	global_store_dwordx2 v[82:83], v[2:3], off
	v_mov_b32_e32 v0, v21
	s_nop 0
	v_lshlrev_b32_e32 v82, 2, v0
	v_add_u32_e32 v84, 0x100, v82
	v_ashrrev_i32_e32 v85, 31, v84
	v_lshlrev_b64 v[86:87], 1, v[84:85]
	v_lshl_add_u64 v[236:237], vcc, 0, v[86:87]
	global_load_dwordx2 v[236:237], v[236:237], off
	v_lshl_add_u64 v[238:239], s[48:49], 0, v[86:87]
	global_load_dwordx2 v[238:239], v[238:239], off
	v_lshl_add_u64 v[240:241], s[46:47], 0, v[86:87]
	global_load_dwordx2 v[240:241], v[240:241], off
	s_nop 0
	s_nop 0
	s_nop 0
	s_nop 0
	s_nop 0
	ds_read_b96 v[0:2], v53 offset:64
	s_nop 0
	v_ashrrev_i32_e32 v83, 31, v82
	s_nop 0
	s_waitcnt vmcnt(2)
	v_lshlrev_b32_e32 v94, 16, v236
	v_and_b32_e32 v95, 0xffff0000, v236
	s_nop 0
	s_waitcnt vmcnt(1)
	v_lshlrev_b32_e32 v104, 16, v238
	v_and_b32_e32 v105, 0xffff0000, v238
	v_lshlrev_b32_e32 v100, 16, v239
	v_and_b32_e32 v101, 0xffff0000, v239
	s_waitcnt lgkmcnt(0)
	v_pk_fma_f32 v[106:107], v[0:1], v[104:105], 0 op_sel_hi:[0,1,0]
	v_pk_fma_f32 v[108:109], v[0:1], v[100:101], 0 op_sel_hi:[0,1,0]
	s_nop 0
	s_waitcnt vmcnt(0)
	v_lshlrev_b32_e32 v110, 16, v240
	v_and_b32_e32 v111, 0xffff0000, v240
	v_lshlrev_b32_e32 v86, 16, v241
	v_and_b32_e32 v87, 0xffff0000, v241
	v_pk_fma_f32 v[108:109], v[0:1], v[86:87], v[108:109] op_sel:[1,0,0]
	v_pk_fma_f32 v[106:107], v[0:1], v[110:111], v[106:107] op_sel:[1,0,0]
	v_lshlrev_b32_e32 v88, 16, v237
	v_and_b32_e32 v89, 0xffff0000, v237
	v_pk_mul_f32 v[112:113], v[0:1], v[86:87] op_sel:[1,0]
	v_pk_mul_f32 v[114:115], v[0:1], v[110:111] op_sel:[1,0]
	v_pk_fma_f32 v[86:87], v[0:1], v[104:105], v[106:107] op_sel_hi:[0,1,1] neg_lo:[1,0,0] neg_hi:[1,0,0]
	v_pk_fma_f32 v[0:1], v[0:1], v[100:101], v[108:109] op_sel_hi:[0,1,1] neg_lo:[1,0,0] neg_hi:[1,0,0]
	v_lshlrev_b64 v[100:101], 1, v[82:83]
	v_pk_mul_f32 v[96:97], v[2:3], v[88:89] op_sel_hi:[0,1]
	v_pk_mul_f32 v[98:99], v[2:3], v[94:95] op_sel_hi:[0,1]
	v_pk_fma_f32 v[0:1], v[2:3], v[88:89], v[0:1] op_sel_hi:[0,1,1]
	v_pk_fma_f32 v[2:3], v[2:3], v[94:95], v[86:87] op_sel_hi:[0,1,1]
	v_lshl_add_u64 v[236:237], s[30:31], 0, v[100:101]
	global_load_dwordx2 v[236:237], v[236:237], off offset:512
	v_lshl_add_u64 v[238:239], s[28:29], 0, v[100:101]
	global_load_dwordx2 v[238:239], v[238:239], off offset:512
	v_lshl_add_u64 v[94:95], s[30:31], 0, v[100:101]
	s_nop 0
	v_pk_fma_f32 v[86:87], v[0:1], 0.5, v[96:97] op_sel_hi:[1,0,1] neg_lo:[0,0,1] neg_hi:[0,0,1]
	v_lshl_add_u32 v0, v84, 2, s17
	v_pk_fma_f32 v[88:89], v[2:3], 0.5, v[98:99] op_sel_hi:[1,0,1] neg_lo:[0,0,1] neg_hi:[0,0,1]
	ds_read_b128 v[0:3], v0
	v_pk_fma_f32 v[96:97], v[106:107], 0.5, v[114:115] op_sel_hi:[1,0,1] neg_lo:[0,0,1] neg_hi:[0,0,1]
	v_pk_fma_f32 v[98:99], v[108:109], 0.5, v[112:113] op_sel_hi:[1,0,1] neg_lo:[0,0,1] neg_hi:[0,0,1]
	s_nop 0
	s_waitcnt vmcnt(1)
	v_lshlrev_b32_e32 v84, 16, v236
	v_and_b32_e32 v85, 0xffff0000, v236
	v_lshlrev_b32_e32 v82, 16, v237
	v_and_b32_e32 v83, 0xffff0000, v237
	s_waitcnt lgkmcnt(0)
	v_pk_fma_f32 v[84:85], v[0:1], v[96:97], v[84:85]
	v_lshl_add_u64 v[96:97], s[28:29], 0, v[100:101]
	v_pk_fma_f32 v[82:83], v[2:3], v[98:99], v[82:83]
	s_nop 0
	s_nop 0
	s_waitcnt vmcnt(0)
	v_lshlrev_b32_e32 v100, 16, v238
	v_and_b32_e32 v101, 0xffff0000, v238
	v_lshlrev_b32_e32 v98, 16, v239
	v_and_b32_e32 v99, 0xffff0000, v239
	v_pk_fma_f32 v[88:89], v[0:1], v[88:89], v[100:101]
	v_cvt_pk_bf16_f32 v0, v84, v85
	v_cvt_pk_bf16_f32 v1, v82, v83
	v_pk_fma_f32 v[86:87], v[2:3], v[86:87], v[98:99]
	v_cvt_pk_bf16_f32 v2, v88, v89
	s_nop 0
	v_cvt_pk_bf16_f32 v3, v86, v87
	global_store_dwordx2 v[94:95], v[0:1], off offset:512
	global_store_dwordx2 v[96:97], v[2:3], off offset:512
	v_mov_b32_e32 v0, v21
	ds_read_b32 v98, v53 offset:72
	v_lshlrev_b32_e32 v94, 2, v0
	v_add_u32_e32 v96, 0x200, v94
	v_ashrrev_i32_e32 v97, 31, v96
	v_lshlrev_b64 v[100:101], 1, v[96:97]
	v_lshl_add_u64 v[236:237], vcc, 0, v[100:101]
	global_load_dwordx2 v[236:237], v[236:237], off
	v_lshl_add_u64 v[238:239], s[52:53], 0, v[100:101]
	global_load_dwordx2 v[238:239], v[238:239], off
	v_lshl_add_u64 v[240:241], s[50:51], 0, v[100:101]
	global_load_dwordx2 v[240:241], v[240:241], off
	v_lshl_add_u64 v[242:243], s[48:49], 0, v[100:101]
	global_load_dwordx2 v[242:243], v[242:243], off
	v_lshl_add_u64 v[244:245], s[46:47], 0, v[100:101]
	global_load_dwordx2 v[244:245], v[244:245], off
	s_nop 0
	s_nop 0
	s_nop 0
	s_nop 0
	s_nop 0
	s_nop 0
	v_ashrrev_i32_e32 v95, 31, v94
	s_nop 0
	s_waitcnt vmcnt(4)
	v_lshlrev_b32_e32 v104, 16, v236
	v_and_b32_e32 v105, 0xffff0000, v236
	v_lshlrev_b32_e32 v106, 16, v237
	v_and_b32_e32 v107, 0xffff0000, v237
	ds_read2_b64 v[0:3], v53 offset0:7 offset1:8
	s_nop 0
	s_waitcnt vmcnt(3)
	v_lshlrev_b32_e32 v114, 16, v238
	v_and_b32_e32 v115, 0xffff0000, v238
	v_lshlrev_b32_e32 v112, 16, v239
	v_and_b32_e32 v113, 0xffff0000, v239
	s_waitcnt lgkmcnt(0)
	v_pk_fma_f32 v[122:123], v[0:1], v[112:113], 0 op_sel_hi:[0,1,0]
	s_nop 0
	s_waitcnt vmcnt(2)
	v_lshlrev_b32_e32 v126, 16, v240
	v_and_b32_e32 v127, 0xffff0000, v240
	v_lshlrev_b32_e32 v124, 16, v241
	v_and_b32_e32 v125, 0xffff0000, v241
	v_pk_fma_f32 v[122:123], v[0:1], v[124:125], v[122:123] op_sel:[1,0,0]
	s_nop 0
	s_nop 0
	s_nop 0
	s_nop 0
	v_pk_fma_f32 v[116:117], v[0:1], v[114:115], 0 op_sel_hi:[0,1,0]
	v_pk_fma_f32 v[116:117], v[0:1], v[126:127], v[116:117] op_sel:[1,0,0]
	v_pk_mul_f32 v[108:109], v[98:99], v[106:107] op_sel_hi:[0,1]
	v_pk_mul_f32 v[110:111], v[98:99], v[104:105] op_sel_hi:[0,1]
	s_nop 0
	s_waitcnt vmcnt(1)
	v_lshlrev_b32_e32 v126, 16, v242
	v_and_b32_e32 v127, 0xffff0000, v242
	v_lshlrev_b32_e32 v124, 16, v243
	v_and_b32_e32 v125, 0xffff0000, v243
	v_pk_fma_f32 v[116:117], v[2:3], v[126:127], v[116:117] op_sel_hi:[0,1,1]
	v_pk_fma_f32 v[122:123], v[2:3], v[124:125], v[122:123] op_sel_hi:[0,1,1]
	s_nop 0
	s_waitcnt vmcnt(0)
	v_lshlrev_b32_e32 v124, 16, v244
	v_and_b32_e32 v125, 0xffff0000, v244
	v_lshlrev_b32_e32 v100, 16, v245
	v_and_b32_e32 v101, 0xffff0000, v245
	v_mov_b32_e32 v2, v3
	v_pk_mul_f32 v[126:127], v[2:3], v[100:101] op_sel_hi:[0,1]
	v_pk_mul_f32 v[128:129], v[2:3], v[124:125] op_sel_hi:[0,1]
	v_pk_fma_f32 v[122:123], v[2:3], v[100:101], v[122:123] op_sel_hi:[0,1,1]
	v_pk_fma_f32 v[2:3], v[2:3], v[124:125], v[116:117] op_sel_hi:[0,1,1]
	v_pk_fma_f32 v[100:101], v[0:1], v[114:115], v[2:3] op_sel_hi:[0,1,1] neg_lo:[1,0,0] neg_hi:[1,0,0]
	v_pk_fma_f32 v[0:1], v[0:1], v[112:113], v[122:123] op_sel_hi:[0,1,1] neg_lo:[1,0,0] neg_hi:[1,0,0]
	v_pk_fma_f32 v[0:1], v[98:99], v[106:107], v[0:1] op_sel_hi:[0,1,1]
	v_pk_fma_f32 v[98:99], v[98:99], v[104:105], v[100:101] op_sel_hi:[0,1,1]
	v_pk_fma_f32 v[100:101], v[98:99], s[12:13], v[110:111] op_sel_hi:[1,0,1] neg_lo:[0,0,1] neg_hi:[0,0,1]
	v_lshlrev_b64 v[110:111], 1, v[94:95]
	v_lshl_add_u64 v[236:237], s[30:31], 0, v[110:111]
	global_load_dwordx2 v[236:237], v[236:237], off offset:1024
	v_lshl_add_u64 v[238:239], s[28:29], 0, v[110:111]
	global_load_dwordx2 v[238:239], v[238:239], off offset:1024
	v_lshl_add_u64 v[104:105], s[30:31], 0, v[110:111]
	s_nop 0
	v_pk_fma_f32 v[98:99], v[0:1], s[12:13], v[108:109] op_sel_hi:[1,0,1] neg_lo:[0,0,1] neg_hi:[0,0,1]
	v_lshl_add_u32 v0, v96, 2, s17
	v_pk_fma_f32 v[106:107], v[102:103], v[2:3], v[128:129] op_sel_hi:[0,1,1] neg_lo:[0,0,1] neg_hi:[0,0,1]
	ds_read_b128 v[0:3], v0
	v_pk_fma_f32 v[108:109], v[102:103], v[122:123], v[126:127] op_sel_hi:[0,1,1] neg_lo:[0,0,1] neg_hi:[0,0,1]
	s_nop 0
	s_waitcnt vmcnt(1)
	v_lshlrev_b32_e32 v96, 16, v236
	v_and_b32_e32 v97, 0xffff0000, v236
	v_lshlrev_b32_e32 v94, 16, v237
	v_and_b32_e32 v95, 0xffff0000, v237
	s_waitcnt lgkmcnt(0)
	v_pk_fma_f32 v[96:97], v[0:1], v[106:107], v[96:97]
	v_lshl_add_u64 v[106:107], s[28:29], 0, v[110:111]
	v_pk_fma_f32 v[94:95], v[2:3], v[108:109], v[94:95]
	s_nop 0
	s_nop 0
	s_waitcnt vmcnt(0)
	v_lshlrev_b32_e32 v110, 16, v238
	v_and_b32_e32 v111, 0xffff0000, v238
	v_lshlrev_b32_e32 v108, 16, v239
	v_and_b32_e32 v109, 0xffff0000, v239
	v_pk_fma_f32 v[100:101], v[0:1], v[100:101], v[110:111]
	v_cvt_pk_bf16_f32 v0, v96, v97
	v_cvt_pk_bf16_f32 v1, v94, v95
	v_pk_fma_f32 v[98:99], v[2:3], v[98:99], v[108:109]
	v_cvt_pk_bf16_f32 v2, v100, v101
	s_nop 0
	v_cvt_pk_bf16_f32 v3, v98, v99
	global_store_dwordx2 v[104:105], v[0:1], off offset:1024
	global_store_dwordx2 v[106:107], v[2:3], off offset:1024
	v_mov_b32_e32 v0, v21
	ds_read_b32 v106, v53 offset:72
	v_lshlrev_b32_e32 v104, 2, v0
	v_add_u32_e32 v110, 0x300, v104
	v_ashrrev_i32_e32 v111, 31, v110
	v_lshlrev_b64 v[108:109], 1, v[110:111]
	v_lshl_add_u64 v[236:237], vcc, 0, v[108:109]
	global_load_dwordx2 v[236:237], v[236:237], off
	v_lshl_add_u64 v[238:239], s[52:53], 0, v[108:109]
	global_load_dwordx2 v[238:239], v[238:239], off
	v_lshl_add_u64 v[240:241], s[50:51], 0, v[108:109]
	global_load_dwordx2 v[240:241], v[240:241], off
	v_lshl_add_u64 v[242:243], s[48:49], 0, v[108:109]
	global_load_dwordx2 v[242:243], v[242:243], off
	v_lshl_add_u64 v[244:245], s[46:47], 0, v[108:109]
	global_load_dwordx2 v[244:245], v[244:245], off
	s_nop 0
	s_nop 0
	s_nop 0
	s_nop 0
	s_nop 0
	s_nop 0
	v_ashrrev_i32_e32 v105, 31, v104
	s_nop 0
	s_waitcnt vmcnt(4)
	v_lshlrev_b32_e32 v112, 16, v236
	v_and_b32_e32 v113, 0xffff0000, v236
	v_lshlrev_b32_e32 v114, 16, v237
	v_and_b32_e32 v115, 0xffff0000, v237
	ds_read2_b64 v[0:3], v53 offset0:7 offset1:8
	s_nop 0
	s_waitcnt vmcnt(3)
	v_lshlrev_b32_e32 v126, 16, v238
	v_and_b32_e32 v127, 0xffff0000, v238
	v_lshlrev_b32_e32 v124, 16, v239
	v_and_b32_e32 v125, 0xffff0000, v239
	s_waitcnt lgkmcnt(0)
	v_pk_fma_f32 v[130:131], v[0:1], v[124:125], 0 op_sel_hi:[0,1,0]
	s_nop 0
	s_waitcnt vmcnt(2)
	v_lshlrev_b32_e32 v134, 16, v240
	v_and_b32_e32 v135, 0xffff0000, v240
	v_lshlrev_b32_e32 v132, 16, v241
	v_and_b32_e32 v133, 0xffff0000, v241
	v_pk_fma_f32 v[130:131], v[0:1], v[132:133], v[130:131] op_sel:[1,0,0]
	s_nop 0
	s_nop 0
	s_nop 0
	s_nop 0
	v_pk_fma_f32 v[128:129], v[0:1], v[126:127], 0 op_sel_hi:[0,1,0]
	v_pk_fma_f32 v[128:129], v[0:1], v[134:135], v[128:129] op_sel:[1,0,0]
	v_pk_mul_f32 v[116:117], v[106:107], v[114:115] op_sel_hi:[0,1]
	v_pk_mul_f32 v[122:123], v[106:107], v[112:113] op_sel_hi:[0,1]
	s_nop 0
	s_waitcnt vmcnt(1)
	v_lshlrev_b32_e32 v134, 16, v242
	v_and_b32_e32 v135, 0xffff0000, v242
	v_lshlrev_b32_e32 v132, 16, v243
	v_and_b32_e32 v133, 0xffff0000, v243
	v_pk_fma_f32 v[128:129], v[2:3], v[134:135], v[128:129] op_sel_hi:[0,1,1]
	v_pk_fma_f32 v[130:131], v[2:3], v[132:133], v[130:131] op_sel_hi:[0,1,1]
	s_nop 0
	s_waitcnt vmcnt(0)
	v_lshlrev_b32_e32 v132, 16, v244
	v_and_b32_e32 v133, 0xffff0000, v244
	v_lshlrev_b32_e32 v108, 16, v245
	v_and_b32_e32 v109, 0xffff0000, v245
	v_mov_b32_e32 v2, v3
	v_pk_mul_f32 v[134:135], v[2:3], v[108:109] op_sel_hi:[0,1]
	v_pk_mul_f32 v[136:137], v[2:3], v[132:133] op_sel_hi:[0,1]
	v_pk_fma_f32 v[130:131], v[2:3], v[108:109], v[130:131] op_sel_hi:[0,1,1]
	v_pk_fma_f32 v[2:3], v[2:3], v[132:133], v[128:129] op_sel_hi:[0,1,1]
	v_pk_fma_f32 v[108:109], v[0:1], v[126:127], v[2:3] op_sel_hi:[0,1,1] neg_lo:[1,0,0] neg_hi:[1,0,0]
	v_pk_fma_f32 v[0:1], v[0:1], v[124:125], v[130:131] op_sel_hi:[0,1,1] neg_lo:[1,0,0] neg_hi:[1,0,0]
	v_pk_fma_f32 v[0:1], v[106:107], v[114:115], v[0:1] op_sel_hi:[0,1,1]
	v_pk_fma_f32 v[106:107], v[106:107], v[112:113], v[108:109] op_sel_hi:[0,1,1]
	v_lshlrev_b64 v[114:115], 1, v[104:105]
	v_pk_fma_f32 v[108:109], v[106:107], s[12:13], v[122:123] op_sel_hi:[1,0,1] neg_lo:[0,0,1] neg_hi:[0,0,1]
	v_pk_fma_f32 v[106:107], v[0:1], s[12:13], v[116:117] op_sel_hi:[1,0,1] neg_lo:[0,0,1] neg_hi:[0,0,1]
	v_lshl_add_u32 v0, v110, 2, s17
	v_lshl_add_u64 v[236:237], s[30:31], 0, v[114:115]
	global_load_dwordx2 v[236:237], v[236:237], off offset:1536
	v_lshl_add_u64 v[238:239], s[28:29], 0, v[114:115]
	global_load_dwordx2 v[238:239], v[238:239], off offset:1536
	v_lshl_add_u64 v[110:111], s[30:31], 0, v[114:115]
	s_nop 0
	v_pk_fma_f32 v[112:113], v[102:103], v[2:3], v[136:137] op_sel_hi:[0,1,1] neg_lo:[0,0,1] neg_hi:[0,0,1]
	ds_read_b128 v[0:3], v0
	v_pk_fma_f32 v[102:103], v[102:103], v[130:131], v[134:135] op_sel_hi:[0,1,1] neg_lo:[0,0,1] neg_hi:[0,0,1]
	s_nop 0
	s_waitcnt vmcnt(1)
	v_lshlrev_b32_e32 v116, 16, v236
	v_and_b32_e32 v117, 0xffff0000, v236
	v_lshlrev_b32_e32 v104, 16, v237
	v_and_b32_e32 v105, 0xffff0000, v237
	s_waitcnt lgkmcnt(0)
	v_pk_fma_f32 v[102:103], v[2:3], v[102:103], v[104:105]
	v_pk_fma_f32 v[104:105], v[0:1], v[112:113], v[116:117]
	v_lshl_add_u64 v[112:113], s[28:29], 0, v[114:115]
	s_nop 0
	s_nop 0
	s_waitcnt vmcnt(0)
	v_lshlrev_b32_e32 v116, 16, v238
	v_and_b32_e32 v117, 0xffff0000, v238
	v_lshlrev_b32_e32 v114, 16, v239
	v_and_b32_e32 v115, 0xffff0000, v239
	v_pk_fma_f32 v[108:109], v[0:1], v[108:109], v[116:117]
	v_cvt_pk_bf16_f32 v0, v104, v105
	v_cvt_pk_bf16_f32 v1, v102, v103
	v_pk_fma_f32 v[106:107], v[2:3], v[106:107], v[114:115]
	v_cvt_pk_bf16_f32 v2, v108, v109
	s_nop 0
	v_cvt_pk_bf16_f32 v3, v106, v107
	global_store_dwordx2 v[110:111], v[0:1], off offset:1536
	global_store_dwordx2 v[112:113], v[2:3], off offset:1536
	v_mov_b32_e32 v0, v21
	s_add_u32 s86, s92, s86
	v_lshlrev_b32_e32 v110, 2, v0
	v_add_u32_e32 v112, 0x400, v110
	v_ashrrev_i32_e32 v113, 31, v112
	v_lshlrev_b64 v[128:129], 1, v[112:113]
	v_lshl_add_u64 v[0:1], vcc, 0, v[128:129]
	global_load_dwordx2 v[0:1], v[0:1], off
	s_addc_u32 s87, s93, s87
	s_add_u32 s0, s92, s0
	v_lshl_add_u64 v[130:131], s[86:87], 0, v[128:129]
	s_addc_u32 s1, s93, s1
	global_load_dwordx2 v[132:133], v[130:131], off
	v_lshl_add_u64 v[138:139], s[0:1], 0, v[128:129]
	global_load_dwordx2 v[138:139], v[138:139], off
	ds_read_b32 v114, v53 offset:72
	s_add_u32 s2, s92, s2
	s_addc_u32 s3, s93, s3
	s_add_u32 s96, s92, s96
	s_addc_u32 s97, s93, s97
	v_ashrrev_i32_e32 v111, 31, v110
	s_add_u32 s42, s92, s42
	s_addc_u32 s43, s93, s43
	s_add_u32 s88, s92, s88
	s_addc_u32 s89, s93, s89
	s_add_u32 s36, s92, s36
	s_addc_u32 s37, s93, s37
	s_add_u32 s78, s92, s78
	s_addc_u32 s79, s93, s79
	s_add_u32 s76, s92, s76
	s_addc_u32 s77, s93, s77
	s_add_u32 s10, s92, s10
	s_addc_u32 s11, s93, s11
	s_add_u32 s8, s92, s8
	s_addc_u32 s9, s93, s9
	s_add_u32 s44, s92, s44
	s_addc_u32 s45, s93, s45
	s_nop 0
	s_waitcnt vmcnt(2)
	v_lshlrev_b32_e32 v116, 16, v0
	v_and_b32_e32 v117, 0xffff0000, v0
	v_lshlrev_b32_e32 v124, 16, v1
	v_and_b32_e32 v125, 0xffff0000, v1
	ds_read2_b64 v[0:3], v53 offset0:5 offset1:6
	s_nop 0
	s_waitcnt vmcnt(1)
	v_lshlrev_b32_e32 v130, 16, v132
	v_and_b32_e32 v131, 0xffff0000, v132
	v_lshlrev_b32_e32 v132, 16, v133
	v_and_b32_e32 v133, 0xffff0000, v133
	s_waitcnt lgkmcnt(0)
	v_pk_fma_f32 v[136:137], v[0:1], v[132:133], 0 op_sel_hi:[0,1,0]
	s_nop 0
	s_waitcnt vmcnt(0)
	v_lshlrev_b32_e32 v140, 16, v138
	v_and_b32_e32 v141, 0xffff0000, v138
	v_lshlrev_b32_e32 v138, 16, v139
	v_and_b32_e32 v139, 0xffff0000, v139
	v_pk_fma_f32 v[136:137], v[0:1], v[138:139], v[136:137] op_sel:[1,0,0]
	v_lshl_add_u64 v[236:237], s[2:3], 0, v[128:129]
	global_load_dwordx2 v[236:237], v[236:237], off
	v_lshl_add_u64 v[238:239], s[96:97], 0, v[128:129]
	global_load_dwordx2 v[238:239], v[238:239], off
	v_lshl_add_u64 v[240:241], s[52:53], 0, v[128:129]
	global_load_dwordx2 v[240:241], v[240:241], off
	v_lshl_add_u64 v[242:243], s[50:51], 0, v[128:129]
	global_load_dwordx2 v[242:243], v[242:243], off
	v_lshl_add_u64 v[244:245], s[48:49], 0, v[128:129]
	global_load_dwordx2 v[244:245], v[244:245], off
	v_lshl_add_u64 v[246:247], s[46:47], 0, v[128:129]
	global_load_dwordx2 v[246:247], v[246:247], off
	s_nop 0
	s_nop 0
	v_pk_fma_f32 v[134:135], v[0:1], v[130:131], 0 op_sel_hi:[0,1,0]
	v_pk_fma_f32 v[134:135], v[0:1], v[140:141], v[134:135] op_sel:[1,0,0]
	v_pk_mul_f32 v[122:123], v[114:115], v[124:125] op_sel_hi:[0,1]
	v_pk_mul_f32 v[126:127], v[114:115], v[116:117] op_sel_hi:[0,1]
	s_nop 0
	s_waitcnt vmcnt(5)
	v_lshlrev_b32_e32 v140, 16, v236
	v_and_b32_e32 v141, 0xffff0000, v236
	v_lshlrev_b32_e32 v138, 16, v237
	v_and_b32_e32 v139, 0xffff0000, v237
	v_pk_fma_f32 v[136:137], v[2:3], v[138:139], v[136:137] op_sel_hi:[0,1,1]
	s_nop 0
	s_nop 0
	v_pk_fma_f32 v[134:135], v[2:3], v[140:141], v[134:135] op_sel_hi:[0,1,1]
	v_mov_b32_e32 v2, v3
	s_nop 0
	s_waitcnt vmcnt(4)
	v_lshlrev_b32_e32 v140, 16, v238
	v_and_b32_e32 v141, 0xffff0000, v238
	v_lshlrev_b32_e32 v138, 16, v239
	v_and_b32_e32 v139, 0xffff0000, v239
	v_pk_fma_f32 v[138:139], v[2:3], v[138:139], v[136:137] op_sel_hi:[0,1,1]
	v_pk_fma_f32 v[2:3], v[2:3], v[140:141], v[134:135] op_sel_hi:[0,1,1]
	s_nop 0
	s_nop 0
	ds_read2_b64 v[134:137], v53 offset0:7 offset1:8
	s_nop 0
	s_waitcnt vmcnt(3)
	v_lshlrev_b32_e32 v142, 16, v240
	v_and_b32_e32 v143, 0xffff0000, v240
	v_lshlrev_b32_e32 v140, 16, v241
	v_and_b32_e32 v141, 0xffff0000, v241
	s_waitcnt lgkmcnt(0)
	v_pk_fma_f32 v[138:139], v[134:135], v[140:141], v[138:139] op_sel_hi:[0,1,1]
	s_nop 0
	s_nop 0
	v_pk_fma_f32 v[2:3], v[134:135], v[142:143], v[2:3] op_sel_hi:[0,1,1]
	s_nop 0
	s_waitcnt vmcnt(2)
	v_lshlrev_b32_e32 v142, 16, v242
	v_and_b32_e32 v143, 0xffff0000, v242
	v_lshlrev_b32_e32 v140, 16, v243
	v_and_b32_e32 v141, 0xffff0000, v243
	v_pk_fma_f32 v[138:139], v[134:135], v[140:141], v[138:139] op_sel:[1,0,0]
	v_pk_fma_f32 v[2:3], v[134:135], v[142:143], v[2:3] op_sel:[1,0,0]
	s_nop 0
	s_nop 0
	s_nop 0
	s_nop 0
	s_nop 0
	s_waitcnt vmcnt(1)
	v_lshlrev_b32_e32 v140, 16, v244
	v_and_b32_e32 v141, 0xffff0000, v244
	v_lshlrev_b32_e32 v134, 16, v245
	v_and_b32_e32 v135, 0xffff0000, v245
	v_pk_fma_f32 v[2:3], v[136:137], v[140:141], v[2:3] op_sel_hi:[0,1,1]
	v_pk_fma_f32 v[134:135], v[136:137], v[134:135], v[138:139] op_sel_hi:[0,1,1]
	s_nop 0
	s_waitcnt vmcnt(0)
	v_lshlrev_b32_e32 v138, 16, v246
	v_and_b32_e32 v139, 0xffff0000, v246
	v_lshlrev_b32_e32 v128, 16, v247
	v_and_b32_e32 v129, 0xffff0000, v247
	v_mov_b32_e32 v136, v137
	v_pk_mul_f32 v[140:141], v[136:137], v[128:129] op_sel_hi:[0,1]
	v_pk_fma_f32 v[128:129], v[136:137], v[128:129], v[134:135] op_sel_hi:[0,1,1]
	v_pk_fma_f32 v[2:3], v[136:137], v[138:139], v[2:3] op_sel_hi:[0,1,1]
	v_pk_fma_f32 v[130:131], v[0:1], v[130:131], v[2:3] op_sel_hi:[0,1,1] neg_lo:[1,0,0] neg_hi:[1,0,0]
	v_pk_fma_f32 v[0:1], v[0:1], v[132:133], v[128:129] op_sel_hi:[0,1,1] neg_lo:[1,0,0] neg_hi:[1,0,0]
	v_pk_fma_f32 v[0:1], v[114:115], v[124:125], v[0:1] op_sel_hi:[0,1,1]
	v_pk_fma_f32 v[114:115], v[114:115], v[116:117], v[130:131] op_sel_hi:[0,1,1]
	v_pk_fma_f32 v[116:117], v[120:121], v[114:115], v[126:127] op_sel_hi:[0,1,1] neg_lo:[0,0,1] neg_hi:[0,0,1]
	v_pk_fma_f32 v[126:127], v[118:119], v[128:129], v[140:141] op_sel_hi:[0,1,1] neg_lo:[0,0,1] neg_hi:[0,0,1]
	v_lshlrev_b64 v[128:129], 1, v[110:111]
	v_pk_fma_f32 v[114:115], v[120:121], v[0:1], v[122:123] op_sel_hi:[0,1,1] neg_lo:[0,0,1] neg_hi:[0,0,1]
	v_lshl_add_u64 v[236:237], s[30:31], 0, v[128:129]
	global_load_dwordx2 v[236:237], v[236:237], off offset:2048
	v_lshl_add_u64 v[238:239], s[28:29], 0, v[128:129]
	global_load_dwordx2 v[238:239], v[238:239], off offset:2048
	v_lshl_add_u64 v[122:123], s[30:31], 0, v[128:129]
	s_nop 0
	v_pk_mul_f32 v[142:143], v[136:137], v[138:139] op_sel_hi:[0,1]
	v_lshl_add_u32 v0, v112, 2, s17
	v_pk_fma_f32 v[124:125], v[118:119], v[2:3], v[142:143] op_sel_hi:[0,1,1] neg_lo:[0,0,1] neg_hi:[0,0,1]
	ds_read_b128 v[0:3], v0
	s_nop 0
	s_waitcnt vmcnt(1)
	v_lshlrev_b32_e32 v112, 16, v236
	v_and_b32_e32 v113, 0xffff0000, v236
	v_lshlrev_b32_e32 v110, 16, v237
	v_and_b32_e32 v111, 0xffff0000, v237
	s_waitcnt lgkmcnt(0)
	v_pk_fma_f32 v[112:113], v[0:1], v[124:125], v[112:113]
	v_lshl_add_u64 v[124:125], s[28:29], 0, v[128:129]
	v_pk_fma_f32 v[110:111], v[2:3], v[126:127], v[110:111]
	s_nop 0
	s_nop 0
	s_waitcnt vmcnt(0)
	v_lshlrev_b32_e32 v128, 16, v238
	v_and_b32_e32 v129, 0xffff0000, v238
	v_lshlrev_b32_e32 v126, 16, v239
	v_and_b32_e32 v127, 0xffff0000, v239
	v_pk_fma_f32 v[116:117], v[0:1], v[116:117], v[128:129]
	v_cvt_pk_bf16_f32 v0, v112, v113
	v_cvt_pk_bf16_f32 v1, v110, v111
	v_pk_fma_f32 v[114:115], v[2:3], v[114:115], v[126:127]
	v_cvt_pk_bf16_f32 v2, v116, v117
	s_nop 0
	v_cvt_pk_bf16_f32 v3, v114, v115
	global_store_dwordx2 v[122:123], v[0:1], off offset:2048
	global_store_dwordx2 v[124:125], v[2:3], off offset:2048
	v_mov_b32_e32 v0, v21
	ds_read_b32 v122, v53 offset:72
	v_lshlrev_b32_e32 v126, 2, v0
	v_add_u32_e32 v128, 0x500, v126
	v_ashrrev_i32_e32 v129, 31, v128
	v_lshlrev_b64 v[136:137], 1, v[128:129]
	v_lshl_add_u64 v[236:237], vcc, 0, v[136:137]
	global_load_dwordx2 v[236:237], v[236:237], off
	v_lshl_add_u64 v[238:239], s[86:87], 0, v[136:137]
	global_load_dwordx2 v[238:239], v[238:239], off
	v_lshl_add_u64 v[240:241], s[0:1], 0, v[136:137]
	global_load_dwordx2 v[240:241], v[240:241], off
	v_lshl_add_u64 v[242:243], s[2:3], 0, v[136:137]
	global_load_dwordx2 v[242:243], v[242:243], off
	v_lshl_add_u64 v[244:245], s[96:97], 0, v[136:137]
	global_load_dwordx2 v[244:245], v[244:245], off
	v_lshl_add_u64 v[246:247], s[52:53], 0, v[136:137]
	global_load_dwordx2 v[246:247], v[246:247], off
	s_nop 0
	s_nop 0
	v_lshl_add_u64 v[138:139], s[86:87], 0, v[136:137]
	s_nop 0
	s_nop 0
	s_nop 0
	v_ashrrev_i32_e32 v127, 31, v126
	s_nop 0
	s_waitcnt vmcnt(5)
	v_lshlrev_b32_e32 v124, 16, v236
	v_and_b32_e32 v125, 0xffff0000, v236
	v_lshlrev_b32_e32 v132, 16, v237
	v_and_b32_e32 v133, 0xffff0000, v237
	ds_read2_b64 v[0:3], v53 offset0:5 offset1:6
	s_nop 0
	s_waitcnt vmcnt(4)
	v_lshlrev_b32_e32 v138, 16, v238
	v_and_b32_e32 v139, 0xffff0000, v238
	v_lshlrev_b32_e32 v140, 16, v239
	v_and_b32_e32 v141, 0xffff0000, v239
	s_waitcnt lgkmcnt(0)
	v_pk_fma_f32 v[144:145], v[0:1], v[140:141], 0 op_sel_hi:[0,1,0]
	s_nop 0
	s_waitcnt vmcnt(3)
	v_lshlrev_b32_e32 v148, 16, v240
	v_and_b32_e32 v149, 0xffff0000, v240
	v_lshlrev_b32_e32 v146, 16, v241
	v_and_b32_e32 v147, 0xffff0000, v241
	v_pk_fma_f32 v[144:145], v[0:1], v[146:147], v[144:145] op_sel:[1,0,0]
	s_nop 0
	s_nop 0
	v_pk_fma_f32 v[142:143], v[0:1], v[138:139], 0 op_sel_hi:[0,1,0]
	v_pk_fma_f32 v[142:143], v[0:1], v[148:149], v[142:143] op_sel:[1,0,0]
	v_pk_mul_f32 v[130:131], v[122:123], v[132:133] op_sel_hi:[0,1]
	v_pk_mul_f32 v[134:135], v[122:123], v[124:125] op_sel_hi:[0,1]
	s_nop 0
	s_waitcnt vmcnt(2)
	v_lshlrev_b32_e32 v148, 16, v242
	v_and_b32_e32 v149, 0xffff0000, v242
	v_lshlrev_b32_e32 v146, 16, v243
	v_and_b32_e32 v147, 0xffff0000, v243
	v_pk_fma_f32 v[144:145], v[2:3], v[146:147], v[144:145] op_sel_hi:[0,1,1]
	s_nop 0
	s_nop 0
	v_pk_fma_f32 v[142:143], v[2:3], v[148:149], v[142:143] op_sel_hi:[0,1,1]
	v_mov_b32_e32 v2, v3
	s_nop 0
	s_waitcnt vmcnt(1)
	v_lshlrev_b32_e32 v148, 16, v244
	v_and_b32_e32 v149, 0xffff0000, v244
	v_lshlrev_b32_e32 v146, 16, v245
	v_and_b32_e32 v147, 0xffff0000, v245
	v_pk_fma_f32 v[146:147], v[2:3], v[146:147], v[144:145] op_sel_hi:[0,1,1]
	v_pk_fma_f32 v[2:3], v[2:3], v[148:149], v[142:143] op_sel_hi:[0,1,1]
	s_nop 0
	s_nop 0
	ds_read2_b64 v[142:145], v53 offset0:7 offset1:8
	s_nop 0
	s_waitcnt vmcnt(0)
	v_lshlrev_b32_e32 v150, 16, v246
	v_and_b32_e32 v151, 0xffff0000, v246
	v_lshlrev_b32_e32 v148, 16, v247
	v_and_b32_e32 v149, 0xffff0000, v247
	s_waitcnt lgkmcnt(0)
	v_pk_fma_f32 v[146:147], v[142:143], v[148:149], v[146:147] op_sel_hi:[0,1,1]
	v_lshl_add_u64 v[236:237], s[50:51], 0, v[136:137]
	global_load_dwordx2 v[236:237], v[236:237], off
	v_lshl_add_u64 v[238:239], s[48:49], 0, v[136:137]
	global_load_dwordx2 v[238:239], v[238:239], off
	v_lshl_add_u64 v[240:241], s[46:47], 0, v[136:137]
	global_load_dwordx2 v[240:241], v[240:241], off
	s_nop 0
	s_nop 0
	v_pk_fma_f32 v[2:3], v[142:143], v[150:151], v[2:3] op_sel_hi:[0,1,1]
	s_nop 0
	s_waitcnt vmcnt(2)
	v_lshlrev_b32_e32 v150, 16, v236
	v_and_b32_e32 v151, 0xffff0000, v236
	v_lshlrev_b32_e32 v148, 16, v237
	v_and_b32_e32 v149, 0xffff0000, v237
	v_pk_fma_f32 v[146:147], v[142:143], v[148:149], v[146:147] op_sel:[1,0,0]
	v_pk_fma_f32 v[2:3], v[142:143], v[150:151], v[2:3] op_sel:[1,0,0]
	s_nop 0
	s_nop 0
	s_nop 0
	s_nop 0
	s_nop 0
	s_waitcnt vmcnt(1)
	v_lshlrev_b32_e32 v148, 16, v238
	v_and_b32_e32 v149, 0xffff0000, v238
	v_lshlrev_b32_e32 v142, 16, v239
	v_and_b32_e32 v143, 0xffff0000, v239
	v_pk_fma_f32 v[2:3], v[144:145], v[148:149], v[2:3] op_sel_hi:[0,1,1]
	v_pk_fma_f32 v[142:143], v[144:145], v[142:143], v[146:147] op_sel_hi:[0,1,1]
	s_nop 0
	s_waitcnt vmcnt(0)
	v_lshlrev_b32_e32 v146, 16, v240
	v_and_b32_e32 v147, 0xffff0000, v240
	v_lshlrev_b32_e32 v136, 16, v241
	v_and_b32_e32 v137, 0xffff0000, v241
	v_mov_b32_e32 v144, v145
	v_pk_mul_f32 v[148:149], v[144:145], v[136:137] op_sel_hi:[0,1]
	v_pk_fma_f32 v[136:137], v[144:145], v[136:137], v[142:143] op_sel_hi:[0,1,1]
	v_pk_fma_f32 v[2:3], v[144:145], v[146:147], v[2:3] op_sel_hi:[0,1,1]
	v_pk_fma_f32 v[138:139], v[0:1], v[138:139], v[2:3] op_sel_hi:[0,1,1] neg_lo:[1,0,0] neg_hi:[1,0,0]
	v_pk_fma_f32 v[0:1], v[0:1], v[140:141], v[136:137] op_sel_hi:[0,1,1] neg_lo:[1,0,0] neg_hi:[1,0,0]
	v_pk_fma_f32 v[0:1], v[122:123], v[132:133], v[0:1] op_sel_hi:[0,1,1]
	v_pk_fma_f32 v[122:123], v[122:123], v[124:125], v[138:139] op_sel_hi:[0,1,1]
	v_pk_fma_f32 v[124:125], v[120:121], v[122:123], v[134:135] op_sel_hi:[0,1,1] neg_lo:[0,0,1] neg_hi:[0,0,1]
	v_pk_fma_f32 v[122:123], v[120:121], v[0:1], v[130:131] op_sel_hi:[0,1,1] neg_lo:[0,0,1] neg_hi:[0,0,1]
	v_lshl_add_u32 v0, v128, 2, s17
	v_lshlrev_b64 v[128:129], 1, v[126:127]
	v_lshl_add_u64 v[126:127], s[30:31], 0, v[128:129]
	global_load_dwordx2 v[130:131], v[126:127], off offset:2560
	v_pk_mul_f32 v[150:151], v[144:145], v[146:147] op_sel_hi:[0,1]
	v_pk_fma_f32 v[120:121], v[118:119], v[2:3], v[150:151] op_sel_hi:[0,1,1] neg_lo:[0,0,1] neg_hi:[0,0,1]
	ds_read_b128 v[0:3], v0
	v_pk_fma_f32 v[118:119], v[118:119], v[136:137], v[148:149] op_sel_hi:[0,1,1] neg_lo:[0,0,1] neg_hi:[0,0,1]
	v_lshl_add_u64 v[128:129], s[28:29], 0, v[128:129]
	s_nop 0
	s_waitcnt vmcnt(0)
	v_lshlrev_b32_e32 v132, 16, v130
	v_and_b32_e32 v133, 0xffff0000, v130
	v_lshlrev_b32_e32 v130, 16, v131
	v_and_b32_e32 v131, 0xffff0000, v131
	s_waitcnt lgkmcnt(0)
	v_pk_fma_f32 v[118:119], v[2:3], v[118:119], v[130:131]
	global_load_dwordx2 v[130:131], v[128:129], off offset:2560
	v_pk_fma_f32 v[120:121], v[0:1], v[120:121], v[132:133]
	s_nop 0
	s_waitcnt vmcnt(0)
	v_lshlrev_b32_e32 v132, 16, v130
	v_and_b32_e32 v133, 0xffff0000, v130
	v_lshlrev_b32_e32 v130, 16, v131
	v_and_b32_e32 v131, 0xffff0000, v131
	v_pk_fma_f32 v[124:125], v[0:1], v[124:125], v[132:133]
	v_cvt_pk_bf16_f32 v0, v120, v121
	v_cvt_pk_bf16_f32 v1, v118, v119
	v_pk_fma_f32 v[122:123], v[2:3], v[122:123], v[130:131]
	v_cvt_pk_bf16_f32 v2, v124, v125
	s_nop 0
	v_cvt_pk_bf16_f32 v3, v122, v123
	global_store_dwordx2 v[126:127], v[0:1], off offset:2560
	global_store_dwordx2 v[128:129], v[2:3], off offset:2560
	v_mov_b32_e32 v0, v21
	ds_read_b32 v130, v53 offset:72
	v_lshlrev_b32_e32 v126, 2, v0
	v_add_u32_e32 v128, 0x600, v126
	v_ashrrev_i32_e32 v129, 31, v128
	v_lshlrev_b64 v[140:141], 1, v[128:129]
	v_lshl_add_u64 v[236:237], vcc, 0, v[140:141]
	global_load_dwordx2 v[236:237], v[236:237], off
	v_lshl_add_u64 v[238:239], s[42:43], 0, v[140:141]
	global_load_dwordx2 v[238:239], v[238:239], off
	v_lshl_add_u64 v[240:241], s[88:89], 0, v[140:141]
	global_load_dwordx2 v[240:241], v[240:241], off
	v_lshl_add_u64 v[242:243], s[36:37], 0, v[140:141]
	global_load_dwordx2 v[242:243], v[242:243], off
	v_lshl_add_u64 v[244:245], s[78:79], 0, v[140:141]
	global_load_dwordx2 v[244:245], v[244:245], off
	v_lshl_add_u64 v[246:247], s[76:77], 0, v[140:141]
	global_load_dwordx2 v[246:247], v[246:247], off
	s_nop 0
	s_nop 0
	v_lshl_add_u64 v[142:143], s[42:43], 0, v[140:141]
	s_nop 0
	s_nop 0
	s_nop 0
	v_ashrrev_i32_e32 v127, 31, v126
	s_nop 0
	s_waitcnt vmcnt(5)
	v_lshlrev_b32_e32 v132, 16, v236
	v_and_b32_e32 v133, 0xffff0000, v236
	v_lshlrev_b32_e32 v136, 16, v237
	v_and_b32_e32 v137, 0xffff0000, v237
	ds_read2_b64 v[0:3], v53 offset0:1 offset1:2
	s_nop 0
	s_waitcnt vmcnt(4)
	v_lshlrev_b32_e32 v142, 16, v238
	v_and_b32_e32 v143, 0xffff0000, v238
	v_lshlrev_b32_e32 v144, 16, v239
	v_and_b32_e32 v145, 0xffff0000, v239
	s_waitcnt lgkmcnt(0)
	v_pk_fma_f32 v[148:149], v[0:1], v[144:145], 0 op_sel_hi:[0,1,0]
	s_nop 0
	s_waitcnt vmcnt(3)
	v_lshlrev_b32_e32 v152, 16, v240
	v_and_b32_e32 v153, 0xffff0000, v240
	v_lshlrev_b32_e32 v150, 16, v241
	v_and_b32_e32 v151, 0xffff0000, v241
	v_pk_fma_f32 v[148:149], v[0:1], v[150:151], v[148:149] op_sel:[1,0,0]
	s_nop 0
	s_nop 0
	v_pk_fma_f32 v[146:147], v[0:1], v[142:143], 0 op_sel_hi:[0,1,0]
	v_pk_fma_f32 v[146:147], v[0:1], v[152:153], v[146:147] op_sel:[1,0,0]
	v_pk_mul_f32 v[134:135], v[130:131], v[136:137] op_sel_hi:[0,1]
	v_pk_mul_f32 v[138:139], v[130:131], v[132:133] op_sel_hi:[0,1]
	s_nop 0
	s_waitcnt vmcnt(2)
	v_lshlrev_b32_e32 v152, 16, v242
	v_and_b32_e32 v153, 0xffff0000, v242
	v_lshlrev_b32_e32 v150, 16, v243
	v_and_b32_e32 v151, 0xffff0000, v243
	v_pk_fma_f32 v[148:149], v[2:3], v[150:151], v[148:149] op_sel_hi:[0,1,1]
	s_nop 0
	s_nop 0
	v_pk_fma_f32 v[146:147], v[2:3], v[152:153], v[146:147] op_sel_hi:[0,1,1]
	v_mov_b32_e32 v2, v3
	s_nop 0
	s_waitcnt vmcnt(1)
	v_lshlrev_b32_e32 v152, 16, v244
	v_and_b32_e32 v153, 0xffff0000, v244
	v_lshlrev_b32_e32 v150, 16, v245
	v_and_b32_e32 v151, 0xffff0000, v245
	v_pk_fma_f32 v[150:151], v[2:3], v[150:151], v[148:149] op_sel_hi:[0,1,1]
	v_pk_fma_f32 v[2:3], v[2:3], v[152:153], v[146:147] op_sel_hi:[0,1,1]
	s_nop 0
	s_nop 0
	ds_read2_b64 v[146:149], v53 offset0:3 offset1:4
	s_nop 0
	s_waitcnt vmcnt(0)
	v_lshlrev_b32_e32 v154, 16, v246
	v_and_b32_e32 v155, 0xffff0000, v246
	v_lshlrev_b32_e32 v152, 16, v247
	v_and_b32_e32 v153, 0xffff0000, v247
	s_waitcnt lgkmcnt(0)
	v_pk_fma_f32 v[150:151], v[146:147], v[152:153], v[150:151] op_sel_hi:[0,1,1]
	v_lshl_add_u64 v[236:237], s[10:11], 0, v[140:141]
	global_load_dwordx2 v[236:237], v[236:237], off
	v_lshl_add_u64 v[238:239], s[8:9], 0, v[140:141]
	global_load_dwordx2 v[238:239], v[238:239], off
	v_lshl_add_u64 v[240:241], s[44:45], 0, v[140:141]
	global_load_dwordx2 v[240:241], v[240:241], off
	v_lshl_add_u64 v[242:243], s[86:87], 0, v[140:141]
	global_load_dwordx2 v[242:243], v[242:243], off
	v_lshl_add_u64 v[244:245], s[0:1], 0, v[140:141]
	global_load_dwordx2 v[244:245], v[244:245], off
	v_lshl_add_u64 v[246:247], s[2:3], 0, v[140:141]
	global_load_dwordx2 v[246:247], v[246:247], off
	s_nop 0
	s_nop 0
	v_pk_fma_f32 v[2:3], v[146:147], v[154:155], v[2:3] op_sel_hi:[0,1,1]
	s_nop 0
	s_waitcnt vmcnt(5)
	v_lshlrev_b32_e32 v154, 16, v236
	v_and_b32_e32 v155, 0xffff0000, v236
	v_lshlrev_b32_e32 v152, 16, v237
	v_and_b32_e32 v153, 0xffff0000, v237
	v_pk_fma_f32 v[150:151], v[146:147], v[152:153], v[150:151] op_sel:[1,0,0]
	v_pk_fma_f32 v[2:3], v[146:147], v[154:155], v[2:3] op_sel:[1,0,0]
	s_nop 0
	s_nop 0
	s_nop 0
	s_waitcnt vmcnt(4)
	v_lshlrev_b32_e32 v152, 16, v238
	v_and_b32_e32 v153, 0xffff0000, v238
	v_lshlrev_b32_e32 v146, 16, v239
	v_and_b32_e32 v147, 0xffff0000, v239
	v_pk_fma_f32 v[146:147], v[148:149], v[146:147], v[150:151] op_sel_hi:[0,1,1]
	s_nop 0
	s_nop 0
	v_pk_fma_f32 v[2:3], v[148:149], v[152:153], v[2:3] op_sel_hi:[0,1,1]
	v_mov_b32_e32 v148, v149
	s_nop 0
	s_waitcnt vmcnt(3)
	v_lshlrev_b32_e32 v152, 16, v240
	v_and_b32_e32 v153, 0xffff0000, v240
	v_pk_fma_f32 v[2:3], v[148:149], v[152:153], v[2:3] op_sel_hi:[0,1,1]
	s_nop 0
	s_nop 0
	v_lshlrev_b32_e32 v150, 16, v241
	v_and_b32_e32 v151, 0xffff0000, v241
	v_pk_fma_f32 v[150:151], v[148:149], v[150:151], v[146:147] op_sel_hi:[0,1,1]
	ds_read2_b64 v[146:149], v53 offset0:5 offset1:6
	s_nop 0
	s_waitcnt vmcnt(2)
	v_lshlrev_b32_e32 v154, 16, v242
	v_and_b32_e32 v155, 0xffff0000, v242
	v_lshlrev_b32_e32 v152, 16, v243
	v_and_b32_e32 v153, 0xffff0000, v243
	s_waitcnt lgkmcnt(0)
	v_pk_fma_f32 v[150:151], v[146:147], v[152:153], v[150:151] op_sel_hi:[0,1,1]
	s_nop 0
	s_nop 0
	v_pk_fma_f32 v[2:3], v[146:147], v[154:155], v[2:3] op_sel_hi:[0,1,1]
	s_nop 0
	s_waitcnt vmcnt(1)
	v_lshlrev_b32_e32 v154, 16, v244
	v_and_b32_e32 v155, 0xffff0000, v244
	v_lshlrev_b32_e32 v152, 16, v245
	v_and_b32_e32 v153, 0xffff0000, v245
	v_pk_fma_f32 v[150:151], v[146:147], v[152:153], v[150:151] op_sel:[1,0,0]
	v_pk_fma_f32 v[2:3], v[146:147], v[154:155], v[2:3] op_sel:[1,0,0]
	s_nop 0
	s_nop 0
	s_nop 0
	s_waitcnt vmcnt(0)
	v_lshlrev_b32_e32 v152, 16, v246
	v_and_b32_e32 v153, 0xffff0000, v246
	v_lshlrev_b32_e32 v146, 16, v247
	v_and_b32_e32 v147, 0xffff0000, v247
	v_pk_fma_f32 v[146:147], v[148:149], v[146:147], v[150:151] op_sel_hi:[0,1,1]
	v_lshl_add_u64 v[236:237], s[96:97], 0, v[140:141]
	global_load_dwordx2 v[236:237], v[236:237], off
	v_lshl_add_u64 v[238:239], s[52:53], 0, v[140:141]
	global_load_dwordx2 v[238:239], v[238:239], off
	v_lshl_add_u64 v[240:241], s[50:51], 0, v[140:141]
	global_load_dwordx2 v[240:241], v[240:241], off
	v_lshl_add_u64 v[242:243], s[48:49], 0, v[140:141]
	global_load_dwordx2 v[242:243], v[242:243], off
	v_lshl_add_u64 v[244:245], s[46:47], 0, v[140:141]
	global_load_dwordx2 v[244:245], v[244:245], off
	s_nop 0
	s_nop 0
	v_pk_fma_f32 v[2:3], v[148:149], v[152:153], v[2:3] op_sel_hi:[0,1,1]
	v_mov_b32_e32 v148, v149
	s_nop 0
	s_waitcnt vmcnt(4)
	v_lshlrev_b32_e32 v152, 16, v236
	v_and_b32_e32 v153, 0xffff0000, v236
	v_pk_fma_f32 v[2:3], v[148:149], v[152:153], v[2:3] op_sel_hi:[0,1,1]
	s_nop 0
	s_nop 0
	v_lshlrev_b32_e32 v150, 16, v237
	v_and_b32_e32 v151, 0xffff0000, v237
	v_pk_fma_f32 v[150:151], v[148:149], v[150:151], v[146:147] op_sel_hi:[0,1,1]
	ds_read2_b64 v[146:149], v53 offset0:7 offset1:8
	s_nop 0
	s_waitcnt vmcnt(3)
	v_lshlrev_b32_e32 v154, 16, v238
	v_and_b32_e32 v155, 0xffff0000, v238
	v_lshlrev_b32_e32 v152, 16, v239
	v_and_b32_e32 v153, 0xffff0000, v239
	s_waitcnt lgkmcnt(0)
	v_pk_fma_f32 v[150:151], v[146:147], v[152:153], v[150:151] op_sel_hi:[0,1,1]
	s_nop 0
	s_nop 0
	v_pk_fma_f32 v[2:3], v[146:147], v[154:155], v[2:3] op_sel_hi:[0,1,1]
	s_nop 0
	s_waitcnt vmcnt(2)
	v_lshlrev_b32_e32 v154, 16, v240
	v_and_b32_e32 v155, 0xffff0000, v240
	v_lshlrev_b32_e32 v152, 16, v241
	v_and_b32_e32 v153, 0xffff0000, v241
	v_pk_fma_f32 v[150:151], v[146:147], v[152:153], v[150:151] op_sel:[1,0,0]
	v_pk_fma_f32 v[2:3], v[146:147], v[154:155], v[2:3] op_sel:[1,0,0]
	s_nop 0
	s_nop 0
	s_nop 0
	s_nop 0
	s_nop 0
	s_waitcnt vmcnt(1)
	v_lshlrev_b32_e32 v152, 16, v242
	v_and_b32_e32 v153, 0xffff0000, v242
	v_lshlrev_b32_e32 v146, 16, v243
	v_and_b32_e32 v147, 0xffff0000, v243
	v_pk_fma_f32 v[2:3], v[148:149], v[152:153], v[2:3] op_sel_hi:[0,1,1]
	v_pk_fma_f32 v[146:147], v[148:149], v[146:147], v[150:151] op_sel_hi:[0,1,1]
	s_nop 0
	s_waitcnt vmcnt(0)
	v_lshlrev_b32_e32 v150, 16, v244
	v_and_b32_e32 v151, 0xffff0000, v244
	v_lshlrev_b32_e32 v140, 16, v245
	v_and_b32_e32 v141, 0xffff0000, v245
	v_mov_b32_e32 v148, v149
	v_pk_mul_f32 v[152:153], v[148:149], v[140:141] op_sel_hi:[0,1]
	v_pk_fma_f32 v[140:141], v[148:149], v[140:141], v[146:147] op_sel_hi:[0,1,1]
	v_pk_fma_f32 v[2:3], v[148:149], v[150:151], v[2:3] op_sel_hi:[0,1,1]
	v_pk_fma_f32 v[142:143], v[0:1], v[142:143], v[2:3] op_sel_hi:[0,1,1] neg_lo:[1,0,0] neg_hi:[1,0,0]
	v_pk_fma_f32 v[0:1], v[0:1], v[144:145], v[140:141] op_sel_hi:[0,1,1] neg_lo:[1,0,0] neg_hi:[1,0,0]
	v_pk_fma_f32 v[0:1], v[130:131], v[136:137], v[0:1] op_sel_hi:[0,1,1]
	v_pk_fma_f32 v[130:131], v[130:131], v[132:133], v[142:143] op_sel_hi:[0,1,1]
	v_pk_fma_f32 v[132:133], v[92:93], v[130:131], v[138:139] op_sel_hi:[0,1,1] neg_lo:[0,0,1] neg_hi:[0,0,1]
	v_pk_fma_f32 v[138:139], v[90:91], v[140:141], v[152:153] op_sel_hi:[0,1,1] neg_lo:[0,0,1] neg_hi:[0,0,1]
	v_lshlrev_b64 v[140:141], 1, v[126:127]
	v_pk_fma_f32 v[130:131], v[92:93], v[0:1], v[134:135] op_sel_hi:[0,1,1] neg_lo:[0,0,1] neg_hi:[0,0,1]
	v_lshl_add_u64 v[236:237], s[30:31], 0, v[140:141]
	global_load_dwordx2 v[236:237], v[236:237], off offset:3072
	v_lshl_add_u64 v[238:239], s[28:29], 0, v[140:141]
	global_load_dwordx2 v[238:239], v[238:239], off offset:3072
	v_lshl_add_u64 v[134:135], s[30:31], 0, v[140:141]
	s_nop 0
	v_pk_mul_f32 v[154:155], v[148:149], v[150:151] op_sel_hi:[0,1]
	v_lshl_add_u32 v0, v128, 2, s17
	v_pk_fma_f32 v[136:137], v[90:91], v[2:3], v[154:155] op_sel_hi:[0,1,1] neg_lo:[0,0,1] neg_hi:[0,0,1]
	ds_read_b128 v[0:3], v0
	s_nop 0
	s_waitcnt vmcnt(1)
	v_lshlrev_b32_e32 v128, 16, v236
	v_and_b32_e32 v129, 0xffff0000, v236
	v_lshlrev_b32_e32 v126, 16, v237
	v_and_b32_e32 v127, 0xffff0000, v237
	s_waitcnt lgkmcnt(0)
	v_pk_fma_f32 v[128:129], v[0:1], v[136:137], v[128:129]
	v_lshl_add_u64 v[136:137], s[28:29], 0, v[140:141]
	v_pk_fma_f32 v[126:127], v[2:3], v[138:139], v[126:127]
	s_nop 0
	s_nop 0
	s_waitcnt vmcnt(0)
	v_lshlrev_b32_e32 v140, 16, v238
	v_and_b32_e32 v141, 0xffff0000, v238
	v_lshlrev_b32_e32 v138, 16, v239
	v_and_b32_e32 v139, 0xffff0000, v239
	v_pk_fma_f32 v[132:133], v[0:1], v[132:133], v[140:141]
	v_cvt_pk_bf16_f32 v0, v128, v129
	v_cvt_pk_bf16_f32 v1, v126, v127
	v_pk_fma_f32 v[130:131], v[2:3], v[130:131], v[138:139]
	v_cvt_pk_bf16_f32 v2, v132, v133
	s_nop 0
	v_cvt_pk_bf16_f32 v3, v130, v131
	global_store_dwordx2 v[134:135], v[0:1], off offset:3072
	global_store_dwordx2 v[136:137], v[2:3], off offset:3072
	v_mov_b32_e32 v0, v21
	ds_read_b32 v138, v53 offset:72
	v_lshlrev_b32_e32 v134, 2, v0
	v_add_u32_e32 v136, 0x700, v134
	v_ashrrev_i32_e32 v137, 31, v136
	v_lshlrev_b64 v[148:149], 1, v[136:137]
	v_lshl_add_u64 v[236:237], vcc, 0, v[148:149]
	global_load_dwordx2 v[236:237], v[236:237], off
	v_lshl_add_u64 v[238:239], s[42:43], 0, v[148:149]
	global_load_dwordx2 v[238:239], v[238:239], off
	v_lshl_add_u64 v[240:241], s[88:89], 0, v[148:149]
	global_load_dwordx2 v[240:241], v[240:241], off
	v_lshl_add_u64 v[242:243], s[36:37], 0, v[148:149]
	global_load_dwordx2 v[242:243], v[242:243], off
	v_lshl_add_u64 v[244:245], s[78:79], 0, v[148:149]
	global_load_dwordx2 v[244:245], v[244:245], off
	v_lshl_add_u64 v[246:247], s[76:77], 0, v[148:149]
	global_load_dwordx2 v[246:247], v[246:247], off
	s_nop 0
	s_nop 0
	v_lshl_add_u64 v[150:151], s[42:43], 0, v[148:149]
	s_nop 0
	s_nop 0
	s_nop 0
	v_ashrrev_i32_e32 v135, 31, v134
	s_nop 0
	s_waitcnt vmcnt(5)
	v_lshlrev_b32_e32 v140, 16, v236
	v_and_b32_e32 v141, 0xffff0000, v236
	v_lshlrev_b32_e32 v144, 16, v237
	v_and_b32_e32 v145, 0xffff0000, v237
	ds_read2_b64 v[0:3], v53 offset0:1 offset1:2
	s_nop 0
	s_waitcnt vmcnt(4)
	v_lshlrev_b32_e32 v150, 16, v238
	v_and_b32_e32 v151, 0xffff0000, v238
	v_lshlrev_b32_e32 v152, 16, v239
	v_and_b32_e32 v153, 0xffff0000, v239
	s_waitcnt lgkmcnt(0)
	v_pk_fma_f32 v[156:157], v[0:1], v[152:153], 0 op_sel_hi:[0,1,0]
	s_nop 0
	s_waitcnt vmcnt(3)
	v_lshlrev_b32_e32 v160, 16, v240
	v_and_b32_e32 v161, 0xffff0000, v240
	v_lshlrev_b32_e32 v158, 16, v241
	v_and_b32_e32 v159, 0xffff0000, v241
	v_pk_fma_f32 v[156:157], v[0:1], v[158:159], v[156:157] op_sel:[1,0,0]
	s_nop 0
	s_nop 0
	v_pk_fma_f32 v[154:155], v[0:1], v[150:151], 0 op_sel_hi:[0,1,0]
	v_pk_fma_f32 v[154:155], v[0:1], v[160:161], v[154:155] op_sel:[1,0,0]
	v_pk_mul_f32 v[142:143], v[138:139], v[144:145] op_sel_hi:[0,1]
	v_pk_mul_f32 v[146:147], v[138:139], v[140:141] op_sel_hi:[0,1]
	s_nop 0
	s_waitcnt vmcnt(2)
	v_lshlrev_b32_e32 v160, 16, v242
	v_and_b32_e32 v161, 0xffff0000, v242
	v_lshlrev_b32_e32 v158, 16, v243
	v_and_b32_e32 v159, 0xffff0000, v243
	v_pk_fma_f32 v[156:157], v[2:3], v[158:159], v[156:157] op_sel_hi:[0,1,1]
	s_nop 0
	s_nop 0
	v_pk_fma_f32 v[154:155], v[2:3], v[160:161], v[154:155] op_sel_hi:[0,1,1]
	v_mov_b32_e32 v2, v3
	s_nop 0
	s_waitcnt vmcnt(1)
	v_lshlrev_b32_e32 v160, 16, v244
	v_and_b32_e32 v161, 0xffff0000, v244
	v_lshlrev_b32_e32 v158, 16, v245
	v_and_b32_e32 v159, 0xffff0000, v245
	v_pk_fma_f32 v[158:159], v[2:3], v[158:159], v[156:157] op_sel_hi:[0,1,1]
	v_pk_fma_f32 v[2:3], v[2:3], v[160:161], v[154:155] op_sel_hi:[0,1,1]
	s_nop 0
	s_nop 0
	ds_read2_b64 v[154:157], v53 offset0:3 offset1:4
	s_nop 0
	s_waitcnt vmcnt(0)
	v_lshlrev_b32_e32 v162, 16, v246
	v_and_b32_e32 v163, 0xffff0000, v246
	v_lshlrev_b32_e32 v160, 16, v247
	v_and_b32_e32 v161, 0xffff0000, v247
	s_waitcnt lgkmcnt(0)
	v_pk_fma_f32 v[158:159], v[154:155], v[160:161], v[158:159] op_sel_hi:[0,1,1]
	v_lshl_add_u64 v[236:237], s[10:11], 0, v[148:149]
	global_load_dwordx2 v[236:237], v[236:237], off
	v_lshl_add_u64 v[238:239], s[8:9], 0, v[148:149]
	global_load_dwordx2 v[238:239], v[238:239], off
	v_lshl_add_u64 v[240:241], s[44:45], 0, v[148:149]
	global_load_dwordx2 v[240:241], v[240:241], off
	v_lshl_add_u64 v[242:243], s[86:87], 0, v[148:149]
	global_load_dwordx2 v[242:243], v[242:243], off
	v_lshl_add_u64 v[244:245], s[0:1], 0, v[148:149]
	global_load_dwordx2 v[244:245], v[244:245], off
	v_lshl_add_u64 v[246:247], s[2:3], 0, v[148:149]
	global_load_dwordx2 v[246:247], v[246:247], off
	s_nop 0
	s_nop 0
	v_pk_fma_f32 v[2:3], v[154:155], v[162:163], v[2:3] op_sel_hi:[0,1,1]
	s_nop 0
	s_waitcnt vmcnt(5)
	v_lshlrev_b32_e32 v162, 16, v236
	v_and_b32_e32 v163, 0xffff0000, v236
	v_lshlrev_b32_e32 v160, 16, v237
	v_and_b32_e32 v161, 0xffff0000, v237
	v_pk_fma_f32 v[158:159], v[154:155], v[160:161], v[158:159] op_sel:[1,0,0]
	v_pk_fma_f32 v[2:3], v[154:155], v[162:163], v[2:3] op_sel:[1,0,0]
	s_nop 0
	s_nop 0
	s_nop 0
	s_waitcnt vmcnt(4)
	v_lshlrev_b32_e32 v160, 16, v238
	v_and_b32_e32 v161, 0xffff0000, v238
	v_lshlrev_b32_e32 v154, 16, v239
	v_and_b32_e32 v155, 0xffff0000, v239
	v_pk_fma_f32 v[154:155], v[156:157], v[154:155], v[158:159] op_sel_hi:[0,1,1]
	s_nop 0
	s_nop 0
	v_pk_fma_f32 v[2:3], v[156:157], v[160:161], v[2:3] op_sel_hi:[0,1,1]
	v_mov_b32_e32 v156, v157
	s_nop 0
	s_waitcnt vmcnt(3)
	v_lshlrev_b32_e32 v160, 16, v240
	v_and_b32_e32 v161, 0xffff0000, v240
	v_pk_fma_f32 v[2:3], v[156:157], v[160:161], v[2:3] op_sel_hi:[0,1,1]
	s_nop 0
	s_nop 0
	v_lshlrev_b32_e32 v158, 16, v241
	v_and_b32_e32 v159, 0xffff0000, v241
	v_pk_fma_f32 v[158:159], v[156:157], v[158:159], v[154:155] op_sel_hi:[0,1,1]
	ds_read2_b64 v[154:157], v53 offset0:5 offset1:6
	s_nop 0
	s_waitcnt vmcnt(2)
	v_lshlrev_b32_e32 v162, 16, v242
	v_and_b32_e32 v163, 0xffff0000, v242
	v_lshlrev_b32_e32 v160, 16, v243
	v_and_b32_e32 v161, 0xffff0000, v243
	s_waitcnt lgkmcnt(0)
	v_pk_fma_f32 v[158:159], v[154:155], v[160:161], v[158:159] op_sel_hi:[0,1,1]
	s_nop 0
	s_nop 0
	v_pk_fma_f32 v[2:3], v[154:155], v[162:163], v[2:3] op_sel_hi:[0,1,1]
	s_nop 0
	s_waitcnt vmcnt(1)
	v_lshlrev_b32_e32 v162, 16, v244
	v_and_b32_e32 v163, 0xffff0000, v244
	v_lshlrev_b32_e32 v160, 16, v245
	v_and_b32_e32 v161, 0xffff0000, v245
	v_pk_fma_f32 v[158:159], v[154:155], v[160:161], v[158:159] op_sel:[1,0,0]
	v_pk_fma_f32 v[2:3], v[154:155], v[162:163], v[2:3] op_sel:[1,0,0]
	s_nop 0
	s_nop 0
	s_nop 0
	s_waitcnt vmcnt(0)
	v_lshlrev_b32_e32 v160, 16, v246
	v_and_b32_e32 v161, 0xffff0000, v246
	v_lshlrev_b32_e32 v154, 16, v247
	v_and_b32_e32 v155, 0xffff0000, v247
	v_pk_fma_f32 v[154:155], v[156:157], v[154:155], v[158:159] op_sel_hi:[0,1,1]
	v_lshl_add_u64 v[236:237], s[96:97], 0, v[148:149]
	global_load_dwordx2 v[236:237], v[236:237], off
	v_lshl_add_u64 v[238:239], s[52:53], 0, v[148:149]
	global_load_dwordx2 v[238:239], v[238:239], off
	v_lshl_add_u64 v[240:241], s[50:51], 0, v[148:149]
	global_load_dwordx2 v[240:241], v[240:241], off
	v_lshl_add_u64 v[242:243], s[48:49], 0, v[148:149]
	global_load_dwordx2 v[242:243], v[242:243], off
	v_lshl_add_u64 v[244:245], s[46:47], 0, v[148:149]
	global_load_dwordx2 v[244:245], v[244:245], off
	s_nop 0
	s_nop 0
	v_pk_fma_f32 v[2:3], v[156:157], v[160:161], v[2:3] op_sel_hi:[0,1,1]
	v_mov_b32_e32 v156, v157
	s_nop 0
	s_waitcnt vmcnt(4)
	v_lshlrev_b32_e32 v160, 16, v236
	v_and_b32_e32 v161, 0xffff0000, v236
	v_pk_fma_f32 v[2:3], v[156:157], v[160:161], v[2:3] op_sel_hi:[0,1,1]
	s_nop 0
	s_nop 0
	v_lshlrev_b32_e32 v158, 16, v237
	v_and_b32_e32 v159, 0xffff0000, v237
	v_pk_fma_f32 v[158:159], v[156:157], v[158:159], v[154:155] op_sel_hi:[0,1,1]
	ds_read2_b64 v[154:157], v53 offset0:7 offset1:8
	s_nop 0
	s_waitcnt vmcnt(3)
	v_lshlrev_b32_e32 v162, 16, v238
	v_and_b32_e32 v163, 0xffff0000, v238
	v_lshlrev_b32_e32 v160, 16, v239
	v_and_b32_e32 v161, 0xffff0000, v239
	s_waitcnt lgkmcnt(0)
	v_pk_fma_f32 v[158:159], v[154:155], v[160:161], v[158:159] op_sel_hi:[0,1,1]
	s_nop 0
	s_nop 0
	v_pk_fma_f32 v[2:3], v[154:155], v[162:163], v[2:3] op_sel_hi:[0,1,1]
	s_nop 0
	s_waitcnt vmcnt(2)
	v_lshlrev_b32_e32 v162, 16, v240
	v_and_b32_e32 v163, 0xffff0000, v240
	v_lshlrev_b32_e32 v160, 16, v241
	v_and_b32_e32 v161, 0xffff0000, v241
	v_pk_fma_f32 v[158:159], v[154:155], v[160:161], v[158:159] op_sel:[1,0,0]
	v_pk_fma_f32 v[2:3], v[154:155], v[162:163], v[2:3] op_sel:[1,0,0]
	s_nop 0
	s_nop 0
	s_nop 0
	s_nop 0
	s_nop 0
	s_waitcnt vmcnt(1)
	v_lshlrev_b32_e32 v160, 16, v242
	v_and_b32_e32 v161, 0xffff0000, v242
	v_lshlrev_b32_e32 v154, 16, v243
	v_and_b32_e32 v155, 0xffff0000, v243
	v_pk_fma_f32 v[2:3], v[156:157], v[160:161], v[2:3] op_sel_hi:[0,1,1]
	v_pk_fma_f32 v[154:155], v[156:157], v[154:155], v[158:159] op_sel_hi:[0,1,1]
	s_nop 0
	s_waitcnt vmcnt(0)
	v_lshlrev_b32_e32 v158, 16, v244
	v_and_b32_e32 v159, 0xffff0000, v244
	v_lshlrev_b32_e32 v148, 16, v245
	v_and_b32_e32 v149, 0xffff0000, v245
	v_mov_b32_e32 v156, v157
	v_pk_mul_f32 v[160:161], v[156:157], v[148:149] op_sel_hi:[0,1]
	v_pk_fma_f32 v[148:149], v[156:157], v[148:149], v[154:155] op_sel_hi:[0,1,1]
	v_pk_fma_f32 v[2:3], v[156:157], v[158:159], v[2:3] op_sel_hi:[0,1,1]
	v_pk_fma_f32 v[150:151], v[0:1], v[150:151], v[2:3] op_sel_hi:[0,1,1] neg_lo:[1,0,0] neg_hi:[1,0,0]
	v_pk_fma_f32 v[0:1], v[0:1], v[152:153], v[148:149] op_sel_hi:[0,1,1] neg_lo:[1,0,0] neg_hi:[1,0,0]
	v_pk_fma_f32 v[0:1], v[138:139], v[144:145], v[0:1] op_sel_hi:[0,1,1]
	v_pk_fma_f32 v[138:139], v[138:139], v[140:141], v[150:151] op_sel_hi:[0,1,1]
	v_pk_fma_f32 v[140:141], v[92:93], v[0:1], v[142:143] op_sel_hi:[0,1,1] neg_lo:[0,0,1] neg_hi:[0,0,1]
	v_lshl_add_u32 v0, v136, 2, s17
	v_lshlrev_b64 v[136:137], 1, v[134:135]
	v_lshl_add_u64 v[236:237], s[30:31], 0, v[136:137]
	global_load_dwordx2 v[236:237], v[236:237], off offset:3584
	v_lshl_add_u64 v[238:239], s[28:29], 0, v[136:137]
	global_load_dwordx2 v[238:239], v[238:239], off offset:3584
	v_lshl_add_u64 v[134:135], s[30:31], 0, v[136:137]
	s_nop 0
	v_pk_mul_f32 v[162:163], v[156:157], v[158:159] op_sel_hi:[0,1]
	v_pk_fma_f32 v[138:139], v[92:93], v[138:139], v[146:147] op_sel_hi:[0,1,1] neg_lo:[0,0,1] neg_hi:[0,0,1]
	v_pk_fma_f32 v[92:93], v[90:91], v[2:3], v[162:163] op_sel_hi:[0,1,1] neg_lo:[0,0,1] neg_hi:[0,0,1]
	ds_read_b128 v[0:3], v0
	v_pk_fma_f32 v[90:91], v[90:91], v[148:149], v[160:161] op_sel_hi:[0,1,1] neg_lo:[0,0,1] neg_hi:[0,0,1]
	s_nop 0
	s_waitcnt vmcnt(1)
	v_lshlrev_b32_e32 v144, 16, v236
	v_and_b32_e32 v145, 0xffff0000, v236
	v_lshlrev_b32_e32 v142, 16, v237
	v_and_b32_e32 v143, 0xffff0000, v237
	s_waitcnt lgkmcnt(0)
	v_pk_fma_f32 v[90:91], v[2:3], v[90:91], v[142:143]
	v_lshl_add_u64 v[142:143], s[28:29], 0, v[136:137]
	s_nop 0
	v_pk_fma_f32 v[92:93], v[0:1], v[92:93], v[144:145]
	s_nop 0
	s_waitcnt vmcnt(0)
	v_lshlrev_b32_e32 v144, 16, v238
	v_and_b32_e32 v145, 0xffff0000, v238
	v_lshlrev_b32_e32 v136, 16, v239
	v_and_b32_e32 v137, 0xffff0000, v239
	v_pk_fma_f32 v[138:139], v[0:1], v[138:139], v[144:145]
	v_cvt_pk_bf16_f32 v0, v92, v93
	v_cvt_pk_bf16_f32 v1, v90, v91
	v_pk_fma_f32 v[136:137], v[2:3], v[140:141], v[136:137]
	v_cvt_pk_bf16_f32 v2, v138, v139
	s_nop 0
	v_cvt_pk_bf16_f32 v3, v136, v137
	global_store_dwordx2 v[134:135], v[0:1], off offset:3584
	global_store_dwordx2 v[142:143], v[2:3], off offset:3584
	v_mul_f32_e32 v0, v81, v81
	v_mul_f32_e32 v1, v15, v15
	v_fmac_f32_e32 v0, v80, v80
	v_fmac_f32_e32 v1, v14, v14
	v_mov_b32_e32 v2, v13
	v_mov_b32_e32 v3, v85
	v_add_f32_e32 v53, v0, v1
	v_mov_b32_e32 v0, v12
	v_mov_b32_e32 v1, v84
	v_pk_mul_f32 v[2:3], v[2:3], v[2:3]
	v_mov_b32_e32 v134, v11
	v_mov_b32_e32 v135, v83
	v_pk_fma_f32 v[0:1], v[0:1], v[0:1], v[2:3]
	v_mov_b32_e32 v2, v10
	v_mov_b32_e32 v3, v82
	v_pk_mul_f32 v[134:135], v[134:135], v[134:135]
	v_mul_f32_e32 v59, v112, v112
	v_pk_fma_f32 v[2:3], v[2:3], v[2:3], v[134:135]
	v_pk_mul_f32 v[134:135], v[96:97], v[96:97]
	v_pk_add_f32 v[0:1], v[0:1], v[2:3]
	v_mul_f32_e32 v2, v89, v89
	v_mul_f32_e32 v3, v87, v87
	v_fmac_f32_e32 v2, v88, v88
	v_fmac_f32_e32 v3, v86, v86
	v_add_f32_e32 v2, v2, v3
	v_add_f32_e32 v53, v53, v2
	v_pk_mul_f32 v[2:3], v[94:95], v[94:95]
	v_mul_f32_e32 v61, v113, v113
	v_pk_mov_b32 v[140:141], v[134:135], v[2:3] op_sel:[1,0]
	v_mov_b32_e32 v135, v3
	v_pk_add_f32 v[2:3], v[140:141], v[134:135]
	v_pk_add_f32 v[0:1], v[0:1], v[0:1] op_sel:[0,1] op_sel_hi:[1,0]
	v_pk_add_f32 v[2:3], v[2:3], v[2:3] op_sel:[0,1] op_sel_hi:[1,0]
	v_mov_b32_e32 v1, v59
	v_mov_b32_e32 v3, v61
	v_pk_add_f32 v[0:1], v[0:1], v[2:3]
	v_mul_f32_e32 v2, v105, v105
	v_mul_f32_e32 v134, v103, v103
	v_mul_f32_e32 v63, v110, v110
	v_mul_f32_e32 v65, v111, v111
	v_pk_fma_f32 v[2:3], v[104:105], v[104:105], v[2:3] op_sel_hi:[1,1,0]
	v_pk_fma_f32 v[134:135], v[102:103], v[102:103], v[134:135] op_sel_hi:[1,1,0]
	v_mov_b32_e32 v3, v63
	v_mov_b32_e32 v135, v65
	v_pk_add_f32 v[2:3], v[2:3], v[134:135]
	v_pk_mul_f32 v[134:135], v[120:121], v[120:121]
	v_pk_add_f32 v[0:1], v[0:1], v[2:3]
	v_pk_mul_f32 v[2:3], v[118:119], v[118:119]
	v_mul_f32_e32 v59, v92, v92
	v_pk_mov_b32 v[140:141], v[134:135], v[2:3] op_sel:[1,0]
	v_mov_b32_e32 v135, v3
	v_pk_add_f32 v[2:3], v[140:141], v[134:135]
	v_mul_f32_e32 v61, v93, v93
	v_pk_add_f32 v[0:1], v[0:1], v[0:1] op_sel:[0,1] op_sel_hi:[1,0]
	v_pk_add_f32 v[2:3], v[2:3], v[2:3] op_sel:[0,1] op_sel_hi:[1,0]
	v_mov_b32_e32 v1, v59
	v_mov_b32_e32 v3, v61
	v_pk_add_f32 v[0:1], v[0:1], v[2:3]
	v_mul_f32_e32 v2, v129, v129
	v_mul_f32_e32 v134, v127, v127
	v_mul_f32_e32 v63, v90, v90
	v_mul_f32_e32 v65, v91, v91
	v_pk_fma_f32 v[2:3], v[128:129], v[128:129], v[2:3] op_sel_hi:[1,1,0]
	v_pk_fma_f32 v[134:135], v[126:127], v[126:127], v[134:135] op_sel_hi:[1,1,0]
	v_mov_b32_e32 v3, v63
	v_mov_b32_e32 v135, v65
	v_pk_add_f32 v[2:3], v[2:3], v[134:135]
	v_mul_f32_e32 v55, v101, v101
	v_pk_add_f32 v[0:1], v[0:1], v[2:3]
	v_mul_f32_e32 v57, v99, v99
	v_add_f32_e32 v0, v0, v1
	ds_bpermute_b32 v1, v31, v0
	v_fmac_f32_e32 v55, v100, v100
	v_fmac_f32_e32 v57, v98, v98
	v_add_f32_e32 v55, v55, v57
	v_add_f32_e32 v53, v53, v55
	s_waitcnt lgkmcnt(0)
	v_add_f32_e32 v0, v0, v1
	ds_bpermute_b32 v1, v33, v0
	v_mul_f32_e32 v55, v109, v109
	v_mul_f32_e32 v57, v107, v107
	v_fmac_f32_e32 v55, v108, v108
	v_fmac_f32_e32 v57, v106, v106
	s_waitcnt lgkmcnt(0)
	v_add_f32_e32 v0, v0, v1
	ds_bpermute_b32 v1, v35, v0
	v_add_f32_e32 v2, v55, v57
	v_add_f32_e32 v2, v53, v2
	v_mul_f32_e32 v3, v117, v117
	v_mul_f32_e32 v53, v115, v115
	s_waitcnt lgkmcnt(0)
	v_add_f32_e32 v0, v0, v1
	ds_bpermute_b32 v1, v41, v0
	v_fmac_f32_e32 v3, v116, v116
	v_fmac_f32_e32 v53, v114, v114
	v_add_f32_e32 v3, v3, v53
	v_add_f32_e32 v2, v2, v3
	s_waitcnt lgkmcnt(0)
	v_add_f32_e32 v0, v0, v1
	ds_bpermute_b32 v1, v37, v0
	v_mul_f32_e32 v3, v125, v125
	v_mul_f32_e32 v53, v123, v123
	v_fmac_f32_e32 v3, v124, v124
	v_fmac_f32_e32 v53, v122, v122
	s_waitcnt lgkmcnt(0)
	v_add_f32_e32 v0, v0, v1
	ds_bpermute_b32 v1, v39, v0
	v_add_f32_e32 v3, v3, v53
	v_add_f32_e32 v2, v2, v3
	v_mul_f32_e32 v3, v133, v133
	v_mul_f32_e32 v53, v131, v131
	s_waitcnt lgkmcnt(0)
	v_add_f32_e32 v0, v0, v1
	v_fmamk_f32 v0, v0, 0x3a000000, v189
	v_mul_f32_e32 v1, 0x4f800000, v0
	v_cmp_gt_f32_e32 vcc, s84, v0
	v_fmac_f32_e32 v3, v132, v132
	v_fmac_f32_e32 v53, v130, v130
	v_cndmask_b32_e32 v0, v0, v1, vcc
	v_add_f32_e32 v3, v3, v53
	v_sqrt_f32_e32 v1, v0
	v_add_f32_e32 v2, v2, v3
	v_mul_f32_e32 v3, v139, v139
	v_mul_f32_e32 v53, v137, v137
	v_fmac_f32_e32 v3, v138, v138
	v_fmac_f32_e32 v53, v136, v136
	v_add_f32_e32 v3, v3, v53
	v_add_f32_e32 v2, v2, v3
	v_add_u32_e32 v3, -1, v1
	v_fma_f32 v53, -v3, v1, v0
	v_cmp_ge_f32_e64 s[46:47], 0, v53
	v_add_u32_e32 v53, 1, v1
	s_mov_b32 s33, 0xff61b1e6
	v_cndmask_b32_e64 v3, v1, v3, s[46:47]
	v_fma_f32 v1, -v53, v1, v0
	v_cmp_lt_f32_e64 s[46:47], 0, v1
	s_nop 1
	v_cndmask_b32_e64 v1, v3, v53, s[46:47]
	v_mul_f32_e32 v3, 0x37800000, v1
	v_cndmask_b32_e32 v1, v1, v3, vcc
	ds_bpermute_b32 v3, v31, v2
	v_cmp_class_f32_e32 vcc, v0, v190
	v_cndmask_b32_e32 v53, v1, v0, vcc
	s_waitcnt lgkmcnt(0)
	v_add_f32_e32 v0, v2, v3
	ds_bpermute_b32 v1, v33, v0
	v_div_scale_f32 v57, s[0:1], v53, v53, 1.0
	v_rcp_f32_e32 v55, v57
	v_div_scale_f32 v61, vcc, 1.0, v53, 1.0
	s_waitcnt lgkmcnt(0)
	v_add_f32_e32 v0, v0, v1
	ds_bpermute_b32 v1, v35, v0
	v_fma_f32 v2, -v57, v55, 1.0
	v_fmac_f32_e32 v55, v2, v55
	v_mul_f32_e32 v59, v61, v55
	v_fma_f32 v65, -v57, v59, v61
	s_waitcnt lgkmcnt(0)
	v_add_f32_e32 v63, v0, v1
	ds_read_b128 v[0:3], v25
	ds_read_b128 v[142:145], v25 offset:1024
	ds_read_b128 v[146:149], v25 offset:2048
	ds_read_b128 v[150:153], v25 offset:3072
	ds_read_b128 v[154:157], v25 offset:4096
	ds_read_b128 v[158:161], v25 offset:5120
	ds_read_b128 v[162:165], v25 offset:6144
	ds_read_b128 v[174:177], v25 offset:7168
	ds_read_b128 v[178:181], v25 offset:8192
	ds_read_b128 v[182:185], v25 offset:9216
	ds_read_b128 v[198:201], v25 offset:10240
	ds_read_b128 v[202:205], v25 offset:11264
	ds_read_b128 v[206:209], v25 offset:12288
	ds_read_b128 v[210:213], v25 offset:13312
	ds_read_b128 v[214:217], v25 offset:14336
	ds_read_b128 v[224:227], v25 offset:15360
	s_waitcnt lgkmcnt(7)
	v_mov_b32_e32 v134, v178
	v_mov_b32_e32 v135, v1
	v_mov_b32_e32 v166, v180
	v_mov_b32_e32 v167, v3
	v_pk_mul_f32 v[140:141], v[12:13], v[134:135]
	v_mov_b32_e32 v1, v179
	v_pk_mul_f32 v[178:179], v[10:11], v[166:167]
	v_mov_b32_e32 v3, v181
	v_pk_fma_f32 v[140:141], v[12:13], v[0:1], v[140:141] op_sel:[0,0,1] op_sel_hi:[1,1,0]
	v_pk_fma_f32 v[178:179], v[10:11], v[2:3], v[178:179] op_sel:[0,0,1] op_sel_hi:[1,1,0]
	v_pk_mul_f32 v[134:135], v[80:81], v[134:135]
	v_pk_add_f32 v[140:141], v[140:141], v[178:179]
	s_waitcnt lgkmcnt(6)
	v_mov_b32_e32 v178, v182
	v_mov_b32_e32 v179, v143
	v_mov_b32_e32 v143, v183
	v_mov_b32_e32 v182, v184
	v_mov_b32_e32 v183, v145
	v_pk_mul_f32 v[180:181], v[84:85], v[178:179]
	v_pk_mul_f32 v[218:219], v[82:83], v[182:183]
	v_mov_b32_e32 v145, v185
	v_pk_fma_f32 v[180:181], v[84:85], v[142:143], v[180:181] op_sel:[0,0,1] op_sel_hi:[1,1,0]
	v_pk_fma_f32 v[184:185], v[82:83], v[144:145], v[218:219] op_sel:[0,0,1] op_sel_hi:[1,1,0]
	v_pk_add_f32 v[140:141], v[140:141], 0 op_sel_hi:[1,0]
	v_pk_add_f32 v[180:181], v[180:181], v[184:185]
	v_pk_fma_f32 v[0:1], v[80:81], v[0:1], v[134:135] op_sel:[0,0,1] op_sel_hi:[1,1,0]
	v_pk_add_f32 v[140:141], v[140:141], v[180:181]
	s_waitcnt lgkmcnt(5)
	v_mov_b32_e32 v180, v198
	v_mov_b32_e32 v181, v147
	v_mov_b32_e32 v147, v199
	v_mov_b32_e32 v198, v200
	v_mov_b32_e32 v199, v149
	v_pk_mul_f32 v[184:185], v[96:97], v[180:181]
	v_pk_mul_f32 v[218:219], v[94:95], v[198:199]
	v_mov_b32_e32 v149, v201
	v_pk_fma_f32 v[184:185], v[96:97], v[146:147], v[184:185] op_sel:[0,0,1] op_sel_hi:[1,1,0]
	v_pk_fma_f32 v[200:201], v[94:95], v[148:149], v[218:219] op_sel:[0,0,1] op_sel_hi:[1,1,0]
	v_pk_mul_f32 v[134:135], v[14:15], v[166:167]
	v_pk_add_f32 v[184:185], v[184:185], v[200:201]
	v_pk_fma_f32 v[2:3], v[14:15], v[2:3], v[134:135] op_sel:[0,0,1] op_sel_hi:[1,1,0]
	v_pk_add_f32 v[140:141], v[140:141], v[184:185]
	s_waitcnt lgkmcnt(4)
	v_mov_b32_e32 v184, v202
	v_mov_b32_e32 v185, v151
	v_mov_b32_e32 v151, v203
	v_mov_b32_e32 v202, v204
	v_mov_b32_e32 v203, v153
	v_pk_add_f32 v[0:1], v[0:1], v[2:3]
	v_pk_mul_f32 v[2:3], v[88:89], v[178:179]
	v_pk_mul_f32 v[134:135], v[86:87], v[182:183]
	v_pk_mul_f32 v[200:201], v[104:105], v[184:185]
	v_pk_mul_f32 v[218:219], v[102:103], v[202:203]
	v_mov_b32_e32 v153, v205
	v_pk_fma_f32 v[2:3], v[88:89], v[142:143], v[2:3] op_sel:[0,0,1] op_sel_hi:[1,1,0]
	v_pk_fma_f32 v[134:135], v[86:87], v[144:145], v[134:135] op_sel:[0,0,1] op_sel_hi:[1,1,0]
	v_pk_fma_f32 v[200:201], v[104:105], v[150:151], v[200:201] op_sel:[0,0,1] op_sel_hi:[1,1,0]
	v_pk_fma_f32 v[204:205], v[102:103], v[152:153], v[218:219] op_sel:[0,0,1] op_sel_hi:[1,1,0]
	v_pk_add_f32 v[0:1], v[0:1], 0 op_sel_hi:[1,0]
	v_pk_add_f32 v[2:3], v[2:3], v[134:135]
	v_pk_add_f32 v[200:201], v[200:201], v[204:205]
	v_pk_add_f32 v[0:1], v[0:1], v[2:3]
	v_pk_mul_f32 v[2:3], v[100:101], v[180:181]
	v_pk_mul_f32 v[134:135], v[98:99], v[198:199]
	v_pk_add_f32 v[140:141], v[140:141], v[200:201]
	s_waitcnt lgkmcnt(3)
	v_mov_b32_e32 v200, v206
	v_mov_b32_e32 v201, v155
	v_mov_b32_e32 v155, v207
	v_mov_b32_e32 v206, v208
	v_mov_b32_e32 v207, v157
	v_pk_fma_f32 v[2:3], v[100:101], v[146:147], v[2:3] op_sel:[0,0,1] op_sel_hi:[1,1,0]
	v_pk_fma_f32 v[134:135], v[98:99], v[148:149], v[134:135] op_sel:[0,0,1] op_sel_hi:[1,1,0]
	v_pk_mul_f32 v[204:205], v[112:113], v[200:201]
	v_pk_mul_f32 v[218:219], v[110:111], v[206:207]
	v_mov_b32_e32 v157, v209
	v_pk_add_f32 v[2:3], v[2:3], v[134:135]
	v_pk_fma_f32 v[204:205], v[112:113], v[154:155], v[204:205] op_sel:[0,0,1] op_sel_hi:[1,1,0]
	v_pk_fma_f32 v[208:209], v[110:111], v[156:157], v[218:219] op_sel:[0,0,1] op_sel_hi:[1,1,0]
	v_pk_add_f32 v[0:1], v[0:1], v[2:3]
	v_pk_mul_f32 v[2:3], v[108:109], v[184:185]
	v_pk_mul_f32 v[134:135], v[106:107], v[202:203]
	v_pk_add_f32 v[204:205], v[204:205], v[208:209]
	v_pk_fma_f32 v[2:3], v[108:109], v[150:151], v[2:3] op_sel:[0,0,1] op_sel_hi:[1,1,0]
	v_pk_fma_f32 v[134:135], v[106:107], v[152:153], v[134:135] op_sel:[0,0,1] op_sel_hi:[1,1,0]
	v_pk_add_f32 v[140:141], v[140:141], v[204:205]
	s_waitcnt lgkmcnt(2)
	v_mov_b32_e32 v204, v210
	v_mov_b32_e32 v205, v159
	v_mov_b32_e32 v159, v211
	v_mov_b32_e32 v210, v212
	v_mov_b32_e32 v211, v161
	v_pk_add_f32 v[2:3], v[2:3], v[134:135]
	v_pk_mul_f32 v[208:209], v[120:121], v[204:205]
	v_pk_mul_f32 v[218:219], v[118:119], v[210:211]
	v_mov_b32_e32 v161, v213
	v_pk_add_f32 v[0:1], v[0:1], v[2:3]
	v_pk_mul_f32 v[2:3], v[116:117], v[200:201]
	v_pk_mul_f32 v[134:135], v[114:115], v[206:207]
	v_pk_fma_f32 v[208:209], v[120:121], v[158:159], v[208:209] op_sel:[0,0,1] op_sel_hi:[1,1,0]
	v_pk_fma_f32 v[212:213], v[118:119], v[160:161], v[218:219] op_sel:[0,0,1] op_sel_hi:[1,1,0]
	v_pk_fma_f32 v[2:3], v[116:117], v[154:155], v[2:3] op_sel:[0,0,1] op_sel_hi:[1,1,0]
	v_pk_fma_f32 v[134:135], v[114:115], v[156:157], v[134:135] op_sel:[0,0,1] op_sel_hi:[1,1,0]
	v_pk_add_f32 v[208:209], v[208:209], v[212:213]
	v_pk_add_f32 v[2:3], v[2:3], v[134:135]
	v_pk_add_f32 v[140:141], v[140:141], v[208:209]
	s_waitcnt lgkmcnt(1)
	v_mov_b32_e32 v208, v214
	v_mov_b32_e32 v209, v163
	v_mov_b32_e32 v163, v215
	v_mov_b32_e32 v214, v216
	v_mov_b32_e32 v215, v165
	v_pk_add_f32 v[0:1], v[0:1], v[2:3]
	v_pk_mul_f32 v[2:3], v[124:125], v[204:205]
	v_pk_mul_f32 v[134:135], v[122:123], v[210:211]
	v_pk_mul_f32 v[212:213], v[128:129], v[208:209]
	v_pk_mul_f32 v[218:219], v[126:127], v[214:215]
	v_mov_b32_e32 v165, v217
	v_pk_fma_f32 v[2:3], v[124:125], v[158:159], v[2:3] op_sel:[0,0,1] op_sel_hi:[1,1,0]
	v_pk_fma_f32 v[134:135], v[122:123], v[160:161], v[134:135] op_sel:[0,0,1] op_sel_hi:[1,1,0]
	v_pk_fma_f32 v[212:213], v[128:129], v[162:163], v[212:213] op_sel:[0,0,1] op_sel_hi:[1,1,0]
	v_pk_fma_f32 v[216:217], v[126:127], v[164:165], v[218:219] op_sel:[0,0,1] op_sel_hi:[1,1,0]
	v_pk_add_f32 v[2:3], v[2:3], v[134:135]
	v_pk_add_f32 v[212:213], v[212:213], v[216:217]
	v_pk_add_f32 v[0:1], v[0:1], v[2:3]
	v_pk_mul_f32 v[2:3], v[132:133], v[208:209]
	v_pk_mul_f32 v[134:135], v[130:131], v[214:215]
	v_pk_add_f32 v[140:141], v[140:141], v[212:213]
	s_waitcnt lgkmcnt(0)
	v_mov_b32_e32 v212, v224
	v_mov_b32_e32 v213, v175
	v_mov_b32_e32 v218, v226
	v_mov_b32_e32 v219, v177
	v_pk_fma_f32 v[2:3], v[132:133], v[162:163], v[2:3] op_sel:[0,0,1] op_sel_hi:[1,1,0]
	v_pk_fma_f32 v[134:135], v[130:131], v[164:165], v[134:135] op_sel:[0,0,1] op_sel_hi:[1,1,0]
	v_pk_mul_f32 v[216:217], v[92:93], v[212:213]
	v_mov_b32_e32 v175, v225
	v_pk_mul_f32 v[224:225], v[90:91], v[218:219]
	v_mov_b32_e32 v177, v227
	v_pk_add_f32 v[2:3], v[2:3], v[134:135]
	v_pk_fma_f32 v[216:217], v[92:93], v[174:175], v[216:217] op_sel:[0,0,1] op_sel_hi:[1,1,0]
	v_pk_fma_f32 v[224:225], v[90:91], v[176:177], v[224:225] op_sel:[0,0,1] op_sel_hi:[1,1,0]
	v_pk_add_f32 v[0:1], v[0:1], v[2:3]
	v_pk_mul_f32 v[2:3], v[138:139], v[212:213]
	v_pk_mul_f32 v[134:135], v[136:137], v[218:219]
	v_pk_add_f32 v[216:217], v[216:217], v[224:225]
	v_pk_fma_f32 v[2:3], v[138:139], v[174:175], v[2:3] op_sel:[0,0,1] op_sel_hi:[1,1,0]
	v_pk_fma_f32 v[134:135], v[136:137], v[176:177], v[134:135] op_sel:[0,0,1] op_sel_hi:[1,1,0]
	v_pk_add_f32 v[140:141], v[140:141], v[216:217]
	v_pk_add_f32 v[2:3], v[2:3], v[134:135]
	ds_read_b128 v[144:147], v25 offset:16384
	ds_read_b128 v[148:151], v25 offset:17408
	ds_read_b128 v[152:155], v25 offset:18432
	ds_read_b128 v[156:159], v25 offset:19456
	ds_read_b128 v[160:163], v25 offset:20480
	ds_read_b128 v[164:167], v25 offset:21504
	ds_read_b128 v[174:177], v25 offset:22528
	ds_read_b128 v[178:181], v25 offset:23552
	ds_read_b128 v[182:185], v25 offset:24576
	ds_read_b128 v[198:201], v25 offset:25600
	ds_read_b128 v[202:205], v25 offset:26624
	ds_read_b128 v[206:209], v25 offset:27648
	ds_read_b128 v[210:213], v25 offset:28672
	ds_read_b128 v[214:217], v25 offset:29696
	ds_read_b128 v[224:227], v25 offset:30720
	ds_read_b128 v[228:231], v25 offset:31744
	v_pk_add_f32 v[0:1], v[0:1], v[2:3]
	s_waitcnt lgkmcnt(7)
	v_mov_b32_e32 v2, v182
	v_mov_b32_e32 v3, v145
	v_mov_b32_e32 v145, v183
	v_mov_b32_e32 v182, v184
	v_mov_b32_e32 v183, v147
	v_pk_mul_f32 v[134:135], v[12:13], v[2:3]
	v_pk_mul_f32 v[142:143], v[10:11], v[182:183]
	v_mov_b32_e32 v147, v185
	v_pk_fma_f32 v[134:135], v[12:13], v[144:145], v[134:135] op_sel:[0,0,1] op_sel_hi:[1,1,0]
	v_pk_fma_f32 v[142:143], v[10:11], v[146:147], v[142:143] op_sel:[0,0,1] op_sel_hi:[1,1,0]
	s_waitcnt lgkmcnt(6)
	v_mov_b32_e32 v184, v198
	v_mov_b32_e32 v185, v149
	v_mov_b32_e32 v149, v199
	v_mov_b32_e32 v198, v200
	v_mov_b32_e32 v199, v151
	v_pk_add_f32 v[134:135], v[134:135], v[142:143]
	v_pk_mul_f32 v[142:143], v[84:85], v[184:185]
	v_pk_mul_f32 v[218:219], v[82:83], v[198:199]
	v_mov_b32_e32 v151, v201
	v_pk_fma_f32 v[142:143], v[84:85], v[148:149], v[142:143] op_sel:[0,0,1] op_sel_hi:[1,1,0]
	v_pk_fma_f32 v[200:201], v[82:83], v[150:151], v[218:219] op_sel:[0,0,1] op_sel_hi:[1,1,0]
	v_pk_add_f32 v[134:135], v[134:135], 0 op_sel_hi:[1,0]
	v_pk_add_f32 v[142:143], v[142:143], v[200:201]
	s_waitcnt lgkmcnt(5)
	v_mov_b32_e32 v200, v202
	v_mov_b32_e32 v201, v153
	v_mov_b32_e32 v153, v203
	v_mov_b32_e32 v202, v204
	v_mov_b32_e32 v203, v155
	v_pk_add_f32 v[134:135], v[134:135], v[142:143]
	v_pk_mul_f32 v[142:143], v[96:97], v[200:201]
	v_pk_mul_f32 v[218:219], v[94:95], v[202:203]
	v_mov_b32_e32 v155, v205
	v_pk_fma_f32 v[142:143], v[96:97], v[152:153], v[142:143] op_sel:[0,0,1] op_sel_hi:[1,1,0]
	v_pk_fma_f32 v[204:205], v[94:95], v[154:155], v[218:219] op_sel:[0,0,1] op_sel_hi:[1,1,0]
	v_pk_mul_f32 v[2:3], v[80:81], v[2:3]
	v_pk_add_f32 v[142:143], v[142:143], v[204:205]
	s_waitcnt lgkmcnt(4)
	v_mov_b32_e32 v204, v206
	v_mov_b32_e32 v205, v157
	v_mov_b32_e32 v157, v207
	v_mov_b32_e32 v206, v208
	v_mov_b32_e32 v207, v159
	v_pk_add_f32 v[134:135], v[134:135], v[142:143]
	v_pk_mul_f32 v[142:143], v[104:105], v[204:205]
	v_pk_mul_f32 v[218:219], v[102:103], v[206:207]
	v_mov_b32_e32 v159, v209
	v_pk_fma_f32 v[142:143], v[104:105], v[156:157], v[142:143] op_sel:[0,0,1] op_sel_hi:[1,1,0]
	v_pk_fma_f32 v[208:209], v[102:103], v[158:159], v[218:219] op_sel:[0,0,1] op_sel_hi:[1,1,0]
	v_pk_fma_f32 v[2:3], v[80:81], v[144:145], v[2:3] op_sel:[0,0,1] op_sel_hi:[1,1,0]
	v_pk_add_f32 v[142:143], v[142:143], v[208:209]
	s_waitcnt lgkmcnt(3)
	v_mov_b32_e32 v208, v210
	v_mov_b32_e32 v209, v161
	v_mov_b32_e32 v161, v211
	v_mov_b32_e32 v210, v212
	v_mov_b32_e32 v211, v163
	v_pk_add_f32 v[134:135], v[134:135], v[142:143]
	v_pk_mul_f32 v[142:143], v[112:113], v[208:209]
	v_pk_mul_f32 v[218:219], v[110:111], v[210:211]
	v_mov_b32_e32 v163, v213
	v_pk_fma_f32 v[142:143], v[112:113], v[160:161], v[142:143] op_sel:[0,0,1] op_sel_hi:[1,1,0]
	v_pk_fma_f32 v[212:213], v[110:111], v[162:163], v[218:219] op_sel:[0,0,1] op_sel_hi:[1,1,0]
	v_pk_mul_f32 v[144:145], v[86:87], v[198:199]
	v_pk_add_f32 v[142:143], v[142:143], v[212:213]
	s_waitcnt lgkmcnt(2)
	v_mov_b32_e32 v212, v214
	v_mov_b32_e32 v213, v165
	v_mov_b32_e32 v165, v215
	v_mov_b32_e32 v214, v216
	v_mov_b32_e32 v215, v167
	v_pk_add_f32 v[134:135], v[134:135], v[142:143]
	v_pk_mul_f32 v[142:143], v[120:121], v[212:213]
	v_pk_mul_f32 v[218:219], v[118:119], v[214:215]
	v_mov_b32_e32 v167, v217
	v_pk_fma_f32 v[142:143], v[120:121], v[164:165], v[142:143] op_sel:[0,0,1] op_sel_hi:[1,1,0]
	v_pk_fma_f32 v[216:217], v[118:119], v[166:167], v[218:219] op_sel:[0,0,1] op_sel_hi:[1,1,0]
	s_waitcnt lgkmcnt(1)
	v_mov_b32_e32 v218, v226
	v_pk_add_f32 v[142:143], v[142:143], v[216:217]
	v_mov_b32_e32 v216, v224
	v_mov_b32_e32 v217, v175
	v_mov_b32_e32 v219, v177
	v_pk_add_f32 v[134:135], v[134:135], v[142:143]
	v_pk_mul_f32 v[142:143], v[128:129], v[216:217]
	v_mov_b32_e32 v175, v225
	v_pk_mul_f32 v[224:225], v[126:127], v[218:219]
	v_mov_b32_e32 v177, v227
	v_pk_fma_f32 v[142:143], v[128:129], v[174:175], v[142:143] op_sel:[0,0,1] op_sel_hi:[1,1,0]
	v_pk_fma_f32 v[224:225], v[126:127], v[176:177], v[224:225] op_sel:[0,0,1] op_sel_hi:[1,1,0]
	s_waitcnt lgkmcnt(0)
	v_mov_b32_e32 v226, v230
	v_pk_add_f32 v[142:143], v[142:143], v[224:225]
	v_mov_b32_e32 v224, v228
	v_mov_b32_e32 v225, v179
	v_mov_b32_e32 v227, v181
	v_pk_add_f32 v[134:135], v[134:135], v[142:143]
	v_pk_mul_f32 v[142:143], v[92:93], v[224:225]
	v_mov_b32_e32 v179, v229
	v_pk_mul_f32 v[228:229], v[90:91], v[226:227]
	v_mov_b32_e32 v181, v231
	v_pk_fma_f32 v[142:143], v[92:93], v[178:179], v[142:143] op_sel:[0,0,1] op_sel_hi:[1,1,0]
	v_pk_fma_f32 v[228:229], v[90:91], v[180:181], v[228:229] op_sel:[0,0,1] op_sel_hi:[1,1,0]
	v_pk_fma_f32 v[144:145], v[86:87], v[150:151], v[144:145] op_sel:[0,0,1] op_sel_hi:[1,1,0]
	v_pk_add_f32 v[142:143], v[142:143], v[228:229]
	ds_bpermute_b32 v67, v41, v63
	v_pk_add_f32 v[142:143], v[134:135], v[142:143]
	v_pk_mul_f32 v[134:135], v[14:15], v[182:183]
	v_fmac_f32_e32 v59, v65, v55
	v_pk_fma_f32 v[134:135], v[14:15], v[146:147], v[134:135] op_sel:[0,0,1] op_sel_hi:[1,1,0]
	v_pk_add_f32 v[2:3], v[2:3], v[134:135]
	v_pk_mul_f32 v[134:135], v[88:89], v[184:185]
	v_pk_add_f32 v[2:3], v[2:3], 0 op_sel_hi:[1,0]
	v_pk_fma_f32 v[134:135], v[88:89], v[148:149], v[134:135] op_sel:[0,0,1] op_sel_hi:[1,1,0]
	v_pk_add_f32 v[134:135], v[134:135], v[144:145]
	v_pk_mul_f32 v[144:145], v[98:99], v[202:203]
	v_pk_add_f32 v[2:3], v[2:3], v[134:135]
	v_pk_mul_f32 v[134:135], v[100:101], v[200:201]
	v_pk_fma_f32 v[144:145], v[98:99], v[154:155], v[144:145] op_sel:[0,0,1] op_sel_hi:[1,1,0]
	v_pk_fma_f32 v[134:135], v[100:101], v[152:153], v[134:135] op_sel:[0,0,1] op_sel_hi:[1,1,0]
	v_pk_add_f32 v[134:135], v[134:135], v[144:145]
	v_pk_mul_f32 v[144:145], v[106:107], v[206:207]
	v_pk_add_f32 v[2:3], v[2:3], v[134:135]
	v_pk_mul_f32 v[134:135], v[108:109], v[204:205]
	v_pk_fma_f32 v[144:145], v[106:107], v[158:159], v[144:145] op_sel:[0,0,1] op_sel_hi:[1,1,0]
	v_pk_fma_f32 v[134:135], v[108:109], v[156:157], v[134:135] op_sel:[0,0,1] op_sel_hi:[1,1,0]
	v_pk_add_f32 v[134:135], v[134:135], v[144:145]
	v_pk_mul_f32 v[144:145], v[114:115], v[210:211]
	v_pk_add_f32 v[2:3], v[2:3], v[134:135]
	v_pk_mul_f32 v[134:135], v[116:117], v[208:209]
	v_pk_fma_f32 v[144:145], v[114:115], v[162:163], v[144:145] op_sel:[0,0,1] op_sel_hi:[1,1,0]
	v_pk_fma_f32 v[134:135], v[116:117], v[160:161], v[134:135] op_sel:[0,0,1] op_sel_hi:[1,1,0]
	v_pk_add_f32 v[134:135], v[134:135], v[144:145]
	v_pk_mul_f32 v[144:145], v[122:123], v[214:215]
	v_pk_add_f32 v[2:3], v[2:3], v[134:135]
	v_pk_mul_f32 v[134:135], v[124:125], v[212:213]
	v_pk_fma_f32 v[144:145], v[122:123], v[166:167], v[144:145] op_sel:[0,0,1] op_sel_hi:[1,1,0]
	v_pk_fma_f32 v[134:135], v[124:125], v[164:165], v[134:135] op_sel:[0,0,1] op_sel_hi:[1,1,0]
	v_pk_add_f32 v[134:135], v[134:135], v[144:145]
	v_pk_mul_f32 v[144:145], v[130:131], v[218:219]
	v_pk_add_f32 v[2:3], v[2:3], v[134:135]
	v_pk_mul_f32 v[134:135], v[132:133], v[216:217]
	v_pk_fma_f32 v[144:145], v[130:131], v[176:177], v[144:145] op_sel:[0,0,1] op_sel_hi:[1,1,0]
	v_pk_fma_f32 v[134:135], v[132:133], v[174:175], v[134:135] op_sel:[0,0,1] op_sel_hi:[1,1,0]
	v_pk_add_f32 v[134:135], v[134:135], v[144:145]
	v_pk_mul_f32 v[144:145], v[136:137], v[226:227]
	v_pk_add_f32 v[2:3], v[2:3], v[134:135]
	v_pk_mul_f32 v[134:135], v[138:139], v[224:225]
	v_pk_fma_f32 v[144:145], v[136:137], v[180:181], v[144:145] op_sel:[0,0,1] op_sel_hi:[1,1,0]
	v_pk_fma_f32 v[134:135], v[138:139], v[178:179], v[134:135] op_sel:[0,0,1] op_sel_hi:[1,1,0]
	ds_read_b128 v[146:149], v25 offset:32768
	ds_read_b128 v[150:153], v25 offset:33792
	ds_read_b128 v[154:157], v25 offset:34816
	ds_read_b128 v[158:161], v25 offset:35840
	ds_read_b128 v[162:165], v25 offset:36864
	ds_read_b128 v[174:177], v25 offset:37888
	ds_read_b128 v[178:181], v25 offset:38912
	ds_read_b128 v[182:185], v25 offset:39936
	ds_read_b128 v[198:201], v25 offset:40960
	ds_read_b128 v[202:205], v25 offset:41984
	ds_read_b128 v[206:209], v25 offset:43008
	ds_read_b128 v[210:213], v25 offset:44032
	ds_read_b128 v[214:217], v25 offset:45056
	ds_read_b128 v[224:227], v25 offset:46080
	ds_read_b128 v[228:231], v25 offset:47104
	ds_read_b128 v[232:235], v25 offset:48128
	v_pk_add_f32 v[134:135], v[134:135], v[144:145]
	s_waitcnt lgkmcnt(7)
	v_mov_b32_e32 v166, v200
	v_pk_add_f32 v[2:3], v[2:3], v[134:135]
	v_mov_b32_e32 v134, v198
	v_mov_b32_e32 v135, v147
	v_mov_b32_e32 v167, v149
	v_pk_mul_f32 v[144:145], v[12:13], v[134:135]
	v_mov_b32_e32 v147, v199
	v_pk_mul_f32 v[198:199], v[10:11], v[166:167]
	v_mov_b32_e32 v149, v201
	v_pk_fma_f32 v[144:145], v[12:13], v[146:147], v[144:145] op_sel:[0,0,1] op_sel_hi:[1,1,0]
	v_pk_fma_f32 v[198:199], v[10:11], v[148:149], v[198:199] op_sel:[0,0,1] op_sel_hi:[1,1,0]
	v_pk_mul_f32 v[134:135], v[80:81], v[134:135]
	v_pk_add_f32 v[144:145], v[144:145], v[198:199]
	s_waitcnt lgkmcnt(6)
	v_mov_b32_e32 v198, v202
	v_mov_b32_e32 v199, v151
	v_mov_b32_e32 v151, v203
	v_mov_b32_e32 v202, v204
	v_mov_b32_e32 v203, v153
	v_pk_mul_f32 v[200:201], v[84:85], v[198:199]
	v_pk_mul_f32 v[218:219], v[82:83], v[202:203]
	v_mov_b32_e32 v153, v205
	v_pk_fma_f32 v[200:201], v[84:85], v[150:151], v[200:201] op_sel:[0,0,1] op_sel_hi:[1,1,0]
	v_pk_fma_f32 v[204:205], v[82:83], v[152:153], v[218:219] op_sel:[0,0,1] op_sel_hi:[1,1,0]
	v_pk_add_f32 v[144:145], v[144:145], 0 op_sel_hi:[1,0]
	v_pk_add_f32 v[200:201], v[200:201], v[204:205]
	v_pk_fma_f32 v[134:135], v[80:81], v[146:147], v[134:135] op_sel:[0,0,1] op_sel_hi:[1,1,0]
	v_pk_add_f32 v[144:145], v[144:145], v[200:201]
	s_waitcnt lgkmcnt(5)
	v_mov_b32_e32 v200, v206
	v_mov_b32_e32 v201, v155
	v_mov_b32_e32 v155, v207
	v_mov_b32_e32 v206, v208
	v_mov_b32_e32 v207, v157
	v_pk_mul_f32 v[204:205], v[96:97], v[200:201]
	v_pk_mul_f32 v[218:219], v[94:95], v[206:207]
	v_mov_b32_e32 v157, v209
	v_pk_mul_f32 v[146:147], v[14:15], v[166:167]
	v_pk_fma_f32 v[204:205], v[96:97], v[154:155], v[204:205] op_sel:[0,0,1] op_sel_hi:[1,1,0]
	v_pk_fma_f32 v[208:209], v[94:95], v[156:157], v[218:219] op_sel:[0,0,1] op_sel_hi:[1,1,0]
	v_pk_fma_f32 v[146:147], v[14:15], v[148:149], v[146:147] op_sel:[0,0,1] op_sel_hi:[1,1,0]
	v_pk_add_f32 v[204:205], v[204:205], v[208:209]
	v_pk_add_f32 v[134:135], v[134:135], v[146:147]
	v_pk_mul_f32 v[146:147], v[88:89], v[198:199]
	v_pk_mul_f32 v[148:149], v[86:87], v[202:203]
	v_pk_add_f32 v[144:145], v[144:145], v[204:205]
	s_waitcnt lgkmcnt(4)
	v_mov_b32_e32 v204, v210
	v_mov_b32_e32 v205, v159
	v_mov_b32_e32 v159, v211
	v_mov_b32_e32 v210, v212
	v_mov_b32_e32 v211, v161
	v_pk_fma_f32 v[146:147], v[88:89], v[150:151], v[146:147] op_sel:[0,0,1] op_sel_hi:[1,1,0]
	v_pk_fma_f32 v[148:149], v[86:87], v[152:153], v[148:149] op_sel:[0,0,1] op_sel_hi:[1,1,0]
	v_pk_mul_f32 v[208:209], v[104:105], v[204:205]
	v_pk_mul_f32 v[218:219], v[102:103], v[210:211]
	v_mov_b32_e32 v161, v213
	v_pk_add_f32 v[134:135], v[134:135], 0 op_sel_hi:[1,0]
	v_pk_add_f32 v[146:147], v[146:147], v[148:149]
	v_pk_fma_f32 v[208:209], v[104:105], v[158:159], v[208:209] op_sel:[0,0,1] op_sel_hi:[1,1,0]
	v_pk_fma_f32 v[212:213], v[102:103], v[160:161], v[218:219] op_sel:[0,0,1] op_sel_hi:[1,1,0]
	v_pk_add_f32 v[134:135], v[134:135], v[146:147]
	v_pk_mul_f32 v[146:147], v[100:101], v[200:201]
	v_pk_mul_f32 v[148:149], v[98:99], v[206:207]
	v_pk_add_f32 v[208:209], v[208:209], v[212:213]
	v_pk_fma_f32 v[146:147], v[100:101], v[154:155], v[146:147] op_sel:[0,0,1] op_sel_hi:[1,1,0]
	v_pk_fma_f32 v[148:149], v[98:99], v[156:157], v[148:149] op_sel:[0,0,1] op_sel_hi:[1,1,0]
	v_pk_add_f32 v[144:145], v[144:145], v[208:209]
	s_waitcnt lgkmcnt(3)
	v_mov_b32_e32 v208, v214
	v_mov_b32_e32 v209, v163
	v_mov_b32_e32 v163, v215
	v_mov_b32_e32 v214, v216
	v_mov_b32_e32 v215, v165
	v_pk_add_f32 v[146:147], v[146:147], v[148:149]
	v_pk_mul_f32 v[212:213], v[112:113], v[208:209]
	v_pk_mul_f32 v[218:219], v[110:111], v[214:215]
	v_mov_b32_e32 v165, v217
	v_pk_add_f32 v[134:135], v[134:135], v[146:147]
	v_pk_mul_f32 v[146:147], v[108:109], v[204:205]
	v_pk_mul_f32 v[148:149], v[106:107], v[210:211]
	v_pk_fma_f32 v[212:213], v[112:113], v[162:163], v[212:213] op_sel:[0,0,1] op_sel_hi:[1,1,0]
	v_pk_fma_f32 v[216:217], v[110:111], v[164:165], v[218:219] op_sel:[0,0,1] op_sel_hi:[1,1,0]
	v_pk_fma_f32 v[146:147], v[108:109], v[158:159], v[146:147] op_sel:[0,0,1] op_sel_hi:[1,1,0]
	v_pk_fma_f32 v[148:149], v[106:107], v[160:161], v[148:149] op_sel:[0,0,1] op_sel_hi:[1,1,0]
	v_pk_add_f32 v[212:213], v[212:213], v[216:217]
	v_pk_add_f32 v[146:147], v[146:147], v[148:149]
	v_pk_add_f32 v[144:145], v[144:145], v[212:213]
	s_waitcnt lgkmcnt(2)
	v_mov_b32_e32 v212, v224
	v_mov_b32_e32 v213, v175
	v_mov_b32_e32 v218, v226
	v_mov_b32_e32 v219, v177
	v_pk_add_f32 v[134:135], v[134:135], v[146:147]
	v_pk_mul_f32 v[146:147], v[116:117], v[208:209]
	v_pk_mul_f32 v[148:149], v[114:115], v[214:215]
	v_pk_mul_f32 v[216:217], v[120:121], v[212:213]
	v_mov_b32_e32 v175, v225
	v_pk_mul_f32 v[224:225], v[118:119], v[218:219]
	v_mov_b32_e32 v177, v227
	v_pk_fma_f32 v[146:147], v[116:117], v[162:163], v[146:147] op_sel:[0,0,1] op_sel_hi:[1,1,0]
	v_pk_fma_f32 v[148:149], v[114:115], v[164:165], v[148:149] op_sel:[0,0,1] op_sel_hi:[1,1,0]
	v_pk_fma_f32 v[216:217], v[120:121], v[174:175], v[216:217] op_sel:[0,0,1] op_sel_hi:[1,1,0]
	v_pk_fma_f32 v[224:225], v[118:119], v[176:177], v[224:225] op_sel:[0,0,1] op_sel_hi:[1,1,0]
	v_pk_add_f32 v[146:147], v[146:147], v[148:149]
	v_pk_add_f32 v[216:217], v[216:217], v[224:225]
	v_pk_add_f32 v[134:135], v[134:135], v[146:147]
	v_pk_mul_f32 v[146:147], v[124:125], v[212:213]
	v_pk_mul_f32 v[148:149], v[122:123], v[218:219]
	v_pk_add_f32 v[144:145], v[144:145], v[216:217]
	s_waitcnt lgkmcnt(1)
	v_mov_b32_e32 v216, v228
	v_mov_b32_e32 v217, v179
	v_mov_b32_e32 v226, v230
	v_mov_b32_e32 v227, v181
	v_pk_fma_f32 v[146:147], v[124:125], v[174:175], v[146:147] op_sel:[0,0,1] op_sel_hi:[1,1,0]
	v_pk_fma_f32 v[148:149], v[122:123], v[176:177], v[148:149] op_sel:[0,0,1] op_sel_hi:[1,1,0]
	v_pk_mul_f32 v[224:225], v[128:129], v[216:217]
	v_mov_b32_e32 v179, v229
	v_pk_mul_f32 v[228:229], v[126:127], v[226:227]
	v_mov_b32_e32 v181, v231
	v_pk_add_f32 v[146:147], v[146:147], v[148:149]
	v_pk_fma_f32 v[224:225], v[128:129], v[178:179], v[224:225] op_sel:[0,0,1] op_sel_hi:[1,1,0]
	v_pk_fma_f32 v[228:229], v[126:127], v[180:181], v[228:229] op_sel:[0,0,1] op_sel_hi:[1,1,0]
	v_pk_add_f32 v[134:135], v[134:135], v[146:147]
	v_pk_mul_f32 v[146:147], v[132:133], v[216:217]
	v_pk_mul_f32 v[148:149], v[130:131], v[226:227]
	v_pk_add_f32 v[224:225], v[224:225], v[228:229]
	v_pk_fma_f32 v[146:147], v[132:133], v[178:179], v[146:147] op_sel:[0,0,1] op_sel_hi:[1,1,0]
	v_pk_fma_f32 v[148:149], v[130:131], v[180:181], v[148:149] op_sel:[0,0,1] op_sel_hi:[1,1,0]
	v_pk_add_f32 v[144:145], v[144:145], v[224:225]
	s_waitcnt lgkmcnt(0)
	v_mov_b32_e32 v224, v232
	v_mov_b32_e32 v225, v183
	v_mov_b32_e32 v230, v234
	v_mov_b32_e32 v231, v185
	v_pk_add_f32 v[146:147], v[146:147], v[148:149]
	v_pk_mul_f32 v[228:229], v[92:93], v[224:225]
	v_mov_b32_e32 v183, v233
	v_pk_mul_f32 v[232:233], v[90:91], v[230:231]
	v_mov_b32_e32 v185, v235
	v_pk_add_f32 v[134:135], v[134:135], v[146:147]
	v_pk_mul_f32 v[146:147], v[138:139], v[224:225]
	v_pk_mul_f32 v[148:149], v[136:137], v[230:231]
	v_pk_fma_f32 v[228:229], v[92:93], v[182:183], v[228:229] op_sel:[0,0,1] op_sel_hi:[1,1,0]
	v_pk_fma_f32 v[232:233], v[90:91], v[184:185], v[232:233] op_sel:[0,0,1] op_sel_hi:[1,1,0]
	v_pk_fma_f32 v[146:147], v[138:139], v[182:183], v[146:147] op_sel:[0,0,1] op_sel_hi:[1,1,0]
	v_pk_fma_f32 v[148:149], v[136:137], v[184:185], v[148:149] op_sel:[0,0,1] op_sel_hi:[1,1,0]
	v_pk_add_f32 v[228:229], v[228:229], v[232:233]
	v_pk_add_f32 v[146:147], v[146:147], v[148:149]
	v_pk_add_f32 v[144:145], v[144:145], v[228:229]
	v_pk_add_f32 v[134:135], v[134:135], v[146:147]
	ds_read_b128 v[146:149], v25 offset:49152
	ds_read_b128 v[150:153], v25 offset:50176
	ds_read_b128 v[154:157], v25 offset:51200
	ds_read_b128 v[158:161], v25 offset:52224
	ds_read_b128 v[162:165], v25 offset:53248
	ds_read_b128 v[174:177], v25 offset:54272
	ds_read_b128 v[178:181], v25 offset:55296
	ds_read_b128 v[182:185], v25 offset:56320
	ds_read_b128 v[198:201], v25 offset:57344
	ds_read_b128 v[202:205], v25 offset:58368
	ds_read_b128 v[206:209], v25 offset:59392
	ds_read_b128 v[210:213], v25 offset:60416
	ds_read_b128 v[214:217], v25 offset:61440
	ds_read_b128 v[224:227], v25 offset:62464
	ds_read_b128 v[228:231], v25 offset:63488
	ds_read_b128 v[232:235], v25 offset:64512
	s_waitcnt lgkmcnt(7)
	v_mov_b32_e32 v166, v198
	v_mov_b32_e32 v167, v147
	v_pk_mul_f32 v[218:219], v[12:13], v[166:167]
	v_mov_b32_e32 v147, v199
	v_mov_b32_e32 v198, v200
	v_mov_b32_e32 v199, v149
	v_pk_fma_f32 v[12:13], v[12:13], v[146:147], v[218:219] op_sel:[0,0,1] op_sel_hi:[1,1,0]
	v_pk_mul_f32 v[218:219], v[10:11], v[198:199]
	v_mov_b32_e32 v149, v201
	v_pk_fma_f32 v[10:11], v[10:11], v[148:149], v[218:219] op_sel:[0,0,1] op_sel_hi:[1,1,0]
	s_waitcnt lgkmcnt(6)
	v_mov_b32_e32 v200, v202
	v_mov_b32_e32 v201, v151
	v_pk_add_f32 v[10:11], v[12:13], v[10:11]
	v_pk_mul_f32 v[12:13], v[84:85], v[200:201]
	v_mov_b32_e32 v151, v203
	v_pk_fma_f32 v[12:13], v[84:85], v[150:151], v[12:13] op_sel:[0,0,1] op_sel_hi:[1,1,0]
	v_mov_b32_e32 v84, v204
	v_mov_b32_e32 v85, v153
	v_pk_mul_f32 v[202:203], v[82:83], v[84:85]
	v_mov_b32_e32 v153, v205
	v_pk_fma_f32 v[82:83], v[82:83], v[152:153], v[202:203] op_sel:[0,0,1] op_sel_hi:[1,1,0]
	v_pk_add_f32 v[10:11], v[10:11], 0 op_sel_hi:[1,0]
	v_pk_add_f32 v[12:13], v[12:13], v[82:83]
	s_waitcnt lgkmcnt(5)
	v_mov_b32_e32 v82, v206
	v_mov_b32_e32 v83, v155
	v_pk_add_f32 v[10:11], v[10:11], v[12:13]
	v_pk_mul_f32 v[12:13], v[96:97], v[82:83]
	v_mov_b32_e32 v155, v207
	v_pk_fma_f32 v[12:13], v[96:97], v[154:155], v[12:13] op_sel:[0,0,1] op_sel_hi:[1,1,0]
	v_mov_b32_e32 v96, v208
	v_mov_b32_e32 v97, v157
	v_pk_mul_f32 v[202:203], v[94:95], v[96:97]
	v_mov_b32_e32 v157, v209
	v_pk_fma_f32 v[94:95], v[94:95], v[156:157], v[202:203] op_sel:[0,0,1] op_sel_hi:[1,1,0]
	v_pk_add_f32 v[12:13], v[12:13], v[94:95]
	s_waitcnt lgkmcnt(4)
	v_mov_b32_e32 v94, v210
	v_mov_b32_e32 v95, v159
	v_pk_add_f32 v[10:11], v[10:11], v[12:13]
	v_pk_mul_f32 v[12:13], v[104:105], v[94:95]
	v_mov_b32_e32 v159, v211
	v_pk_fma_f32 v[12:13], v[104:105], v[158:159], v[12:13] op_sel:[0,0,1] op_sel_hi:[1,1,0]
	v_mov_b32_e32 v104, v212
	v_mov_b32_e32 v105, v161
	v_pk_mul_f32 v[202:203], v[102:103], v[104:105]
	v_mov_b32_e32 v161, v213
	v_pk_fma_f32 v[102:103], v[102:103], v[160:161], v[202:203] op_sel:[0,0,1] op_sel_hi:[1,1,0]
	v_pk_add_f32 v[12:13], v[12:13], v[102:103]
	s_waitcnt lgkmcnt(3)
	v_mov_b32_e32 v102, v214
	v_mov_b32_e32 v103, v163
	v_pk_add_f32 v[10:11], v[10:11], v[12:13]
	v_pk_mul_f32 v[12:13], v[112:113], v[102:103]
	v_mov_b32_e32 v163, v215
	v_pk_fma_f32 v[12:13], v[112:113], v[162:163], v[12:13] op_sel:[0,0,1] op_sel_hi:[1,1,0]
	v_mov_b32_e32 v112, v216
	v_mov_b32_e32 v113, v165
	v_pk_mul_f32 v[202:203], v[110:111], v[112:113]
	v_mov_b32_e32 v165, v217
	v_pk_fma_f32 v[110:111], v[110:111], v[164:165], v[202:203] op_sel:[0,0,1] op_sel_hi:[1,1,0]
	v_pk_add_f32 v[12:13], v[12:13], v[110:111]
	s_waitcnt lgkmcnt(2)
	v_mov_b32_e32 v110, v224
	v_mov_b32_e32 v111, v175
	v_pk_add_f32 v[10:11], v[10:11], v[12:13]
	v_pk_mul_f32 v[12:13], v[120:121], v[110:111]
	v_mov_b32_e32 v175, v225
	v_pk_fma_f32 v[12:13], v[120:121], v[174:175], v[12:13] op_sel:[0,0,1] op_sel_hi:[1,1,0]
	v_mov_b32_e32 v120, v226
	v_mov_b32_e32 v121, v177
	v_pk_mul_f32 v[202:203], v[118:119], v[120:121]
	v_mov_b32_e32 v177, v227
	v_pk_fma_f32 v[118:119], v[118:119], v[176:177], v[202:203] op_sel:[0,0,1] op_sel_hi:[1,1,0]
	v_pk_add_f32 v[12:13], v[12:13], v[118:119]
	s_waitcnt lgkmcnt(1)
	v_mov_b32_e32 v118, v228
	v_mov_b32_e32 v119, v179
	v_pk_add_f32 v[10:11], v[10:11], v[12:13]
	v_pk_mul_f32 v[12:13], v[128:129], v[118:119]
	v_mov_b32_e32 v179, v229
	v_pk_fma_f32 v[12:13], v[128:129], v[178:179], v[12:13] op_sel:[0,0,1] op_sel_hi:[1,1,0]
	v_mov_b32_e32 v128, v230
	v_mov_b32_e32 v129, v181
	v_pk_mul_f32 v[202:203], v[126:127], v[128:129]
	v_mov_b32_e32 v181, v231
	v_pk_fma_f32 v[126:127], v[126:127], v[180:181], v[202:203] op_sel:[0,0,1] op_sel_hi:[1,1,0]
	v_pk_add_f32 v[12:13], v[12:13], v[126:127]
	s_waitcnt lgkmcnt(0)
	v_mov_b32_e32 v126, v232
	v_mov_b32_e32 v127, v183
	v_pk_add_f32 v[10:11], v[10:11], v[12:13]
	v_pk_mul_f32 v[12:13], v[92:93], v[126:127]
	v_mov_b32_e32 v183, v233
	v_pk_fma_f32 v[12:13], v[92:93], v[182:183], v[12:13] op_sel:[0,0,1] op_sel_hi:[1,1,0]
	v_mov_b32_e32 v92, v234
	v_mov_b32_e32 v93, v185
	v_pk_mul_f32 v[202:203], v[90:91], v[92:93]
	v_mov_b32_e32 v185, v235
	v_pk_fma_f32 v[90:91], v[90:91], v[184:185], v[202:203] op_sel:[0,0,1] op_sel_hi:[1,1,0]
	v_pk_add_f32 v[12:13], v[12:13], v[90:91]
	v_pk_add_f32 v[12:13], v[10:11], v[12:13]
	v_pk_mul_f32 v[10:11], v[80:81], v[166:167]
	v_pk_fma_f32 v[10:11], v[80:81], v[146:147], v[10:11] op_sel:[0,0,1] op_sel_hi:[1,1,0]
	v_pk_mul_f32 v[80:81], v[14:15], v[198:199]
	v_pk_fma_f32 v[14:15], v[14:15], v[148:149], v[80:81] op_sel:[0,0,1] op_sel_hi:[1,1,0]
	v_pk_mul_f32 v[80:81], v[86:87], v[84:85]
	v_pk_add_f32 v[10:11], v[10:11], v[14:15]
	v_pk_mul_f32 v[14:15], v[88:89], v[200:201]
	v_pk_fma_f32 v[80:81], v[86:87], v[152:153], v[80:81] op_sel:[0,0,1] op_sel_hi:[1,1,0]
	v_pk_fma_f32 v[14:15], v[88:89], v[150:151], v[14:15] op_sel:[0,0,1] op_sel_hi:[1,1,0]
	v_pk_add_f32 v[10:11], v[10:11], 0 op_sel_hi:[1,0]
	v_pk_add_f32 v[14:15], v[14:15], v[80:81]
	v_pk_mul_f32 v[80:81], v[98:99], v[96:97]
	v_pk_add_f32 v[10:11], v[10:11], v[14:15]
	v_pk_mul_f32 v[14:15], v[100:101], v[82:83]
	v_pk_fma_f32 v[80:81], v[98:99], v[156:157], v[80:81] op_sel:[0,0,1] op_sel_hi:[1,1,0]
	v_pk_fma_f32 v[14:15], v[100:101], v[154:155], v[14:15] op_sel:[0,0,1] op_sel_hi:[1,1,0]
	v_pk_add_f32 v[14:15], v[14:15], v[80:81]
	v_pk_mul_f32 v[80:81], v[106:107], v[104:105]
	v_pk_add_f32 v[10:11], v[10:11], v[14:15]
	v_pk_mul_f32 v[14:15], v[108:109], v[94:95]
	v_pk_fma_f32 v[80:81], v[106:107], v[160:161], v[80:81] op_sel:[0,0,1] op_sel_hi:[1,1,0]
	v_pk_fma_f32 v[14:15], v[108:109], v[158:159], v[14:15] op_sel:[0,0,1] op_sel_hi:[1,1,0]
	v_pk_add_f32 v[14:15], v[14:15], v[80:81]
	v_pk_mul_f32 v[80:81], v[114:115], v[112:113]
	v_pk_add_f32 v[10:11], v[10:11], v[14:15]
	v_pk_mul_f32 v[14:15], v[116:117], v[102:103]
	v_pk_fma_f32 v[80:81], v[114:115], v[164:165], v[80:81] op_sel:[0,0,1] op_sel_hi:[1,1,0]
	v_pk_fma_f32 v[14:15], v[116:117], v[162:163], v[14:15] op_sel:[0,0,1] op_sel_hi:[1,1,0]
	v_pk_add_f32 v[14:15], v[14:15], v[80:81]
	v_pk_mul_f32 v[80:81], v[122:123], v[120:121]
	v_pk_add_f32 v[10:11], v[10:11], v[14:15]
	v_pk_mul_f32 v[14:15], v[124:125], v[110:111]
	v_pk_fma_f32 v[80:81], v[122:123], v[176:177], v[80:81] op_sel:[0,0,1] op_sel_hi:[1,1,0]
	v_pk_fma_f32 v[14:15], v[124:125], v[174:175], v[14:15] op_sel:[0,0,1] op_sel_hi:[1,1,0]
	v_pk_add_f32 v[14:15], v[14:15], v[80:81]
	v_pk_mul_f32 v[80:81], v[130:131], v[128:129]
	v_pk_add_f32 v[10:11], v[10:11], v[14:15]
	v_pk_mul_f32 v[14:15], v[132:133], v[118:119]
	v_pk_fma_f32 v[80:81], v[130:131], v[180:181], v[80:81] op_sel:[0,0,1] op_sel_hi:[1,1,0]
	v_pk_fma_f32 v[14:15], v[132:133], v[178:179], v[14:15] op_sel:[0,0,1] op_sel_hi:[1,1,0]
	v_pk_add_f32 v[14:15], v[14:15], v[80:81]
	v_pk_mul_f32 v[80:81], v[136:137], v[92:93]
	v_pk_add_f32 v[10:11], v[10:11], v[14:15]
	v_pk_mul_f32 v[14:15], v[138:139], v[126:127]
	v_pk_fma_f32 v[80:81], v[136:137], v[184:185], v[80:81] op_sel:[0,0,1] op_sel_hi:[1,1,0]
	v_pk_fma_f32 v[14:15], v[138:139], v[182:183], v[14:15] op_sel:[0,0,1] op_sel_hi:[1,1,0]
	v_pk_add_f32 v[14:15], v[14:15], v[80:81]
	v_pk_add_f32 v[10:11], v[10:11], v[14:15]
	v_cmp_eq_u32_e64 s[46:47], 8, v20
	s_nop 1
	v_cndmask_b32_e64 v14, v140, v0, s[46:47]
	ds_bpermute_b32 v14, v39, v14
	v_cmp_eq_u32_e64 s[46:47], 8, v22
	s_nop 1
	v_cndmask_b32_e64 v15, v140, v0, s[46:47]
	s_waitcnt lgkmcnt(0)
	v_add_f32_e32 v69, v15, v14
	v_cmp_eq_u32_e64 s[46:47], 9, v24
	s_nop 1
	v_cndmask_b32_e64 v14, v141, v1, s[46:47]
	ds_bpermute_b32 v14, v39, v14
	v_cmp_eq_u32_e64 s[46:47], 9, v26
	s_nop 1
	v_cndmask_b32_e64 v15, v141, v1, s[46:47]
	s_waitcnt lgkmcnt(0)
	v_add_f32_e32 v71, v15, v14
	v_cmp_eq_u32_e64 s[46:47], 10, v28
	s_nop 1
	v_cndmask_b32_e64 v14, v142, v2, s[46:47]
	ds_bpermute_b32 v14, v39, v14
	v_cmp_eq_u32_e64 s[46:47], 10, v30
	s_nop 1
	v_cndmask_b32_e64 v15, v142, v2, s[46:47]
	s_waitcnt lgkmcnt(0)
	v_add_f32_e32 v73, v15, v14
	v_cmp_eq_u32_e64 s[46:47], 11, v32
	s_nop 1
	v_cndmask_b32_e64 v14, v143, v3, s[46:47]
	ds_bpermute_b32 v14, v39, v14
	v_cmp_eq_u32_e64 s[46:47], 11, v34
	s_nop 1
	v_cndmask_b32_e64 v15, v143, v3, s[46:47]
	s_waitcnt lgkmcnt(0)
	v_add_f32_e32 v75, v15, v14
	v_cmp_eq_u32_e64 s[46:47], 12, v36
	s_nop 1
	v_cndmask_b32_e64 v14, v144, v134, s[46:47]
	ds_bpermute_b32 v14, v39, v14
	v_cmp_eq_u32_e64 s[46:47], 12, v38
	s_nop 1
	v_cndmask_b32_e64 v15, v144, v134, s[46:47]
	s_waitcnt lgkmcnt(0)
	v_add_f32_e32 v14, v15, v14
	v_cmp_eq_u32_e64 s[46:47], 13, v40
	s_nop 1
	v_cndmask_b32_e64 v15, v145, v135, s[46:47]
	ds_bpermute_b32 v15, v39, v15
	v_cmp_eq_u32_e64 s[46:47], 13, v42
	s_nop 1
	v_cndmask_b32_e64 v80, v145, v135, s[46:47]
	s_waitcnt lgkmcnt(0)
	v_add_f32_e32 v15, v80, v15
	v_cmp_eq_u32_e64 s[46:47], 14, v44
	s_nop 1
	v_cndmask_b32_e64 v80, v12, v10, s[46:47]
	ds_bpermute_b32 v80, v39, v80
	v_cmp_eq_u32_e64 s[46:47], 14, v46
	s_nop 1
	v_cndmask_b32_e64 v12, v12, v10, s[46:47]
	s_waitcnt lgkmcnt(0)
	v_add_f32_e32 v12, v12, v80
	v_cmp_eq_u32_e64 s[46:47], 15, v48
	s_nop 1
	v_cndmask_b32_e64 v80, v13, v11, s[46:47]
	ds_bpermute_b32 v80, v39, v80
	v_cmp_eq_u32_e64 s[46:47], 15, v50
	s_nop 1
	v_cndmask_b32_e64 v13, v13, v11, s[46:47]
	s_waitcnt lgkmcnt(0)
	v_add_f32_e32 v13, v13, v80
	v_cmp_eq_u32_e64 s[46:47], 4, v52
	s_nop 1
	v_cndmask_b32_e64 v80, v69, v14, s[46:47]
	ds_bpermute_b32 v80, v37, v80
	v_cmp_eq_u32_e64 s[46:47], 4, v54
	s_nop 1
	v_cndmask_b32_e64 v69, v69, v14, s[46:47]
	s_waitcnt lgkmcnt(0)
	v_add_f32_e32 v69, v69, v80
	v_cmp_eq_u32_e64 s[46:47], 5, v56
	s_nop 1
	v_cndmask_b32_e64 v80, v71, v15, s[46:47]
	ds_bpermute_b32 v80, v37, v80
	v_cmp_eq_u32_e64 s[46:47], 5, v58
	s_nop 1
	v_cndmask_b32_e64 v71, v71, v15, s[46:47]
	s_waitcnt lgkmcnt(0)
	v_add_f32_e32 v71, v71, v80
	v_cmp_eq_u32_e64 s[46:47], 6, v60
	s_nop 1
	v_cndmask_b32_e64 v80, v73, v12, s[46:47]
	ds_bpermute_b32 v80, v37, v80
	v_cmp_eq_u32_e64 s[46:47], 6, v62
	s_nop 1
	v_cndmask_b32_e64 v73, v73, v12, s[46:47]
	s_waitcnt lgkmcnt(0)
	v_add_f32_e32 v73, v73, v80
	v_cmp_eq_u32_e64 s[46:47], 7, v64
	s_nop 1
	v_cndmask_b32_e64 v80, v75, v13, s[46:47]
	ds_bpermute_b32 v80, v37, v80
	v_cmp_eq_u32_e64 s[46:47], 7, v66
	s_nop 1
	v_cndmask_b32_e64 v75, v75, v13, s[46:47]
	s_waitcnt lgkmcnt(0)
	v_add_f32_e32 v75, v75, v80
	v_cmp_eq_u32_e64 s[46:47], 2, v68
	s_nop 1
	v_cndmask_b32_e64 v80, v69, v73, s[46:47]
	ds_bpermute_b32 v80, v41, v80
	v_cmp_eq_u32_e64 s[46:47], 2, v70
	s_nop 1
	v_cndmask_b32_e64 v69, v69, v73, s[46:47]
	s_waitcnt lgkmcnt(0)
	v_add_f32_e32 v69, v69, v80
	v_cmp_eq_u32_e64 s[46:47], 3, v72
	s_nop 1
	v_cndmask_b32_e64 v80, v71, v75, s[46:47]
	ds_bpermute_b32 v41, v41, v80
	v_cmp_eq_u32_e64 s[46:47], 3, v74
	s_nop 1
	v_cndmask_b32_e64 v71, v71, v75, s[46:47]
	s_waitcnt lgkmcnt(0)
	v_add_f32_e32 v41, v71, v41
	v_cmp_ne_u64_e64 s[46:47], 0, v[76:77]
	s_nop 1
	v_cndmask_b32_e64 v71, v69, v41, s[46:47]
	v_cmp_ne_u64_e64 s[46:47], 0, v[78:79]
	s_nop 1
	v_cndmask_b32_e64 v41, v69, v41, s[46:47]
	v_mov_b32_e32 v14, v41
	v_mov_b32_e32 v12, v14
	v_mov_b32_e32 v0, v12
	v_fma_f32 v2, -v57, v59, v61
	v_add_f32_e32 v3, v63, v67
	ds_bpermute_b32 v0, v35, v0
	v_mov_b32_e32 v1, v71
	ds_bpermute_b32 v10, v37, v3
	s_waitcnt lgkmcnt(1)
	v_add_f32_e32 v0, v1, v0
	ds_bpermute_b32 v1, v33, v0
	s_waitcnt lgkmcnt(0)
	v_add_f32_e32 v1, v0, v1
	ds_bpermute_b32 v11, v31, v1
	v_div_fmas_f32 v0, v2, v55, v59
	v_div_fixup_f32 v12, v0, v53, 1.0
	v_add_f32_e32 v0, v3, v10
	ds_bpermute_b32 v2, v39, v0
	s_waitcnt lgkmcnt(1)
	v_add_f32_e32 v3, v1, v11
	s_nop 0
	v_readlane_b32 s1, v3, 0
	v_readlane_b32 s0, v3, 4
	v_readlane_b32 s8, v3, 32
	v_readlane_b32 s9, v3, 36
	v_pk_mul_f32 v[14:15], v[12:13], s[0:1] op_sel_hi:[0,1]
	v_readlane_b32 s0, v3, 8
	v_cmp_gt_f32_e32 vcc, v14, v15
	v_readlane_b32 s10, v3, 40
	v_mul_f32_e32 v11, s0, v12
	v_readlane_b32 s0, v3, 12
	v_readlane_b32 s11, v3, 44
	v_readlane_b32 s12, v3, 48
	v_mul_f32_e32 v13, s0, v12
	v_readlane_b32 s0, v3, 16
	v_readlane_b32 s13, v3, 52
	v_readlane_b32 s14, v3, 56
	v_mul_f32_e32 v31, s0, v12
	v_readlane_b32 s0, v3, 20
	v_readlane_b32 s15, v3, 60
	v_cndmask_b32_e64 v10, 0, 1, vcc
	v_mul_f32_e32 v33, s0, v12
	v_readlane_b32 s0, v3, 24
	v_cmp_lt_f32_e64 s[52:53], s33, v15
	s_nop 0
	v_mul_f32_e32 v35, s0, v12
	v_readlane_b32 s0, v3, 28
	v_cndmask_b32_e32 v3, v15, v14, vcc
	v_cmp_gt_f32_e32 vcc, v11, v3
	v_mul_f32_e32 v1, s0, v12
	s_nop 0
	v_cndmask_b32_e32 v3, v3, v11, vcc
	v_cndmask_b32_e64 v10, v10, 2, vcc
	v_cmp_gt_f32_e32 vcc, v13, v3
	s_nop 1
	v_cndmask_b32_e32 v3, v3, v13, vcc
	v_cndmask_b32_e64 v10, v10, 3, vcc
	v_cmp_gt_f32_e32 vcc, v31, v3
	s_nop 1
	v_cndmask_b32_e32 v3, v3, v31, vcc
	v_cndmask_b32_e64 v10, v10, 4, vcc
	v_cmp_gt_f32_e32 vcc, v33, v3
	s_nop 1
	v_cndmask_b32_e32 v3, v3, v33, vcc
	v_cndmask_b32_e64 v10, v10, 5, vcc
	v_cmp_ngt_f32_e32 vcc, v35, v3
	s_nop 1
	v_cndmask_b32_e32 v3, v35, v3, vcc
	v_cndmask_b32_e32 v10, 6, v10, vcc
	v_cmp_gt_f32_e64 s[48:49], v1, v3
	s_or_b64 s[0:1], vcc, s[48:49]
	v_cmp_ngt_f32_e64 s[46:47], v1, v3
	v_cndmask_b32_e64 v10, v10, 7, s[48:49]
	v_cmp_ne_u32_e64 s[50:51], 0, v10
	s_and_b64 s[50:51], s[50:51], s[52:53]
	s_nop 0
	v_cndmask_b32_e64 v15, v196, v15, s[50:51]
	v_cmp_ne_u32_e64 s[50:51], 1, v10
	v_cmp_gt_f32_e64 s[52:53], v14, v15
	s_and_b64 s[50:51], s[50:51], s[52:53]
	v_cndmask_b32_e64 v14, v15, v14, s[50:51]
	v_cndmask_b32_e64 v15, 0, 1, s[50:51]
	v_cmp_ne_u32_e64 s[50:51], 2, v10
	v_cmp_gt_f32_e64 s[52:53], v11, v14
	s_and_b64 s[50:51], s[50:51], s[52:53]
	v_cndmask_b32_e64 v11, v14, v11, s[50:51]
	v_cndmask_b32_e64 v14, v15, 2, s[50:51]
	v_cmp_ne_u32_e64 s[50:51], 3, v10
	v_cmp_gt_f32_e64 s[52:53], v13, v11
	s_and_b64 s[50:51], s[50:51], s[52:53]
	v_cndmask_b32_e64 v11, v11, v13, s[50:51]
	v_cndmask_b32_e64 v13, v14, 3, s[50:51]
	v_cmp_ne_u32_e64 s[50:51], 4, v10
	v_cmp_gt_f32_e64 s[52:53], v31, v11
	s_and_b64 s[50:51], s[50:51], s[52:53]
	v_cndmask_b32_e64 v11, v11, v31, s[50:51]
	v_cndmask_b32_e64 v13, v13, 4, s[50:51]
	v_cmp_ne_u32_e64 s[50:51], 5, v10
	v_cmp_gt_f32_e64 s[52:53], v33, v11
	s_and_b64 s[50:51], s[50:51], s[52:53]
	v_cndmask_b32_e64 v11, v11, v33, s[50:51]
	v_cmp_gt_f32_e32 vcc, v35, v11
	v_cndmask_b32_e64 v13, v13, 5, s[50:51]
	s_and_b64 vcc, s[0:1], vcc
	v_cndmask_b32_e32 v35, v11, v35, vcc
	v_cndmask_b32_e64 v13, v13, 6, vcc
	s_and_saveexec_b64 s[0:1], s[46:47]
	s_cbranch_execz .LBB0_1352
	v_cmp_gt_f32_e32 vcc, v1, v35
	s_and_saveexec_b64 s[2:3], vcc
	v_mov_b32_e32 v13, 7
	v_mov_b32_e32 v35, v1
	s_or_b64 exec, exec, s[2:3]
	v_mov_b32_e32 v1, v3
